# loop-edge rotation: K-loop counter/exit test/next-tile address SALU moved in front of the loop-back barrier at five GEMM sites
# baseline (speedup 1.0000x reference)
.LBB0_809:
	s_andn2_b64 vcc, exec, s[52:53]
	s_waitcnt vmcnt(0)
	s_cbranch_vccnz .LBB0_812
	s_add_u32 s26, s26, 0x80
	s_addc_u32 s27, s27, 0
	s_add_u32 s19, s30, 0x100
	s_addc_u32 s20, s31, 0
	s_mov_b32 s21, 0
	s_add_i32 s22, s21, 2
	s_add_u32 s23, s26, 0x80
	s_addc_u32 s28, s27, 0
	s_add_i32 s34, 0, 0x10000
	s_cmp_eq_u32 s81, s21
	s_cselect_b32 s31, s3, s28
	s_cselect_b32 s30, s2, s23
	v_add_u32_e32 v2, s34, v231
	s_cselect_b32 s29, s61, s20
	s_cselect_b32 s28, s60, s19
	s_add_i32 s21, 0, 0x14000
	ds_read_b128 v[100:103], v2
	ds_read_b128 v[104:107], v2 offset:1024
	ds_read_b128 v[108:111], v2 offset:2048
	ds_read_b128 v[112:115], v2 offset:3072
	v_add_u32_e32 v2, s21, v231
	ds_read_b128 v[132:135], v2
	ds_read_b128 v[136:139], v2 offset:1024
	ds_read_b128 v[140:143], v2 offset:2048
	ds_read_b128 v[144:147], v2 offset:3072
	v_lshl_add_u64 v[208:209], s[26:27], 0, v[204:205]
	s_add_i32 m0, s72, 0xc000
	ds_read_b128 v[164:167], v240
	ds_read_b128 v[168:171], v240 offset:1024
	ds_read_b128 v[172:175], v240 offset:2048
	ds_read_b128 v[176:179], v240 offset:3072
	ds_read_b128 v[180:183], v240 offset:4096
	ds_read_b128 v[184:187], v240 offset:5120
	ds_read_b128 v[188:191], v240 offset:6144
	ds_read_b128 v[192:195], v240 offset:7168
	global_load_lds_dwordx4 v[208:209], off
	v_lshl_add_u64 v[208:209], s[26:27], 0, v[206:207]
	s_add_i32 m0, s72, 0xe000
	s_nop 0
	global_load_lds_dwordx4 v[208:209], off
	s_waitcnt vmcnt(8)
	s_waitcnt lgkmcnt(0)
	s_barrier
	s_setprio 1
	s_waitcnt lgkmcnt(0)
	v_mfma_f32_16x16x32_bf16 v[160:163], v[100:103], v[164:167], 0
	v_mfma_f32_16x16x32_bf16 v[156:159], v[108:111], v[164:167], 0
	v_mfma_f32_16x16x32_bf16 v[128:131], v[100:103], v[172:175], 0
	v_mfma_f32_16x16x32_bf16 v[124:127], v[108:111], v[172:175], 0
	v_mfma_f32_16x16x32_bf16 v[96:99], v[100:103], v[180:183], 0
	v_mfma_f32_16x16x32_bf16 v[92:95], v[108:111], v[180:183], 0
	v_mfma_f32_16x16x32_bf16 v[80:83], v[100:103], v[188:191], 0
	v_mfma_f32_16x16x32_bf16 v[76:79], v[108:111], v[188:191], 0
	v_mfma_f32_16x16x32_bf16 v[160:163], v[104:107], v[168:171], v[160:163]
	v_mfma_f32_16x16x32_bf16 v[156:159], v[112:115], v[168:171], v[156:159]
	v_mfma_f32_16x16x32_bf16 v[128:131], v[104:107], v[176:179], v[128:131]
	v_mfma_f32_16x16x32_bf16 v[124:127], v[112:115], v[176:179], v[124:127]
	v_mfma_f32_16x16x32_bf16 v[96:99], v[104:107], v[184:187], v[96:99]
	v_mfma_f32_16x16x32_bf16 v[92:95], v[112:115], v[184:187], v[92:95]
	v_mfma_f32_16x16x32_bf16 v[80:83], v[104:107], v[192:195], v[80:83]
	v_mfma_f32_16x16x32_bf16 v[76:79], v[112:115], v[192:195], v[76:79]
	s_setprio 0
	s_setprio 1
	v_mfma_f32_16x16x32_bf16 v[152:155], v[132:135], v[164:167], 0
	v_mfma_f32_16x16x32_bf16 v[148:151], v[140:143], v[164:167], 0
	v_mfma_f32_16x16x32_bf16 v[120:123], v[132:135], v[172:175], 0
	v_mfma_f32_16x16x32_bf16 v[116:119], v[140:143], v[172:175], 0
	v_mfma_f32_16x16x32_bf16 v[88:91], v[132:135], v[180:183], 0
	v_mfma_f32_16x16x32_bf16 v[84:87], v[140:143], v[180:183], 0
	v_mfma_f32_16x16x32_bf16 v[72:75], v[132:135], v[188:191], 0
	v_mfma_f32_16x16x32_bf16 v[68:71], v[140:143], v[188:191], 0
	v_mfma_f32_16x16x32_bf16 v[152:155], v[136:139], v[168:171], v[152:155]
	v_mfma_f32_16x16x32_bf16 v[148:151], v[144:147], v[168:171], v[148:151]
	v_mfma_f32_16x16x32_bf16 v[120:123], v[136:139], v[176:179], v[120:123]
	v_mfma_f32_16x16x32_bf16 v[116:119], v[144:147], v[176:179], v[116:119]
	v_mfma_f32_16x16x32_bf16 v[88:91], v[136:139], v[184:187], v[88:91]
	v_mfma_f32_16x16x32_bf16 v[84:87], v[144:147], v[184:187], v[84:87]
	v_mfma_f32_16x16x32_bf16 v[72:75], v[136:139], v[192:195], v[72:75]
	v_mfma_f32_16x16x32_bf16 v[68:71], v[144:147], v[192:195], v[68:71]
	s_setprio 0
	s_barrier
	s_add_i32 s23, s34, s69
	v_lshl_add_u64 v[208:209], s[28:29], 0, v[200:201]
	s_mov_b32 m0, s23
	ds_read_b128 v[164:167], v240 offset:16384
	ds_read_b128 v[168:171], v240 offset:17408
	ds_read_b128 v[172:175], v240 offset:18432
	ds_read_b128 v[176:179], v240 offset:19456
	ds_read_b128 v[180:183], v240 offset:20480
	ds_read_b128 v[184:187], v240 offset:21504
	ds_read_b128 v[188:191], v240 offset:22528
	ds_read_b128 v[192:195], v240 offset:23552
	global_load_lds_dwordx4 v[208:209], off
	s_add_i32 m0, s23, 0x2000
	v_lshl_add_u64 v[210:211], s[28:29], 0, v[196:197]
	s_add_u32 s28, s28, s6
	s_addc_u32 s29, s29, s7
	s_add_i32 s21, s21, s69
	global_load_lds_dwordx4 v[210:211], off
	v_lshl_add_u64 v[218:219], s[28:29], 0, v[200:201]
	s_mov_b32 m0, s21
	v_lshl_add_u64 v[220:221], s[28:29], 0, v[196:197]
	global_load_lds_dwordx4 v[218:219], off
	s_add_i32 m0, s21, 0x2000
	v_lshl_add_u64 v[222:223], s[30:31], 0, v[202:203]
	global_load_lds_dwordx4 v[220:221], off
	s_mov_b32 m0, s72
	v_lshl_add_u64 v[224:225], s[30:31], 0, v[198:199]
	global_load_lds_dwordx4 v[222:223], off
	s_mov_b32 m0, s73
	s_nop 0
	global_load_lds_dwordx4 v[224:225], off
	s_waitcnt vmcnt(8)
	s_waitcnt lgkmcnt(0)
	s_barrier
	s_setprio 1
	s_waitcnt lgkmcnt(0)
	v_mfma_f32_16x16x32_bf16 v[64:67], v[100:103], v[164:167], 0
	v_mfma_f32_16x16x32_bf16 v[60:63], v[108:111], v[164:167], 0
	v_mfma_f32_16x16x32_bf16 v[48:51], v[100:103], v[172:175], 0
	v_mfma_f32_16x16x32_bf16 v[44:47], v[108:111], v[172:175], 0
	v_mfma_f32_16x16x32_bf16 v[32:35], v[100:103], v[180:183], 0
	v_mfma_f32_16x16x32_bf16 v[28:31], v[108:111], v[180:183], 0
	v_mfma_f32_16x16x32_bf16 v[16:19], v[100:103], v[188:191], 0
	v_mfma_f32_16x16x32_bf16 v[12:15], v[108:111], v[188:191], 0
	v_mfma_f32_16x16x32_bf16 v[64:67], v[104:107], v[168:171], v[64:67]
	v_mfma_f32_16x16x32_bf16 v[60:63], v[112:115], v[168:171], v[60:63]
	v_mfma_f32_16x16x32_bf16 v[48:51], v[104:107], v[176:179], v[48:51]
	v_mfma_f32_16x16x32_bf16 v[44:47], v[112:115], v[176:179], v[44:47]
	v_mfma_f32_16x16x32_bf16 v[32:35], v[104:107], v[184:187], v[32:35]
	v_mfma_f32_16x16x32_bf16 v[28:31], v[112:115], v[184:187], v[28:31]
	v_mfma_f32_16x16x32_bf16 v[16:19], v[104:107], v[192:195], v[16:19]
	v_mfma_f32_16x16x32_bf16 v[12:15], v[112:115], v[192:195], v[12:15]
	s_setprio 0
	s_setprio 1
	v_mfma_f32_16x16x32_bf16 v[56:59], v[132:135], v[164:167], 0
	v_mfma_f32_16x16x32_bf16 v[52:55], v[140:143], v[164:167], 0
	v_mfma_f32_16x16x32_bf16 v[40:43], v[132:135], v[172:175], 0
	v_mfma_f32_16x16x32_bf16 v[36:39], v[140:143], v[172:175], 0
	v_mfma_f32_16x16x32_bf16 v[24:27], v[132:135], v[180:183], 0
	v_mfma_f32_16x16x32_bf16 v[20:23], v[140:143], v[180:183], 0
	v_mfma_f32_16x16x32_bf16 v[8:11], v[132:135], v[188:191], 0
	v_mfma_f32_16x16x32_bf16 v[4:7], v[140:143], v[188:191], 0
	v_mfma_f32_16x16x32_bf16 v[56:59], v[136:139], v[168:171], v[56:59]
	v_mfma_f32_16x16x32_bf16 v[52:55], v[144:147], v[168:171], v[52:55]
	v_mfma_f32_16x16x32_bf16 v[40:43], v[136:139], v[176:179], v[40:43]
	v_mfma_f32_16x16x32_bf16 v[36:39], v[144:147], v[176:179], v[36:39]
	v_mfma_f32_16x16x32_bf16 v[24:27], v[136:139], v[184:187], v[24:27]
	v_mfma_f32_16x16x32_bf16 v[20:23], v[144:147], v[184:187], v[20:23]
	v_mfma_f32_16x16x32_bf16 v[8:11], v[136:139], v[192:195], v[8:11]
	v_mfma_f32_16x16x32_bf16 v[4:7], v[144:147], v[192:195], v[4:7]
	s_setprio 0
	s_barrier
	s_add_i32 s21, 0, 0x18000
	v_add_u32_e32 v2, s21, v231
	s_add_i32 s23, 0, 0x1c000
	ds_read_b128 v[100:103], v2
	ds_read_b128 v[104:107], v2 offset:1024
	ds_read_b128 v[108:111], v2 offset:2048
	ds_read_b128 v[112:115], v2 offset:3072
	v_add_u32_e32 v2, s23, v231
	ds_read_b128 v[132:135], v2
	ds_read_b128 v[136:139], v2 offset:1024
	ds_read_b128 v[140:143], v2 offset:2048
	ds_read_b128 v[144:147], v2 offset:3072
	s_add_u32 s28, s30, s6
	s_addc_u32 s29, s31, s7
	s_mov_b32 m0, s74
	v_lshl_add_u64 v[226:227], s[28:29], 0, v[202:203]
	ds_read_b128 v[164:167], v240 offset:32768
	ds_read_b128 v[168:171], v240 offset:33792
	ds_read_b128 v[172:175], v240 offset:34816
	ds_read_b128 v[176:179], v240 offset:35840
	ds_read_b128 v[180:183], v240 offset:36864
	ds_read_b128 v[184:187], v240 offset:37888
	ds_read_b128 v[188:191], v240 offset:38912
	ds_read_b128 v[192:195], v240 offset:39936
	global_load_lds_dwordx4 v[226:227], off
	v_lshl_add_u64 v[226:227], s[28:29], 0, v[198:199]
	s_mov_b32 m0, s75
	s_nop 0
	global_load_lds_dwordx4 v[226:227], off
	s_waitcnt vmcnt(8)
	s_waitcnt lgkmcnt(0)
	s_barrier
	s_setprio 1
	s_waitcnt lgkmcnt(0)
	v_mfma_f32_16x16x32_bf16 v[160:163], v[100:103], v[164:167], v[160:163]
	v_mfma_f32_16x16x32_bf16 v[156:159], v[108:111], v[164:167], v[156:159]
	v_mfma_f32_16x16x32_bf16 v[128:131], v[100:103], v[172:175], v[128:131]
	v_mfma_f32_16x16x32_bf16 v[124:127], v[108:111], v[172:175], v[124:127]
	v_mfma_f32_16x16x32_bf16 v[96:99], v[100:103], v[180:183], v[96:99]
	v_mfma_f32_16x16x32_bf16 v[92:95], v[108:111], v[180:183], v[92:95]
	v_mfma_f32_16x16x32_bf16 v[80:83], v[100:103], v[188:191], v[80:83]
	v_mfma_f32_16x16x32_bf16 v[76:79], v[108:111], v[188:191], v[76:79]
	v_mfma_f32_16x16x32_bf16 v[160:163], v[104:107], v[168:171], v[160:163]
	v_mfma_f32_16x16x32_bf16 v[156:159], v[112:115], v[168:171], v[156:159]
	v_mfma_f32_16x16x32_bf16 v[128:131], v[104:107], v[176:179], v[128:131]
	v_mfma_f32_16x16x32_bf16 v[124:127], v[112:115], v[176:179], v[124:127]
	v_mfma_f32_16x16x32_bf16 v[96:99], v[104:107], v[184:187], v[96:99]
	v_mfma_f32_16x16x32_bf16 v[92:95], v[112:115], v[184:187], v[92:95]
	v_mfma_f32_16x16x32_bf16 v[80:83], v[104:107], v[192:195], v[80:83]
	v_mfma_f32_16x16x32_bf16 v[76:79], v[112:115], v[192:195], v[76:79]
	s_setprio 0
	s_setprio 1
	v_mfma_f32_16x16x32_bf16 v[152:155], v[132:135], v[164:167], v[152:155]
	v_mfma_f32_16x16x32_bf16 v[148:151], v[140:143], v[164:167], v[148:151]
	v_mfma_f32_16x16x32_bf16 v[120:123], v[132:135], v[172:175], v[120:123]
	v_mfma_f32_16x16x32_bf16 v[116:119], v[140:143], v[172:175], v[116:119]
	v_mfma_f32_16x16x32_bf16 v[88:91], v[132:135], v[180:183], v[88:91]
	v_mfma_f32_16x16x32_bf16 v[84:87], v[140:143], v[180:183], v[84:87]
	v_mfma_f32_16x16x32_bf16 v[72:75], v[132:135], v[188:191], v[72:75]
	v_mfma_f32_16x16x32_bf16 v[68:71], v[140:143], v[188:191], v[68:71]
	v_mfma_f32_16x16x32_bf16 v[152:155], v[136:139], v[168:171], v[152:155]
	v_mfma_f32_16x16x32_bf16 v[148:151], v[144:147], v[168:171], v[148:151]
	v_mfma_f32_16x16x32_bf16 v[120:123], v[136:139], v[176:179], v[120:123]
	v_mfma_f32_16x16x32_bf16 v[116:119], v[144:147], v[176:179], v[116:119]
	v_mfma_f32_16x16x32_bf16 v[88:91], v[136:139], v[184:187], v[88:91]
	v_mfma_f32_16x16x32_bf16 v[84:87], v[144:147], v[184:187], v[84:87]
	v_mfma_f32_16x16x32_bf16 v[72:75], v[136:139], v[192:195], v[72:75]
	v_mfma_f32_16x16x32_bf16 v[68:71], v[144:147], v[192:195], v[68:71]
	s_setprio 0
	s_barrier
	s_add_i32 s21, s21, s69
	v_lshl_add_u64 v[208:209], v[208:209], 0, s[24:25]
	s_mov_b32 m0, s21
	ds_read_b128 v[164:167], v240 offset:49152
	ds_read_b128 v[168:171], v240 offset:50176
	ds_read_b128 v[172:175], v240 offset:51200
	ds_read_b128 v[176:179], v240 offset:52224
	ds_read_b128 v[180:183], v240 offset:53248
	ds_read_b128 v[184:187], v240 offset:54272
	ds_read_b128 v[188:191], v240 offset:55296
	ds_read_b128 v[192:195], v240 offset:56320
	global_load_lds_dwordx4 v[208:209], off
	v_lshl_add_u64 v[208:209], v[210:211], 0, s[24:25]
	s_add_i32 m0, s21, 0x2000
	s_add_i32 s21, s23, s69
	global_load_lds_dwordx4 v[208:209], off
	v_lshl_add_u64 v[208:209], v[218:219], 0, s[24:25]
	s_mov_b32 m0, s21
	s_nop 0
	global_load_lds_dwordx4 v[208:209], off
	v_lshl_add_u64 v[208:209], v[220:221], 0, s[24:25]
	s_add_i32 m0, s21, 0x2000
	s_nop 0
	global_load_lds_dwordx4 v[208:209], off
	v_lshl_add_u64 v[208:209], v[222:223], 0, s[24:25]
	s_mov_b32 m0, s79
	s_nop 0
	global_load_lds_dwordx4 v[208:209], off
	v_lshl_add_u64 v[208:209], v[224:225], 0, s[24:25]
	s_mov_b32 m0, s80
	s_nop 0
	global_load_lds_dwordx4 v[208:209], off
	s_waitcnt vmcnt(8)
	s_waitcnt lgkmcnt(0)
	s_barrier
	s_setprio 1
	s_waitcnt lgkmcnt(0)
	v_mfma_f32_16x16x32_bf16 v[64:67], v[100:103], v[164:167], v[64:67]
	v_mfma_f32_16x16x32_bf16 v[60:63], v[108:111], v[164:167], v[60:63]
	v_mfma_f32_16x16x32_bf16 v[48:51], v[100:103], v[172:175], v[48:51]
	v_mfma_f32_16x16x32_bf16 v[44:47], v[108:111], v[172:175], v[44:47]
	v_mfma_f32_16x16x32_bf16 v[32:35], v[100:103], v[180:183], v[32:35]
	v_mfma_f32_16x16x32_bf16 v[28:31], v[108:111], v[180:183], v[28:31]
	v_mfma_f32_16x16x32_bf16 v[16:19], v[100:103], v[188:191], v[16:19]
	v_mfma_f32_16x16x32_bf16 v[12:15], v[108:111], v[188:191], v[12:15]
	v_mfma_f32_16x16x32_bf16 v[64:67], v[104:107], v[168:171], v[64:67]
	v_mfma_f32_16x16x32_bf16 v[60:63], v[112:115], v[168:171], v[60:63]
	v_mfma_f32_16x16x32_bf16 v[48:51], v[104:107], v[176:179], v[48:51]
	v_mfma_f32_16x16x32_bf16 v[44:47], v[112:115], v[176:179], v[44:47]
	v_mfma_f32_16x16x32_bf16 v[32:35], v[104:107], v[184:187], v[32:35]
	v_mfma_f32_16x16x32_bf16 v[28:31], v[112:115], v[184:187], v[28:31]
	v_mfma_f32_16x16x32_bf16 v[16:19], v[104:107], v[192:195], v[16:19]
	v_mfma_f32_16x16x32_bf16 v[12:15], v[112:115], v[192:195], v[12:15]
	s_setprio 0
	s_setprio 1
	v_mfma_f32_16x16x32_bf16 v[56:59], v[132:135], v[164:167], v[56:59]
	v_mfma_f32_16x16x32_bf16 v[52:55], v[140:143], v[164:167], v[52:55]
	v_mfma_f32_16x16x32_bf16 v[40:43], v[132:135], v[172:175], v[40:43]
	v_mfma_f32_16x16x32_bf16 v[36:39], v[140:143], v[172:175], v[36:39]
	v_mfma_f32_16x16x32_bf16 v[24:27], v[132:135], v[180:183], v[24:27]
	v_mfma_f32_16x16x32_bf16 v[20:23], v[140:143], v[180:183], v[20:23]
	v_mfma_f32_16x16x32_bf16 v[8:11], v[132:135], v[188:191], v[8:11]
	v_mfma_f32_16x16x32_bf16 v[4:7], v[140:143], v[188:191], v[4:7]
	v_mfma_f32_16x16x32_bf16 v[56:59], v[136:139], v[168:171], v[56:59]
	v_mfma_f32_16x16x32_bf16 v[52:55], v[144:147], v[168:171], v[52:55]
	v_mfma_f32_16x16x32_bf16 v[40:43], v[136:139], v[176:179], v[40:43]
	v_mfma_f32_16x16x32_bf16 v[36:39], v[144:147], v[176:179], v[36:39]
	v_mfma_f32_16x16x32_bf16 v[24:27], v[136:139], v[184:187], v[24:27]
	v_mfma_f32_16x16x32_bf16 v[20:23], v[144:147], v[184:187], v[20:23]
	v_mfma_f32_16x16x32_bf16 v[8:11], v[136:139], v[192:195], v[8:11]
	v_mfma_f32_16x16x32_bf16 v[4:7], v[144:147], v[192:195], v[4:7]
	s_setprio 0
	s_add_u32 s26, s26, 0x100
	s_addc_u32 s27, s27, 0
	s_add_u32 s19, s19, 0x100
	s_addc_u32 s20, s20, 0
	s_cmp_ge_i32 s22, s78
	s_mov_b32 s21, s22
	s_cbranch_scc1 .Lmy_rot0
	s_add_i32 s22, s21, 2
	s_add_u32 s23, s26, 0x80
	s_addc_u32 s28, s27, 0
	s_add_i32 s34, 0, 0x10000
	s_cmp_eq_u32 s81, s21
	s_cselect_b32 s31, s3, s28
	s_cselect_b32 s30, s2, s23
	s_cselect_b32 s29, s61, s20
	s_cselect_b32 s28, s60, s19
	s_add_i32 s21, 0, 0x14000
.LBB0_811:
	s_barrier
	v_add_u32_e32 v2, s34, v231
	ds_read_b128 v[100:103], v2
	ds_read_b128 v[104:107], v2 offset:1024
	ds_read_b128 v[108:111], v2 offset:2048
	ds_read_b128 v[112:115], v2 offset:3072
	v_add_u32_e32 v2, s21, v231
	ds_read_b128 v[132:135], v2
	ds_read_b128 v[136:139], v2 offset:1024
	ds_read_b128 v[140:143], v2 offset:2048
	ds_read_b128 v[144:147], v2 offset:3072
	v_lshl_add_u64 v[208:209], s[26:27], 0, v[204:205]
	s_add_i32 m0, s72, 0xc000
	ds_read_b128 v[164:167], v240
	ds_read_b128 v[168:171], v240 offset:1024
	ds_read_b128 v[172:175], v240 offset:2048
	ds_read_b128 v[176:179], v240 offset:3072
	ds_read_b128 v[180:183], v240 offset:4096
	ds_read_b128 v[184:187], v240 offset:5120
	ds_read_b128 v[188:191], v240 offset:6144
	ds_read_b128 v[192:195], v240 offset:7168
	global_load_lds_dwordx4 v[208:209], off
	v_lshl_add_u64 v[208:209], s[26:27], 0, v[206:207]
	s_add_i32 m0, s72, 0xe000
	s_nop 0
	global_load_lds_dwordx4 v[208:209], off
	s_waitcnt vmcnt(8)
	s_waitcnt lgkmcnt(0)
	s_barrier
	s_setprio 1
	s_waitcnt lgkmcnt(0)
	v_mfma_f32_16x16x32_bf16 v[160:163], v[100:103], v[164:167], v[160:163]
	v_mfma_f32_16x16x32_bf16 v[156:159], v[108:111], v[164:167], v[156:159]
	v_mfma_f32_16x16x32_bf16 v[128:131], v[100:103], v[172:175], v[128:131]
	v_mfma_f32_16x16x32_bf16 v[124:127], v[108:111], v[172:175], v[124:127]
	v_mfma_f32_16x16x32_bf16 v[96:99], v[100:103], v[180:183], v[96:99]
	v_mfma_f32_16x16x32_bf16 v[92:95], v[108:111], v[180:183], v[92:95]
	v_mfma_f32_16x16x32_bf16 v[80:83], v[100:103], v[188:191], v[80:83]
	v_mfma_f32_16x16x32_bf16 v[76:79], v[108:111], v[188:191], v[76:79]
	v_mfma_f32_16x16x32_bf16 v[160:163], v[104:107], v[168:171], v[160:163]
	v_mfma_f32_16x16x32_bf16 v[156:159], v[112:115], v[168:171], v[156:159]
	v_mfma_f32_16x16x32_bf16 v[128:131], v[104:107], v[176:179], v[128:131]
	v_mfma_f32_16x16x32_bf16 v[124:127], v[112:115], v[176:179], v[124:127]
	v_mfma_f32_16x16x32_bf16 v[96:99], v[104:107], v[184:187], v[96:99]
	v_mfma_f32_16x16x32_bf16 v[92:95], v[112:115], v[184:187], v[92:95]
	v_mfma_f32_16x16x32_bf16 v[80:83], v[104:107], v[192:195], v[80:83]
	v_mfma_f32_16x16x32_bf16 v[76:79], v[112:115], v[192:195], v[76:79]
	s_setprio 0
	s_setprio 1
	v_mfma_f32_16x16x32_bf16 v[152:155], v[132:135], v[164:167], v[152:155]
	v_mfma_f32_16x16x32_bf16 v[148:151], v[140:143], v[164:167], v[148:151]
	v_mfma_f32_16x16x32_bf16 v[120:123], v[132:135], v[172:175], v[120:123]
	v_mfma_f32_16x16x32_bf16 v[116:119], v[140:143], v[172:175], v[116:119]
	v_mfma_f32_16x16x32_bf16 v[88:91], v[132:135], v[180:183], v[88:91]
	v_mfma_f32_16x16x32_bf16 v[84:87], v[140:143], v[180:183], v[84:87]
	v_mfma_f32_16x16x32_bf16 v[72:75], v[132:135], v[188:191], v[72:75]
	v_mfma_f32_16x16x32_bf16 v[68:71], v[140:143], v[188:191], v[68:71]
	v_mfma_f32_16x16x32_bf16 v[152:155], v[136:139], v[168:171], v[152:155]
	v_mfma_f32_16x16x32_bf16 v[148:151], v[144:147], v[168:171], v[148:151]
	v_mfma_f32_16x16x32_bf16 v[120:123], v[136:139], v[176:179], v[120:123]
	v_mfma_f32_16x16x32_bf16 v[116:119], v[144:147], v[176:179], v[116:119]
	v_mfma_f32_16x16x32_bf16 v[88:91], v[136:139], v[184:187], v[88:91]
	v_mfma_f32_16x16x32_bf16 v[84:87], v[144:147], v[184:187], v[84:87]
	v_mfma_f32_16x16x32_bf16 v[72:75], v[136:139], v[192:195], v[72:75]
	v_mfma_f32_16x16x32_bf16 v[68:71], v[144:147], v[192:195], v[68:71]
	s_setprio 0
	s_barrier
	s_add_i32 s23, s34, s69
	v_lshl_add_u64 v[208:209], s[28:29], 0, v[200:201]
	s_mov_b32 m0, s23
	ds_read_b128 v[164:167], v240 offset:16384
	ds_read_b128 v[168:171], v240 offset:17408
	ds_read_b128 v[172:175], v240 offset:18432
	ds_read_b128 v[176:179], v240 offset:19456
	ds_read_b128 v[180:183], v240 offset:20480
	ds_read_b128 v[184:187], v240 offset:21504
	ds_read_b128 v[188:191], v240 offset:22528
	ds_read_b128 v[192:195], v240 offset:23552
	global_load_lds_dwordx4 v[208:209], off
	s_add_i32 m0, s23, 0x2000
	v_lshl_add_u64 v[210:211], s[28:29], 0, v[196:197]
	s_add_u32 s28, s28, s6
	s_addc_u32 s29, s29, s7
	s_add_i32 s21, s21, s69
	global_load_lds_dwordx4 v[210:211], off
	v_lshl_add_u64 v[218:219], s[28:29], 0, v[200:201]
	s_mov_b32 m0, s21
	v_lshl_add_u64 v[220:221], s[28:29], 0, v[196:197]
	global_load_lds_dwordx4 v[218:219], off
	s_add_i32 m0, s21, 0x2000
	v_lshl_add_u64 v[222:223], s[30:31], 0, v[202:203]
	global_load_lds_dwordx4 v[220:221], off
	s_mov_b32 m0, s72
	v_lshl_add_u64 v[224:225], s[30:31], 0, v[198:199]
	global_load_lds_dwordx4 v[222:223], off
	s_mov_b32 m0, s73
	s_nop 0
	global_load_lds_dwordx4 v[224:225], off
	s_waitcnt vmcnt(8)
	s_waitcnt lgkmcnt(0)
	s_barrier
	s_setprio 1
	s_waitcnt lgkmcnt(0)
	v_mfma_f32_16x16x32_bf16 v[64:67], v[100:103], v[164:167], v[64:67]
	v_mfma_f32_16x16x32_bf16 v[60:63], v[108:111], v[164:167], v[60:63]
	v_mfma_f32_16x16x32_bf16 v[48:51], v[100:103], v[172:175], v[48:51]
	v_mfma_f32_16x16x32_bf16 v[44:47], v[108:111], v[172:175], v[44:47]
	v_mfma_f32_16x16x32_bf16 v[32:35], v[100:103], v[180:183], v[32:35]
	v_mfma_f32_16x16x32_bf16 v[28:31], v[108:111], v[180:183], v[28:31]
	v_mfma_f32_16x16x32_bf16 v[16:19], v[100:103], v[188:191], v[16:19]
	v_mfma_f32_16x16x32_bf16 v[12:15], v[108:111], v[188:191], v[12:15]
	v_mfma_f32_16x16x32_bf16 v[64:67], v[104:107], v[168:171], v[64:67]
	v_mfma_f32_16x16x32_bf16 v[60:63], v[112:115], v[168:171], v[60:63]
	v_mfma_f32_16x16x32_bf16 v[48:51], v[104:107], v[176:179], v[48:51]
	v_mfma_f32_16x16x32_bf16 v[44:47], v[112:115], v[176:179], v[44:47]
	v_mfma_f32_16x16x32_bf16 v[32:35], v[104:107], v[184:187], v[32:35]
	v_mfma_f32_16x16x32_bf16 v[28:31], v[112:115], v[184:187], v[28:31]
	v_mfma_f32_16x16x32_bf16 v[16:19], v[104:107], v[192:195], v[16:19]
	v_mfma_f32_16x16x32_bf16 v[12:15], v[112:115], v[192:195], v[12:15]
	s_setprio 0
	s_setprio 1
	v_mfma_f32_16x16x32_bf16 v[56:59], v[132:135], v[164:167], v[56:59]
	v_mfma_f32_16x16x32_bf16 v[52:55], v[140:143], v[164:167], v[52:55]
	v_mfma_f32_16x16x32_bf16 v[40:43], v[132:135], v[172:175], v[40:43]
	v_mfma_f32_16x16x32_bf16 v[36:39], v[140:143], v[172:175], v[36:39]
	v_mfma_f32_16x16x32_bf16 v[24:27], v[132:135], v[180:183], v[24:27]
	v_mfma_f32_16x16x32_bf16 v[20:23], v[140:143], v[180:183], v[20:23]
	v_mfma_f32_16x16x32_bf16 v[8:11], v[132:135], v[188:191], v[8:11]
	v_mfma_f32_16x16x32_bf16 v[4:7], v[140:143], v[188:191], v[4:7]
	v_mfma_f32_16x16x32_bf16 v[56:59], v[136:139], v[168:171], v[56:59]
	v_mfma_f32_16x16x32_bf16 v[52:55], v[144:147], v[168:171], v[52:55]
	v_mfma_f32_16x16x32_bf16 v[40:43], v[136:139], v[176:179], v[40:43]
	v_mfma_f32_16x16x32_bf16 v[36:39], v[144:147], v[176:179], v[36:39]
	v_mfma_f32_16x16x32_bf16 v[24:27], v[136:139], v[184:187], v[24:27]
	v_mfma_f32_16x16x32_bf16 v[20:23], v[144:147], v[184:187], v[20:23]
	v_mfma_f32_16x16x32_bf16 v[8:11], v[136:139], v[192:195], v[8:11]
	v_mfma_f32_16x16x32_bf16 v[4:7], v[144:147], v[192:195], v[4:7]
	s_setprio 0
	s_barrier
	s_add_i32 s21, 0, 0x18000
	v_add_u32_e32 v2, s21, v231
	s_add_i32 s23, 0, 0x1c000
	ds_read_b128 v[100:103], v2
	ds_read_b128 v[104:107], v2 offset:1024
	ds_read_b128 v[108:111], v2 offset:2048
	ds_read_b128 v[112:115], v2 offset:3072
	v_add_u32_e32 v2, s23, v231
	ds_read_b128 v[132:135], v2
	ds_read_b128 v[136:139], v2 offset:1024
	ds_read_b128 v[140:143], v2 offset:2048
	ds_read_b128 v[144:147], v2 offset:3072
	s_add_u32 s28, s30, s6
	s_addc_u32 s29, s31, s7
	s_mov_b32 m0, s74
	v_lshl_add_u64 v[226:227], s[28:29], 0, v[202:203]
	ds_read_b128 v[164:167], v240 offset:32768
	ds_read_b128 v[168:171], v240 offset:33792
	ds_read_b128 v[172:175], v240 offset:34816
	ds_read_b128 v[176:179], v240 offset:35840
	ds_read_b128 v[180:183], v240 offset:36864
	ds_read_b128 v[184:187], v240 offset:37888
	ds_read_b128 v[188:191], v240 offset:38912
	ds_read_b128 v[192:195], v240 offset:39936
	global_load_lds_dwordx4 v[226:227], off
	v_lshl_add_u64 v[226:227], s[28:29], 0, v[198:199]
	s_mov_b32 m0, s75
	s_nop 0
	global_load_lds_dwordx4 v[226:227], off
	s_waitcnt vmcnt(8)
	s_waitcnt lgkmcnt(0)
	s_barrier
	s_setprio 1
	s_waitcnt lgkmcnt(0)
	v_mfma_f32_16x16x32_bf16 v[160:163], v[100:103], v[164:167], v[160:163]
	v_mfma_f32_16x16x32_bf16 v[156:159], v[108:111], v[164:167], v[156:159]
	v_mfma_f32_16x16x32_bf16 v[128:131], v[100:103], v[172:175], v[128:131]
	v_mfma_f32_16x16x32_bf16 v[124:127], v[108:111], v[172:175], v[124:127]
	v_mfma_f32_16x16x32_bf16 v[96:99], v[100:103], v[180:183], v[96:99]
	v_mfma_f32_16x16x32_bf16 v[92:95], v[108:111], v[180:183], v[92:95]
	v_mfma_f32_16x16x32_bf16 v[80:83], v[100:103], v[188:191], v[80:83]
	v_mfma_f32_16x16x32_bf16 v[76:79], v[108:111], v[188:191], v[76:79]
	v_mfma_f32_16x16x32_bf16 v[160:163], v[104:107], v[168:171], v[160:163]
	v_mfma_f32_16x16x32_bf16 v[156:159], v[112:115], v[168:171], v[156:159]
	v_mfma_f32_16x16x32_bf16 v[128:131], v[104:107], v[176:179], v[128:131]
	v_mfma_f32_16x16x32_bf16 v[124:127], v[112:115], v[176:179], v[124:127]
	v_mfma_f32_16x16x32_bf16 v[96:99], v[104:107], v[184:187], v[96:99]
	v_mfma_f32_16x16x32_bf16 v[92:95], v[112:115], v[184:187], v[92:95]
	v_mfma_f32_16x16x32_bf16 v[80:83], v[104:107], v[192:195], v[80:83]
	v_mfma_f32_16x16x32_bf16 v[76:79], v[112:115], v[192:195], v[76:79]
	s_setprio 0
	s_setprio 1
	v_mfma_f32_16x16x32_bf16 v[152:155], v[132:135], v[164:167], v[152:155]
	v_mfma_f32_16x16x32_bf16 v[148:151], v[140:143], v[164:167], v[148:151]
	v_mfma_f32_16x16x32_bf16 v[120:123], v[132:135], v[172:175], v[120:123]
	v_mfma_f32_16x16x32_bf16 v[116:119], v[140:143], v[172:175], v[116:119]
	v_mfma_f32_16x16x32_bf16 v[88:91], v[132:135], v[180:183], v[88:91]
	v_mfma_f32_16x16x32_bf16 v[84:87], v[140:143], v[180:183], v[84:87]
	v_mfma_f32_16x16x32_bf16 v[72:75], v[132:135], v[188:191], v[72:75]
	v_mfma_f32_16x16x32_bf16 v[68:71], v[140:143], v[188:191], v[68:71]
	v_mfma_f32_16x16x32_bf16 v[152:155], v[136:139], v[168:171], v[152:155]
	v_mfma_f32_16x16x32_bf16 v[148:151], v[144:147], v[168:171], v[148:151]
	v_mfma_f32_16x16x32_bf16 v[120:123], v[136:139], v[176:179], v[120:123]
	v_mfma_f32_16x16x32_bf16 v[116:119], v[144:147], v[176:179], v[116:119]
	v_mfma_f32_16x16x32_bf16 v[88:91], v[136:139], v[184:187], v[88:91]
	v_mfma_f32_16x16x32_bf16 v[84:87], v[144:147], v[184:187], v[84:87]
	v_mfma_f32_16x16x32_bf16 v[72:75], v[136:139], v[192:195], v[72:75]
	v_mfma_f32_16x16x32_bf16 v[68:71], v[144:147], v[192:195], v[68:71]
	s_setprio 0
	s_barrier
	s_add_i32 s21, s21, s69
	v_lshl_add_u64 v[208:209], v[208:209], 0, s[24:25]
	s_mov_b32 m0, s21
	ds_read_b128 v[164:167], v240 offset:49152
	ds_read_b128 v[168:171], v240 offset:50176
	ds_read_b128 v[172:175], v240 offset:51200
	ds_read_b128 v[176:179], v240 offset:52224
	ds_read_b128 v[180:183], v240 offset:53248
	ds_read_b128 v[184:187], v240 offset:54272
	ds_read_b128 v[188:191], v240 offset:55296
	ds_read_b128 v[192:195], v240 offset:56320
	global_load_lds_dwordx4 v[208:209], off
	v_lshl_add_u64 v[208:209], v[210:211], 0, s[24:25]
	s_add_i32 m0, s21, 0x2000
	s_add_i32 s21, s23, s69
	global_load_lds_dwordx4 v[208:209], off
	v_lshl_add_u64 v[208:209], v[218:219], 0, s[24:25]
	s_mov_b32 m0, s21
	s_nop 0
	global_load_lds_dwordx4 v[208:209], off
	v_lshl_add_u64 v[208:209], v[220:221], 0, s[24:25]
	s_add_i32 m0, s21, 0x2000
	s_nop 0
	global_load_lds_dwordx4 v[208:209], off
	v_lshl_add_u64 v[208:209], v[222:223], 0, s[24:25]
	s_mov_b32 m0, s79
	s_nop 0
	global_load_lds_dwordx4 v[208:209], off
	v_lshl_add_u64 v[208:209], v[224:225], 0, s[24:25]
	s_mov_b32 m0, s80
	s_nop 0
	global_load_lds_dwordx4 v[208:209], off
	s_waitcnt vmcnt(8)
	s_waitcnt lgkmcnt(0)
	s_barrier
	s_setprio 1
	s_waitcnt lgkmcnt(0)
	v_mfma_f32_16x16x32_bf16 v[64:67], v[100:103], v[164:167], v[64:67]
	v_mfma_f32_16x16x32_bf16 v[60:63], v[108:111], v[164:167], v[60:63]
	v_mfma_f32_16x16x32_bf16 v[48:51], v[100:103], v[172:175], v[48:51]
	v_mfma_f32_16x16x32_bf16 v[44:47], v[108:111], v[172:175], v[44:47]
	v_mfma_f32_16x16x32_bf16 v[32:35], v[100:103], v[180:183], v[32:35]
	v_mfma_f32_16x16x32_bf16 v[28:31], v[108:111], v[180:183], v[28:31]
	v_mfma_f32_16x16x32_bf16 v[16:19], v[100:103], v[188:191], v[16:19]
	v_mfma_f32_16x16x32_bf16 v[12:15], v[108:111], v[188:191], v[12:15]
	v_mfma_f32_16x16x32_bf16 v[64:67], v[104:107], v[168:171], v[64:67]
	v_mfma_f32_16x16x32_bf16 v[60:63], v[112:115], v[168:171], v[60:63]
	v_mfma_f32_16x16x32_bf16 v[48:51], v[104:107], v[176:179], v[48:51]
	v_mfma_f32_16x16x32_bf16 v[44:47], v[112:115], v[176:179], v[44:47]
	v_mfma_f32_16x16x32_bf16 v[32:35], v[104:107], v[184:187], v[32:35]
	v_mfma_f32_16x16x32_bf16 v[28:31], v[112:115], v[184:187], v[28:31]
	v_mfma_f32_16x16x32_bf16 v[16:19], v[104:107], v[192:195], v[16:19]
	v_mfma_f32_16x16x32_bf16 v[12:15], v[112:115], v[192:195], v[12:15]
	s_setprio 0
	s_setprio 1
	v_mfma_f32_16x16x32_bf16 v[56:59], v[132:135], v[164:167], v[56:59]
	v_mfma_f32_16x16x32_bf16 v[52:55], v[140:143], v[164:167], v[52:55]
	v_mfma_f32_16x16x32_bf16 v[40:43], v[132:135], v[172:175], v[40:43]
	v_mfma_f32_16x16x32_bf16 v[36:39], v[140:143], v[172:175], v[36:39]
	v_mfma_f32_16x16x32_bf16 v[24:27], v[132:135], v[180:183], v[24:27]
	v_mfma_f32_16x16x32_bf16 v[20:23], v[140:143], v[180:183], v[20:23]
	v_mfma_f32_16x16x32_bf16 v[8:11], v[132:135], v[188:191], v[8:11]
	v_mfma_f32_16x16x32_bf16 v[4:7], v[140:143], v[188:191], v[4:7]
	v_mfma_f32_16x16x32_bf16 v[56:59], v[136:139], v[168:171], v[56:59]
	v_mfma_f32_16x16x32_bf16 v[52:55], v[144:147], v[168:171], v[52:55]
	v_mfma_f32_16x16x32_bf16 v[40:43], v[136:139], v[176:179], v[40:43]
	v_mfma_f32_16x16x32_bf16 v[36:39], v[144:147], v[176:179], v[36:39]
	v_mfma_f32_16x16x32_bf16 v[24:27], v[136:139], v[184:187], v[24:27]
	v_mfma_f32_16x16x32_bf16 v[20:23], v[144:147], v[184:187], v[20:23]
	v_mfma_f32_16x16x32_bf16 v[8:11], v[136:139], v[192:195], v[8:11]
	v_mfma_f32_16x16x32_bf16 v[4:7], v[144:147], v[192:195], v[4:7]
	s_setprio 0
	s_add_u32 s26, s26, 0x100
	s_addc_u32 s27, s27, 0
	s_add_u32 s19, s19, 0x100
	s_addc_u32 s20, s20, 0
	s_cmp_ge_i32 s22, s78
	s_mov_b32 s21, s22
	s_cbranch_scc1 .Lmy_rot0
	s_add_i32 s22, s21, 2
	s_add_u32 s23, s26, 0x80
	s_addc_u32 s28, s27, 0
	s_add_i32 s34, 0, 0x10000
	s_cmp_eq_u32 s81, s21
	s_cselect_b32 s31, s3, s28
	s_cselect_b32 s30, s2, s23
	s_cselect_b32 s29, s61, s20
	s_cselect_b32 s28, s60, s19
	s_add_i32 s21, 0, 0x14000
	s_branch .LBB0_811
.Lmy_rot0:
	s_barrier
.LBB0_812:
	s_and_b64 vcc, exec, s[54:55]
	s_cbranch_vccz .LBB0_814
	s_barrier

.LBB0_1302:
	s_andn2_b64 vcc, exec, s[42:43]
	s_cbranch_vccnz .LBB0_1305
	s_add_u32 s2, s30, 0x80
	s_addc_u32 s3, s31, 0
	s_add_u32 s19, s26, 0x100
	s_addc_u32 s20, s27, 0
	s_mov_b32 s21, 0
	s_add_i32 s22, s21, 2
	s_add_u32 s23, s2, 0x80
	s_addc_u32 s26, s3, 0
	s_add_i32 s30, 0, 0x10000
	s_cmp_eq_u32 s64, s21
	s_cselect_b32 s27, s47, s26
	s_cselect_b32 s26, s46, s23
	s_cselect_b32 s29, s49, s20
	s_cselect_b32 s28, s48, s19
	s_add_i32 s21, 0, 0x14000
	v_add_u32_e32 v144, s30, v220
	v_add_u32_e32 v160, s21, v220
	ds_read_b128 v[132:135], v144
	ds_read_b128 v[136:139], v144 offset:1024
	ds_read_b128 v[140:143], v144 offset:2048
	ds_read_b128 v[144:147], v144 offset:3072
	ds_read_b128 v[148:151], v160
	ds_read_b128 v[152:155], v160 offset:1024
	ds_read_b128 v[156:159], v160 offset:2048
	ds_read_b128 v[160:163], v160 offset:3072
	v_lshl_add_u64 v[210:211], s[2:3], 0, v[198:199]
	s_add_i32 m0, s56, 0xc000
	ds_read_b128 v[164:167], v221
	ds_read_b128 v[168:171], v221 offset:1024
	ds_read_b128 v[172:175], v221 offset:2048
	ds_read_b128 v[176:179], v221 offset:3072
	ds_read_b128 v[180:183], v221 offset:4096
	ds_read_b128 v[184:187], v221 offset:5120
	ds_read_b128 v[202:205], v221 offset:6144
	ds_read_b128 v[206:209], v221 offset:7168
	global_load_lds_dwordx4 v[210:211], off
	v_lshl_add_u64 v[210:211], s[2:3], 0, v[200:201]
	s_add_i32 m0, s56, 0xe000
	s_nop 0
	global_load_lds_dwordx4 v[210:211], off
	s_waitcnt vmcnt(8)
	s_waitcnt lgkmcnt(0)
	s_barrier
	s_setprio 1
	s_waitcnt lgkmcnt(0)
	v_mfma_f32_16x16x32_bf16 v[124:127], v[132:135], v[164:167], 0
	v_mfma_f32_16x16x32_bf16 v[128:131], v[140:143], v[164:167], 0
	v_mfma_f32_16x16x32_bf16 v[112:115], v[132:135], v[172:175], 0
	v_mfma_f32_16x16x32_bf16 v[108:111], v[140:143], v[172:175], 0
	v_mfma_f32_16x16x32_bf16 v[96:99], v[132:135], v[180:183], 0
	v_mfma_f32_16x16x32_bf16 v[92:95], v[140:143], v[180:183], 0
	v_mfma_f32_16x16x32_bf16 v[80:83], v[132:135], v[202:205], 0
	v_mfma_f32_16x16x32_bf16 v[76:79], v[140:143], v[202:205], 0
	v_mfma_f32_16x16x32_bf16 v[124:127], v[136:139], v[168:171], v[124:127]
	v_mfma_f32_16x16x32_bf16 v[128:131], v[144:147], v[168:171], v[128:131]
	v_mfma_f32_16x16x32_bf16 v[112:115], v[136:139], v[176:179], v[112:115]
	v_mfma_f32_16x16x32_bf16 v[108:111], v[144:147], v[176:179], v[108:111]
	v_mfma_f32_16x16x32_bf16 v[96:99], v[136:139], v[184:187], v[96:99]
	v_mfma_f32_16x16x32_bf16 v[92:95], v[144:147], v[184:187], v[92:95]
	v_mfma_f32_16x16x32_bf16 v[80:83], v[136:139], v[206:209], v[80:83]
	v_mfma_f32_16x16x32_bf16 v[76:79], v[144:147], v[206:209], v[76:79]
	s_setprio 0
	s_setprio 1
	v_mfma_f32_16x16x32_bf16 v[120:123], v[148:151], v[164:167], 0
	v_mfma_f32_16x16x32_bf16 v[116:119], v[156:159], v[164:167], 0
	v_mfma_f32_16x16x32_bf16 v[104:107], v[148:151], v[172:175], 0
	v_mfma_f32_16x16x32_bf16 v[100:103], v[156:159], v[172:175], 0
	v_mfma_f32_16x16x32_bf16 v[88:91], v[148:151], v[180:183], 0
	v_mfma_f32_16x16x32_bf16 v[84:87], v[156:159], v[180:183], 0
	v_mfma_f32_16x16x32_bf16 v[72:75], v[148:151], v[202:205], 0
	v_mfma_f32_16x16x32_bf16 v[68:71], v[156:159], v[202:205], 0
	v_mfma_f32_16x16x32_bf16 v[120:123], v[152:155], v[168:171], v[120:123]
	v_mfma_f32_16x16x32_bf16 v[116:119], v[160:163], v[168:171], v[116:119]
	v_mfma_f32_16x16x32_bf16 v[104:107], v[152:155], v[176:179], v[104:107]
	v_mfma_f32_16x16x32_bf16 v[100:103], v[160:163], v[176:179], v[100:103]
	v_mfma_f32_16x16x32_bf16 v[88:91], v[152:155], v[184:187], v[88:91]
	v_mfma_f32_16x16x32_bf16 v[84:87], v[160:163], v[184:187], v[84:87]
	v_mfma_f32_16x16x32_bf16 v[72:75], v[152:155], v[206:209], v[72:75]
	v_mfma_f32_16x16x32_bf16 v[68:71], v[160:163], v[206:209], v[68:71]
	s_setprio 0
	s_barrier
	s_add_i32 s23, s30, s55
	v_lshl_add_u64 v[210:211], s[28:29], 0, v[2:3]
	s_mov_b32 m0, s23
	ds_read_b128 v[164:167], v221 offset:16384
	ds_read_b128 v[168:171], v221 offset:17408
	ds_read_b128 v[172:175], v221 offset:18432
	ds_read_b128 v[176:179], v221 offset:19456
	ds_read_b128 v[180:183], v221 offset:20480
	ds_read_b128 v[184:187], v221 offset:21504
	ds_read_b128 v[202:205], v221 offset:22528
	ds_read_b128 v[206:209], v221 offset:23552
	global_load_lds_dwordx4 v[210:211], off
	s_add_i32 m0, s23, 0x2000
	v_lshl_add_u64 v[212:213], s[28:29], 0, v[188:189]
	s_add_u32 s28, s28, s8
	s_addc_u32 s29, s29, s9
	s_add_i32 s21, s21, s55
	global_load_lds_dwordx4 v[212:213], off
	v_lshl_add_u64 v[214:215], s[28:29], 0, v[2:3]
	s_mov_b32 m0, s21
	v_lshl_add_u64 v[222:223], s[28:29], 0, v[188:189]
	global_load_lds_dwordx4 v[214:215], off
	s_add_i32 m0, s21, 0x2000
	v_lshl_add_u64 v[224:225], s[26:27], 0, v[192:193]
	global_load_lds_dwordx4 v[222:223], off
	s_mov_b32 m0, s56
	v_lshl_add_u64 v[226:227], s[26:27], 0, v[190:191]
	global_load_lds_dwordx4 v[224:225], off
	s_mov_b32 m0, s57
	s_nop 0
	global_load_lds_dwordx4 v[226:227], off
	s_waitcnt vmcnt(8)
	s_waitcnt lgkmcnt(0)
	s_barrier
	s_setprio 1
	s_waitcnt lgkmcnt(0)
	v_mfma_f32_16x16x32_bf16 v[64:67], v[132:135], v[164:167], 0
	v_mfma_f32_16x16x32_bf16 v[60:63], v[140:143], v[164:167], 0
	v_mfma_f32_16x16x32_bf16 v[48:51], v[132:135], v[172:175], 0
	v_mfma_f32_16x16x32_bf16 v[44:47], v[140:143], v[172:175], 0
	v_mfma_f32_16x16x32_bf16 v[32:35], v[132:135], v[180:183], 0
	v_mfma_f32_16x16x32_bf16 v[28:31], v[140:143], v[180:183], 0
	v_mfma_f32_16x16x32_bf16 v[16:19], v[132:135], v[202:205], 0
	v_mfma_f32_16x16x32_bf16 v[12:15], v[140:143], v[202:205], 0
	v_mfma_f32_16x16x32_bf16 v[64:67], v[136:139], v[168:171], v[64:67]
	v_mfma_f32_16x16x32_bf16 v[60:63], v[144:147], v[168:171], v[60:63]
	v_mfma_f32_16x16x32_bf16 v[48:51], v[136:139], v[176:179], v[48:51]
	v_mfma_f32_16x16x32_bf16 v[44:47], v[144:147], v[176:179], v[44:47]
	v_mfma_f32_16x16x32_bf16 v[32:35], v[136:139], v[184:187], v[32:35]
	v_mfma_f32_16x16x32_bf16 v[28:31], v[144:147], v[184:187], v[28:31]
	v_mfma_f32_16x16x32_bf16 v[16:19], v[136:139], v[206:209], v[16:19]
	v_mfma_f32_16x16x32_bf16 v[12:15], v[144:147], v[206:209], v[12:15]
	s_setprio 0
	s_setprio 1
	v_mfma_f32_16x16x32_bf16 v[56:59], v[148:151], v[164:167], 0
	v_mfma_f32_16x16x32_bf16 v[52:55], v[156:159], v[164:167], 0
	v_mfma_f32_16x16x32_bf16 v[40:43], v[148:151], v[172:175], 0
	v_mfma_f32_16x16x32_bf16 v[36:39], v[156:159], v[172:175], 0
	v_mfma_f32_16x16x32_bf16 v[24:27], v[148:151], v[180:183], 0
	v_mfma_f32_16x16x32_bf16 v[20:23], v[156:159], v[180:183], 0
	v_mfma_f32_16x16x32_bf16 v[8:11], v[148:151], v[202:205], 0
	v_mfma_f32_16x16x32_bf16 v[4:7], v[156:159], v[202:205], 0
	v_mfma_f32_16x16x32_bf16 v[56:59], v[152:155], v[168:171], v[56:59]
	v_mfma_f32_16x16x32_bf16 v[52:55], v[160:163], v[168:171], v[52:55]
	v_mfma_f32_16x16x32_bf16 v[40:43], v[152:155], v[176:179], v[40:43]
	v_mfma_f32_16x16x32_bf16 v[36:39], v[160:163], v[176:179], v[36:39]
	v_mfma_f32_16x16x32_bf16 v[24:27], v[152:155], v[184:187], v[24:27]
	v_mfma_f32_16x16x32_bf16 v[20:23], v[160:163], v[184:187], v[20:23]
	v_mfma_f32_16x16x32_bf16 v[8:11], v[152:155], v[206:209], v[8:11]
	v_mfma_f32_16x16x32_bf16 v[4:7], v[160:163], v[206:209], v[4:7]
	s_setprio 0
	s_barrier
	s_add_i32 s21, 0, 0x18000
	s_add_i32 s23, 0, 0x1c000
	v_add_u32_e32 v144, s21, v220
	v_add_u32_e32 v160, s23, v220
	ds_read_b128 v[132:135], v144
	ds_read_b128 v[136:139], v144 offset:1024
	ds_read_b128 v[140:143], v144 offset:2048
	ds_read_b128 v[144:147], v144 offset:3072
	ds_read_b128 v[148:151], v160
	ds_read_b128 v[152:155], v160 offset:1024
	ds_read_b128 v[156:159], v160 offset:2048
	ds_read_b128 v[160:163], v160 offset:3072
	s_add_u32 s26, s26, s8
	s_addc_u32 s27, s27, s9
	s_mov_b32 m0, s58
	v_lshl_add_u64 v[228:229], s[26:27], 0, v[192:193]
	ds_read_b128 v[164:167], v221 offset:32768
	ds_read_b128 v[168:171], v221 offset:33792
	ds_read_b128 v[172:175], v221 offset:34816
	ds_read_b128 v[176:179], v221 offset:35840
	ds_read_b128 v[180:183], v221 offset:36864
	ds_read_b128 v[184:187], v221 offset:37888
	ds_read_b128 v[202:205], v221 offset:38912
	ds_read_b128 v[206:209], v221 offset:39936
	global_load_lds_dwordx4 v[228:229], off
	v_lshl_add_u64 v[228:229], s[26:27], 0, v[190:191]
	s_mov_b32 m0, s59
	s_nop 0
	global_load_lds_dwordx4 v[228:229], off
	s_waitcnt vmcnt(8)
	s_waitcnt lgkmcnt(0)
	s_barrier
	s_setprio 1
	s_waitcnt lgkmcnt(0)
	v_mfma_f32_16x16x32_bf16 v[124:127], v[132:135], v[164:167], v[124:127]
	v_mfma_f32_16x16x32_bf16 v[128:131], v[140:143], v[164:167], v[128:131]
	v_mfma_f32_16x16x32_bf16 v[112:115], v[132:135], v[172:175], v[112:115]
	v_mfma_f32_16x16x32_bf16 v[108:111], v[140:143], v[172:175], v[108:111]
	v_mfma_f32_16x16x32_bf16 v[96:99], v[132:135], v[180:183], v[96:99]
	v_mfma_f32_16x16x32_bf16 v[92:95], v[140:143], v[180:183], v[92:95]
	v_mfma_f32_16x16x32_bf16 v[80:83], v[132:135], v[202:205], v[80:83]
	v_mfma_f32_16x16x32_bf16 v[76:79], v[140:143], v[202:205], v[76:79]
	v_mfma_f32_16x16x32_bf16 v[124:127], v[136:139], v[168:171], v[124:127]
	v_mfma_f32_16x16x32_bf16 v[128:131], v[144:147], v[168:171], v[128:131]
	v_mfma_f32_16x16x32_bf16 v[112:115], v[136:139], v[176:179], v[112:115]
	v_mfma_f32_16x16x32_bf16 v[108:111], v[144:147], v[176:179], v[108:111]
	v_mfma_f32_16x16x32_bf16 v[96:99], v[136:139], v[184:187], v[96:99]
	v_mfma_f32_16x16x32_bf16 v[92:95], v[144:147], v[184:187], v[92:95]
	v_mfma_f32_16x16x32_bf16 v[80:83], v[136:139], v[206:209], v[80:83]
	v_mfma_f32_16x16x32_bf16 v[76:79], v[144:147], v[206:209], v[76:79]
	s_setprio 0
	s_setprio 1
	v_mfma_f32_16x16x32_bf16 v[120:123], v[148:151], v[164:167], v[120:123]
	v_mfma_f32_16x16x32_bf16 v[116:119], v[156:159], v[164:167], v[116:119]
	v_mfma_f32_16x16x32_bf16 v[104:107], v[148:151], v[172:175], v[104:107]
	v_mfma_f32_16x16x32_bf16 v[100:103], v[156:159], v[172:175], v[100:103]
	v_mfma_f32_16x16x32_bf16 v[88:91], v[148:151], v[180:183], v[88:91]
	v_mfma_f32_16x16x32_bf16 v[84:87], v[156:159], v[180:183], v[84:87]
	v_mfma_f32_16x16x32_bf16 v[72:75], v[148:151], v[202:205], v[72:75]
	v_mfma_f32_16x16x32_bf16 v[68:71], v[156:159], v[202:205], v[68:71]
	v_mfma_f32_16x16x32_bf16 v[120:123], v[152:155], v[168:171], v[120:123]
	v_mfma_f32_16x16x32_bf16 v[116:119], v[160:163], v[168:171], v[116:119]
	v_mfma_f32_16x16x32_bf16 v[104:107], v[152:155], v[176:179], v[104:107]
	v_mfma_f32_16x16x32_bf16 v[100:103], v[160:163], v[176:179], v[100:103]
	v_mfma_f32_16x16x32_bf16 v[88:91], v[152:155], v[184:187], v[88:91]
	v_mfma_f32_16x16x32_bf16 v[84:87], v[160:163], v[184:187], v[84:87]
	v_mfma_f32_16x16x32_bf16 v[72:75], v[152:155], v[206:209], v[72:75]
	v_mfma_f32_16x16x32_bf16 v[68:71], v[160:163], v[206:209], v[68:71]
	s_setprio 0
	s_barrier
	s_add_i32 s21, s21, s55
	v_lshl_add_u64 v[210:211], v[210:211], 0, s[24:25]
	s_mov_b32 m0, s21
	ds_read_b128 v[164:167], v221 offset:49152
	ds_read_b128 v[168:171], v221 offset:50176
	ds_read_b128 v[172:175], v221 offset:51200
	ds_read_b128 v[176:179], v221 offset:52224
	ds_read_b128 v[180:183], v221 offset:53248
	ds_read_b128 v[184:187], v221 offset:54272
	ds_read_b128 v[202:205], v221 offset:55296
	ds_read_b128 v[206:209], v221 offset:56320
	global_load_lds_dwordx4 v[210:211], off
	v_lshl_add_u64 v[210:211], v[212:213], 0, s[24:25]
	s_add_i32 m0, s21, 0x2000
	s_add_i32 s21, s23, s55
	global_load_lds_dwordx4 v[210:211], off
	v_lshl_add_u64 v[210:211], v[214:215], 0, s[24:25]
	s_mov_b32 m0, s21
	s_nop 0
	global_load_lds_dwordx4 v[210:211], off
	v_lshl_add_u64 v[210:211], v[222:223], 0, s[24:25]
	s_add_i32 m0, s21, 0x2000
	s_nop 0
	global_load_lds_dwordx4 v[210:211], off
	v_lshl_add_u64 v[210:211], v[224:225], 0, s[24:25]
	s_mov_b32 m0, s60
	s_nop 0
	global_load_lds_dwordx4 v[210:211], off
	v_lshl_add_u64 v[210:211], v[226:227], 0, s[24:25]
	s_mov_b32 m0, s61
	s_nop 0
	global_load_lds_dwordx4 v[210:211], off
	s_waitcnt vmcnt(8)
	s_waitcnt lgkmcnt(0)
	s_barrier
	s_setprio 1
	s_waitcnt lgkmcnt(0)
	v_mfma_f32_16x16x32_bf16 v[64:67], v[132:135], v[164:167], v[64:67]
	v_mfma_f32_16x16x32_bf16 v[60:63], v[140:143], v[164:167], v[60:63]
	v_mfma_f32_16x16x32_bf16 v[48:51], v[132:135], v[172:175], v[48:51]
	v_mfma_f32_16x16x32_bf16 v[44:47], v[140:143], v[172:175], v[44:47]
	v_mfma_f32_16x16x32_bf16 v[32:35], v[132:135], v[180:183], v[32:35]
	v_mfma_f32_16x16x32_bf16 v[28:31], v[140:143], v[180:183], v[28:31]
	v_mfma_f32_16x16x32_bf16 v[16:19], v[132:135], v[202:205], v[16:19]
	v_mfma_f32_16x16x32_bf16 v[12:15], v[140:143], v[202:205], v[12:15]
	v_mfma_f32_16x16x32_bf16 v[64:67], v[136:139], v[168:171], v[64:67]
	v_mfma_f32_16x16x32_bf16 v[60:63], v[144:147], v[168:171], v[60:63]
	v_mfma_f32_16x16x32_bf16 v[48:51], v[136:139], v[176:179], v[48:51]
	v_mfma_f32_16x16x32_bf16 v[44:47], v[144:147], v[176:179], v[44:47]
	v_mfma_f32_16x16x32_bf16 v[32:35], v[136:139], v[184:187], v[32:35]
	v_mfma_f32_16x16x32_bf16 v[28:31], v[144:147], v[184:187], v[28:31]
	v_mfma_f32_16x16x32_bf16 v[16:19], v[136:139], v[206:209], v[16:19]
	v_mfma_f32_16x16x32_bf16 v[12:15], v[144:147], v[206:209], v[12:15]
	s_setprio 0
	s_setprio 1
	v_mfma_f32_16x16x32_bf16 v[56:59], v[148:151], v[164:167], v[56:59]
	v_mfma_f32_16x16x32_bf16 v[52:55], v[156:159], v[164:167], v[52:55]
	v_mfma_f32_16x16x32_bf16 v[40:43], v[148:151], v[172:175], v[40:43]
	v_mfma_f32_16x16x32_bf16 v[36:39], v[156:159], v[172:175], v[36:39]
	v_mfma_f32_16x16x32_bf16 v[24:27], v[148:151], v[180:183], v[24:27]
	v_mfma_f32_16x16x32_bf16 v[20:23], v[156:159], v[180:183], v[20:23]
	v_mfma_f32_16x16x32_bf16 v[8:11], v[148:151], v[202:205], v[8:11]
	v_mfma_f32_16x16x32_bf16 v[4:7], v[156:159], v[202:205], v[4:7]
	v_mfma_f32_16x16x32_bf16 v[56:59], v[152:155], v[168:171], v[56:59]
	v_mfma_f32_16x16x32_bf16 v[52:55], v[160:163], v[168:171], v[52:55]
	v_mfma_f32_16x16x32_bf16 v[40:43], v[152:155], v[176:179], v[40:43]
	v_mfma_f32_16x16x32_bf16 v[36:39], v[160:163], v[176:179], v[36:39]
	v_mfma_f32_16x16x32_bf16 v[24:27], v[152:155], v[184:187], v[24:27]
	v_mfma_f32_16x16x32_bf16 v[20:23], v[160:163], v[184:187], v[20:23]
	v_mfma_f32_16x16x32_bf16 v[8:11], v[152:155], v[206:209], v[8:11]
	v_mfma_f32_16x16x32_bf16 v[4:7], v[160:163], v[206:209], v[4:7]
	s_setprio 0
	s_add_u32 s2, s2, 0x100
	s_addc_u32 s3, s3, 0
	s_add_u32 s19, s19, 0x100
	s_addc_u32 s20, s20, 0
	s_cmp_ge_i32 s22, s62
	s_mov_b32 s21, s22
	s_cbranch_scc1 .Lmy_rot1
	s_add_i32 s22, s21, 2
	s_add_u32 s23, s2, 0x80
	s_addc_u32 s26, s3, 0
	s_add_i32 s30, 0, 0x10000
	s_cmp_eq_u32 s64, s21
	s_cselect_b32 s27, s47, s26
	s_cselect_b32 s26, s46, s23
	s_cselect_b32 s29, s49, s20
	s_cselect_b32 s28, s48, s19
	s_add_i32 s21, 0, 0x14000
.LBB0_1304:
	s_barrier
	v_add_u32_e32 v144, s30, v220
	v_add_u32_e32 v160, s21, v220
	ds_read_b128 v[132:135], v144
	ds_read_b128 v[136:139], v144 offset:1024
	ds_read_b128 v[140:143], v144 offset:2048
	ds_read_b128 v[144:147], v144 offset:3072
	ds_read_b128 v[148:151], v160
	ds_read_b128 v[152:155], v160 offset:1024
	ds_read_b128 v[156:159], v160 offset:2048
	ds_read_b128 v[160:163], v160 offset:3072
	v_lshl_add_u64 v[210:211], s[2:3], 0, v[198:199]
	s_add_i32 m0, s56, 0xc000
	ds_read_b128 v[164:167], v221
	ds_read_b128 v[168:171], v221 offset:1024
	ds_read_b128 v[172:175], v221 offset:2048
	ds_read_b128 v[176:179], v221 offset:3072
	ds_read_b128 v[180:183], v221 offset:4096
	ds_read_b128 v[184:187], v221 offset:5120
	ds_read_b128 v[202:205], v221 offset:6144
	ds_read_b128 v[206:209], v221 offset:7168
	global_load_lds_dwordx4 v[210:211], off
	v_lshl_add_u64 v[210:211], s[2:3], 0, v[200:201]
	s_add_i32 m0, s56, 0xe000
	s_nop 0
	global_load_lds_dwordx4 v[210:211], off
	s_waitcnt vmcnt(8)
	s_waitcnt lgkmcnt(0)
	s_barrier
	s_setprio 1
	s_waitcnt lgkmcnt(0)
	v_mfma_f32_16x16x32_bf16 v[124:127], v[132:135], v[164:167], v[124:127]
	v_mfma_f32_16x16x32_bf16 v[128:131], v[140:143], v[164:167], v[128:131]
	v_mfma_f32_16x16x32_bf16 v[112:115], v[132:135], v[172:175], v[112:115]
	v_mfma_f32_16x16x32_bf16 v[108:111], v[140:143], v[172:175], v[108:111]
	v_mfma_f32_16x16x32_bf16 v[96:99], v[132:135], v[180:183], v[96:99]
	v_mfma_f32_16x16x32_bf16 v[92:95], v[140:143], v[180:183], v[92:95]
	v_mfma_f32_16x16x32_bf16 v[80:83], v[132:135], v[202:205], v[80:83]
	v_mfma_f32_16x16x32_bf16 v[76:79], v[140:143], v[202:205], v[76:79]
	v_mfma_f32_16x16x32_bf16 v[124:127], v[136:139], v[168:171], v[124:127]
	v_mfma_f32_16x16x32_bf16 v[128:131], v[144:147], v[168:171], v[128:131]
	v_mfma_f32_16x16x32_bf16 v[112:115], v[136:139], v[176:179], v[112:115]
	v_mfma_f32_16x16x32_bf16 v[108:111], v[144:147], v[176:179], v[108:111]
	v_mfma_f32_16x16x32_bf16 v[96:99], v[136:139], v[184:187], v[96:99]
	v_mfma_f32_16x16x32_bf16 v[92:95], v[144:147], v[184:187], v[92:95]
	v_mfma_f32_16x16x32_bf16 v[80:83], v[136:139], v[206:209], v[80:83]
	v_mfma_f32_16x16x32_bf16 v[76:79], v[144:147], v[206:209], v[76:79]
	s_setprio 0
	s_setprio 1
	v_mfma_f32_16x16x32_bf16 v[120:123], v[148:151], v[164:167], v[120:123]
	v_mfma_f32_16x16x32_bf16 v[116:119], v[156:159], v[164:167], v[116:119]
	v_mfma_f32_16x16x32_bf16 v[104:107], v[148:151], v[172:175], v[104:107]
	v_mfma_f32_16x16x32_bf16 v[100:103], v[156:159], v[172:175], v[100:103]
	v_mfma_f32_16x16x32_bf16 v[88:91], v[148:151], v[180:183], v[88:91]
	v_mfma_f32_16x16x32_bf16 v[84:87], v[156:159], v[180:183], v[84:87]
	v_mfma_f32_16x16x32_bf16 v[72:75], v[148:151], v[202:205], v[72:75]
	v_mfma_f32_16x16x32_bf16 v[68:71], v[156:159], v[202:205], v[68:71]
	v_mfma_f32_16x16x32_bf16 v[120:123], v[152:155], v[168:171], v[120:123]
	v_mfma_f32_16x16x32_bf16 v[116:119], v[160:163], v[168:171], v[116:119]
	v_mfma_f32_16x16x32_bf16 v[104:107], v[152:155], v[176:179], v[104:107]
	v_mfma_f32_16x16x32_bf16 v[100:103], v[160:163], v[176:179], v[100:103]
	v_mfma_f32_16x16x32_bf16 v[88:91], v[152:155], v[184:187], v[88:91]
	v_mfma_f32_16x16x32_bf16 v[84:87], v[160:163], v[184:187], v[84:87]
	v_mfma_f32_16x16x32_bf16 v[72:75], v[152:155], v[206:209], v[72:75]
	v_mfma_f32_16x16x32_bf16 v[68:71], v[160:163], v[206:209], v[68:71]
	s_setprio 0
	s_barrier
	s_add_i32 s23, s30, s55
	v_lshl_add_u64 v[210:211], s[28:29], 0, v[2:3]
	s_mov_b32 m0, s23
	ds_read_b128 v[164:167], v221 offset:16384
	ds_read_b128 v[168:171], v221 offset:17408
	ds_read_b128 v[172:175], v221 offset:18432
	ds_read_b128 v[176:179], v221 offset:19456
	ds_read_b128 v[180:183], v221 offset:20480
	ds_read_b128 v[184:187], v221 offset:21504
	ds_read_b128 v[202:205], v221 offset:22528
	ds_read_b128 v[206:209], v221 offset:23552
	global_load_lds_dwordx4 v[210:211], off
	s_add_i32 m0, s23, 0x2000
	v_lshl_add_u64 v[212:213], s[28:29], 0, v[188:189]
	s_add_u32 s28, s28, s8
	s_addc_u32 s29, s29, s9
	s_add_i32 s21, s21, s55
	global_load_lds_dwordx4 v[212:213], off
	v_lshl_add_u64 v[214:215], s[28:29], 0, v[2:3]
	s_mov_b32 m0, s21
	v_lshl_add_u64 v[222:223], s[28:29], 0, v[188:189]
	global_load_lds_dwordx4 v[214:215], off
	s_add_i32 m0, s21, 0x2000
	v_lshl_add_u64 v[224:225], s[26:27], 0, v[192:193]
	global_load_lds_dwordx4 v[222:223], off
	s_mov_b32 m0, s56
	v_lshl_add_u64 v[226:227], s[26:27], 0, v[190:191]
	global_load_lds_dwordx4 v[224:225], off
	s_mov_b32 m0, s57
	s_nop 0
	global_load_lds_dwordx4 v[226:227], off
	s_waitcnt vmcnt(8)
	s_waitcnt lgkmcnt(0)
	s_barrier
	s_setprio 1
	s_waitcnt lgkmcnt(0)
	v_mfma_f32_16x16x32_bf16 v[64:67], v[132:135], v[164:167], v[64:67]
	v_mfma_f32_16x16x32_bf16 v[60:63], v[140:143], v[164:167], v[60:63]
	v_mfma_f32_16x16x32_bf16 v[48:51], v[132:135], v[172:175], v[48:51]
	v_mfma_f32_16x16x32_bf16 v[44:47], v[140:143], v[172:175], v[44:47]
	v_mfma_f32_16x16x32_bf16 v[32:35], v[132:135], v[180:183], v[32:35]
	v_mfma_f32_16x16x32_bf16 v[28:31], v[140:143], v[180:183], v[28:31]
	v_mfma_f32_16x16x32_bf16 v[16:19], v[132:135], v[202:205], v[16:19]
	v_mfma_f32_16x16x32_bf16 v[12:15], v[140:143], v[202:205], v[12:15]
	v_mfma_f32_16x16x32_bf16 v[64:67], v[136:139], v[168:171], v[64:67]
	v_mfma_f32_16x16x32_bf16 v[60:63], v[144:147], v[168:171], v[60:63]
	v_mfma_f32_16x16x32_bf16 v[48:51], v[136:139], v[176:179], v[48:51]
	v_mfma_f32_16x16x32_bf16 v[44:47], v[144:147], v[176:179], v[44:47]
	v_mfma_f32_16x16x32_bf16 v[32:35], v[136:139], v[184:187], v[32:35]
	v_mfma_f32_16x16x32_bf16 v[28:31], v[144:147], v[184:187], v[28:31]
	v_mfma_f32_16x16x32_bf16 v[16:19], v[136:139], v[206:209], v[16:19]
	v_mfma_f32_16x16x32_bf16 v[12:15], v[144:147], v[206:209], v[12:15]
	s_setprio 0
	s_setprio 1
	v_mfma_f32_16x16x32_bf16 v[56:59], v[148:151], v[164:167], v[56:59]
	v_mfma_f32_16x16x32_bf16 v[52:55], v[156:159], v[164:167], v[52:55]
	v_mfma_f32_16x16x32_bf16 v[40:43], v[148:151], v[172:175], v[40:43]
	v_mfma_f32_16x16x32_bf16 v[36:39], v[156:159], v[172:175], v[36:39]
	v_mfma_f32_16x16x32_bf16 v[24:27], v[148:151], v[180:183], v[24:27]
	v_mfma_f32_16x16x32_bf16 v[20:23], v[156:159], v[180:183], v[20:23]
	v_mfma_f32_16x16x32_bf16 v[8:11], v[148:151], v[202:205], v[8:11]
	v_mfma_f32_16x16x32_bf16 v[4:7], v[156:159], v[202:205], v[4:7]
	v_mfma_f32_16x16x32_bf16 v[56:59], v[152:155], v[168:171], v[56:59]
	v_mfma_f32_16x16x32_bf16 v[52:55], v[160:163], v[168:171], v[52:55]
	v_mfma_f32_16x16x32_bf16 v[40:43], v[152:155], v[176:179], v[40:43]
	v_mfma_f32_16x16x32_bf16 v[36:39], v[160:163], v[176:179], v[36:39]
	v_mfma_f32_16x16x32_bf16 v[24:27], v[152:155], v[184:187], v[24:27]
	v_mfma_f32_16x16x32_bf16 v[20:23], v[160:163], v[184:187], v[20:23]
	v_mfma_f32_16x16x32_bf16 v[8:11], v[152:155], v[206:209], v[8:11]
	v_mfma_f32_16x16x32_bf16 v[4:7], v[160:163], v[206:209], v[4:7]
	s_setprio 0
	s_barrier
	s_add_i32 s21, 0, 0x18000
	s_add_i32 s23, 0, 0x1c000
	v_add_u32_e32 v144, s21, v220
	v_add_u32_e32 v160, s23, v220
	ds_read_b128 v[132:135], v144
	ds_read_b128 v[136:139], v144 offset:1024
	ds_read_b128 v[140:143], v144 offset:2048
	ds_read_b128 v[144:147], v144 offset:3072
	ds_read_b128 v[148:151], v160
	ds_read_b128 v[152:155], v160 offset:1024
	ds_read_b128 v[156:159], v160 offset:2048
	ds_read_b128 v[160:163], v160 offset:3072
	s_add_u32 s26, s26, s8
	s_addc_u32 s27, s27, s9
	s_mov_b32 m0, s58
	v_lshl_add_u64 v[228:229], s[26:27], 0, v[192:193]
	ds_read_b128 v[164:167], v221 offset:32768
	ds_read_b128 v[168:171], v221 offset:33792
	ds_read_b128 v[172:175], v221 offset:34816
	ds_read_b128 v[176:179], v221 offset:35840
	ds_read_b128 v[180:183], v221 offset:36864
	ds_read_b128 v[184:187], v221 offset:37888
	ds_read_b128 v[202:205], v221 offset:38912
	ds_read_b128 v[206:209], v221 offset:39936
	global_load_lds_dwordx4 v[228:229], off
	v_lshl_add_u64 v[228:229], s[26:27], 0, v[190:191]
	s_mov_b32 m0, s59
	s_nop 0
	global_load_lds_dwordx4 v[228:229], off
	s_waitcnt vmcnt(8)
	s_waitcnt lgkmcnt(0)
	s_barrier
	s_setprio 1
	s_waitcnt lgkmcnt(0)
	v_mfma_f32_16x16x32_bf16 v[124:127], v[132:135], v[164:167], v[124:127]
	v_mfma_f32_16x16x32_bf16 v[128:131], v[140:143], v[164:167], v[128:131]
	v_mfma_f32_16x16x32_bf16 v[112:115], v[132:135], v[172:175], v[112:115]
	v_mfma_f32_16x16x32_bf16 v[108:111], v[140:143], v[172:175], v[108:111]
	v_mfma_f32_16x16x32_bf16 v[96:99], v[132:135], v[180:183], v[96:99]
	v_mfma_f32_16x16x32_bf16 v[92:95], v[140:143], v[180:183], v[92:95]
	v_mfma_f32_16x16x32_bf16 v[80:83], v[132:135], v[202:205], v[80:83]
	v_mfma_f32_16x16x32_bf16 v[76:79], v[140:143], v[202:205], v[76:79]
	v_mfma_f32_16x16x32_bf16 v[124:127], v[136:139], v[168:171], v[124:127]
	v_mfma_f32_16x16x32_bf16 v[128:131], v[144:147], v[168:171], v[128:131]
	v_mfma_f32_16x16x32_bf16 v[112:115], v[136:139], v[176:179], v[112:115]
	v_mfma_f32_16x16x32_bf16 v[108:111], v[144:147], v[176:179], v[108:111]
	v_mfma_f32_16x16x32_bf16 v[96:99], v[136:139], v[184:187], v[96:99]
	v_mfma_f32_16x16x32_bf16 v[92:95], v[144:147], v[184:187], v[92:95]
	v_mfma_f32_16x16x32_bf16 v[80:83], v[136:139], v[206:209], v[80:83]
	v_mfma_f32_16x16x32_bf16 v[76:79], v[144:147], v[206:209], v[76:79]
	s_setprio 0
	s_setprio 1
	v_mfma_f32_16x16x32_bf16 v[120:123], v[148:151], v[164:167], v[120:123]
	v_mfma_f32_16x16x32_bf16 v[116:119], v[156:159], v[164:167], v[116:119]
	v_mfma_f32_16x16x32_bf16 v[104:107], v[148:151], v[172:175], v[104:107]
	v_mfma_f32_16x16x32_bf16 v[100:103], v[156:159], v[172:175], v[100:103]
	v_mfma_f32_16x16x32_bf16 v[88:91], v[148:151], v[180:183], v[88:91]
	v_mfma_f32_16x16x32_bf16 v[84:87], v[156:159], v[180:183], v[84:87]
	v_mfma_f32_16x16x32_bf16 v[72:75], v[148:151], v[202:205], v[72:75]
	v_mfma_f32_16x16x32_bf16 v[68:71], v[156:159], v[202:205], v[68:71]
	v_mfma_f32_16x16x32_bf16 v[120:123], v[152:155], v[168:171], v[120:123]
	v_mfma_f32_16x16x32_bf16 v[116:119], v[160:163], v[168:171], v[116:119]
	v_mfma_f32_16x16x32_bf16 v[104:107], v[152:155], v[176:179], v[104:107]
	v_mfma_f32_16x16x32_bf16 v[100:103], v[160:163], v[176:179], v[100:103]
	v_mfma_f32_16x16x32_bf16 v[88:91], v[152:155], v[184:187], v[88:91]
	v_mfma_f32_16x16x32_bf16 v[84:87], v[160:163], v[184:187], v[84:87]
	v_mfma_f32_16x16x32_bf16 v[72:75], v[152:155], v[206:209], v[72:75]
	v_mfma_f32_16x16x32_bf16 v[68:71], v[160:163], v[206:209], v[68:71]
	s_setprio 0
	s_barrier
	s_add_i32 s21, s21, s55
	v_lshl_add_u64 v[210:211], v[210:211], 0, s[24:25]
	s_mov_b32 m0, s21
	ds_read_b128 v[164:167], v221 offset:49152
	ds_read_b128 v[168:171], v221 offset:50176
	ds_read_b128 v[172:175], v221 offset:51200
	ds_read_b128 v[176:179], v221 offset:52224
	ds_read_b128 v[180:183], v221 offset:53248
	ds_read_b128 v[184:187], v221 offset:54272
	ds_read_b128 v[202:205], v221 offset:55296
	ds_read_b128 v[206:209], v221 offset:56320
	global_load_lds_dwordx4 v[210:211], off
	v_lshl_add_u64 v[210:211], v[212:213], 0, s[24:25]
	s_add_i32 m0, s21, 0x2000
	s_add_i32 s21, s23, s55
	global_load_lds_dwordx4 v[210:211], off
	v_lshl_add_u64 v[210:211], v[214:215], 0, s[24:25]
	s_mov_b32 m0, s21
	s_nop 0
	global_load_lds_dwordx4 v[210:211], off
	v_lshl_add_u64 v[210:211], v[222:223], 0, s[24:25]
	s_add_i32 m0, s21, 0x2000
	s_nop 0
	global_load_lds_dwordx4 v[210:211], off
	v_lshl_add_u64 v[210:211], v[224:225], 0, s[24:25]
	s_mov_b32 m0, s60
	s_nop 0
	global_load_lds_dwordx4 v[210:211], off
	v_lshl_add_u64 v[210:211], v[226:227], 0, s[24:25]
	s_mov_b32 m0, s61
	s_nop 0
	global_load_lds_dwordx4 v[210:211], off
	s_waitcnt vmcnt(8)
	s_waitcnt lgkmcnt(0)
	s_barrier
	s_setprio 1
	s_waitcnt lgkmcnt(0)
	v_mfma_f32_16x16x32_bf16 v[64:67], v[132:135], v[164:167], v[64:67]
	v_mfma_f32_16x16x32_bf16 v[60:63], v[140:143], v[164:167], v[60:63]
	v_mfma_f32_16x16x32_bf16 v[48:51], v[132:135], v[172:175], v[48:51]
	v_mfma_f32_16x16x32_bf16 v[44:47], v[140:143], v[172:175], v[44:47]
	v_mfma_f32_16x16x32_bf16 v[32:35], v[132:135], v[180:183], v[32:35]
	v_mfma_f32_16x16x32_bf16 v[28:31], v[140:143], v[180:183], v[28:31]
	v_mfma_f32_16x16x32_bf16 v[16:19], v[132:135], v[202:205], v[16:19]
	v_mfma_f32_16x16x32_bf16 v[12:15], v[140:143], v[202:205], v[12:15]
	v_mfma_f32_16x16x32_bf16 v[64:67], v[136:139], v[168:171], v[64:67]
	v_mfma_f32_16x16x32_bf16 v[60:63], v[144:147], v[168:171], v[60:63]
	v_mfma_f32_16x16x32_bf16 v[48:51], v[136:139], v[176:179], v[48:51]
	v_mfma_f32_16x16x32_bf16 v[44:47], v[144:147], v[176:179], v[44:47]
	v_mfma_f32_16x16x32_bf16 v[32:35], v[136:139], v[184:187], v[32:35]
	v_mfma_f32_16x16x32_bf16 v[28:31], v[144:147], v[184:187], v[28:31]
	v_mfma_f32_16x16x32_bf16 v[16:19], v[136:139], v[206:209], v[16:19]
	v_mfma_f32_16x16x32_bf16 v[12:15], v[144:147], v[206:209], v[12:15]
	s_setprio 0
	s_setprio 1
	v_mfma_f32_16x16x32_bf16 v[56:59], v[148:151], v[164:167], v[56:59]
	v_mfma_f32_16x16x32_bf16 v[52:55], v[156:159], v[164:167], v[52:55]
	v_mfma_f32_16x16x32_bf16 v[40:43], v[148:151], v[172:175], v[40:43]
	v_mfma_f32_16x16x32_bf16 v[36:39], v[156:159], v[172:175], v[36:39]
	v_mfma_f32_16x16x32_bf16 v[24:27], v[148:151], v[180:183], v[24:27]
	v_mfma_f32_16x16x32_bf16 v[20:23], v[156:159], v[180:183], v[20:23]
	v_mfma_f32_16x16x32_bf16 v[8:11], v[148:151], v[202:205], v[8:11]
	v_mfma_f32_16x16x32_bf16 v[4:7], v[156:159], v[202:205], v[4:7]
	v_mfma_f32_16x16x32_bf16 v[56:59], v[152:155], v[168:171], v[56:59]
	v_mfma_f32_16x16x32_bf16 v[52:55], v[160:163], v[168:171], v[52:55]
	v_mfma_f32_16x16x32_bf16 v[40:43], v[152:155], v[176:179], v[40:43]
	v_mfma_f32_16x16x32_bf16 v[36:39], v[160:163], v[176:179], v[36:39]
	v_mfma_f32_16x16x32_bf16 v[24:27], v[152:155], v[184:187], v[24:27]
	v_mfma_f32_16x16x32_bf16 v[20:23], v[160:163], v[184:187], v[20:23]
	v_mfma_f32_16x16x32_bf16 v[8:11], v[152:155], v[206:209], v[8:11]
	v_mfma_f32_16x16x32_bf16 v[4:7], v[160:163], v[206:209], v[4:7]
	s_setprio 0
	s_add_u32 s2, s2, 0x100
	s_addc_u32 s3, s3, 0
	s_add_u32 s19, s19, 0x100
	s_addc_u32 s20, s20, 0
	s_cmp_ge_i32 s22, s62
	s_mov_b32 s21, s22
	s_cbranch_scc1 .Lmy_rot1
	s_add_i32 s22, s21, 2
	s_add_u32 s23, s2, 0x80
	s_addc_u32 s26, s3, 0
	s_add_i32 s30, 0, 0x10000
	s_cmp_eq_u32 s64, s21
	s_cselect_b32 s27, s47, s26
	s_cselect_b32 s26, s46, s23
	s_cselect_b32 s29, s49, s20
	s_cselect_b32 s28, s48, s19
	s_add_i32 s21, 0, 0x14000
	s_branch .LBB0_1304
.Lmy_rot1:
	s_barrier
.LBB0_1305:
	s_and_b64 vcc, exec, s[44:45]
	s_cbranch_vccz .LBB0_1307
	s_barrier

.LBB0_1327:
	s_andn2_b64 vcc, exec, s[16:17]
	s_waitcnt lgkmcnt(0)
	s_cbranch_vccnz .LBB0_1330
	s_add_u32 s2, s30, 0x80
	s_addc_u32 s3, s31, 0
	s_add_u32 s19, s26, 0x100
	s_addc_u32 s20, s27, 0
	s_mov_b32 s21, 0
	s_add_i32 s22, s21, 2
	s_add_u32 s23, s2, 0x80
	s_addc_u32 s26, s3, 0
	s_add_i32 s30, 0, 0x10000
	s_cmp_eq_u32 s63, s21
	s_cselect_b32 s27, s45, s26
	s_cselect_b32 s26, s44, s23
	s_cselect_b32 s29, s47, s20
	s_cselect_b32 s28, s46, s19
	s_add_i32 s21, 0, 0x14000
	v_add_u32_e32 v154, s30, v166
	v_add_u32_e32 v162, s21, v166
	ds_read_b128 v[132:135], v154
	ds_read_b128 v[136:139], v154 offset:1024
	ds_read_b128 v[140:143], v154 offset:2048
	ds_read_b128 v[154:157], v154 offset:3072
	ds_read_b128 v[158:161], v162
	ds_read_b128 v[170:173], v162 offset:1024
	ds_read_b128 v[174:177], v162 offset:2048
	ds_read_b128 v[178:181], v162 offset:3072
	v_lshl_add_u64 v[162:163], s[2:3], 0, v[150:151]
	s_add_i32 m0, s53, 0xc000
	ds_read_b128 v[182:185], v168
	ds_read_b128 v[186:189], v168 offset:1024
	ds_read_b128 v[190:193], v168 offset:2048
	ds_read_b128 v[194:197], v168 offset:3072
	ds_read_b128 v[198:201], v168 offset:4096
	ds_read_b128 v[202:205], v168 offset:5120
	ds_read_b128 v[206:209], v168 offset:6144
	ds_read_b128 v[218:221], v168 offset:7168
	global_load_lds_dwordx4 v[162:163], off
	v_lshl_add_u64 v[162:163], s[2:3], 0, v[152:153]
	s_add_i32 m0, s53, 0xe000
	s_nop 0
	global_load_lds_dwordx4 v[162:163], off
	s_waitcnt vmcnt(8)
	s_waitcnt lgkmcnt(0)
	s_barrier
	s_setprio 1
	s_waitcnt lgkmcnt(0)
	v_mfma_f32_16x16x32_bf16 v[128:131], v[132:135], v[182:185], 0
	v_mfma_f32_16x16x32_bf16 v[124:127], v[140:143], v[182:185], 0
	v_mfma_f32_16x16x32_bf16 v[112:115], v[132:135], v[190:193], 0
	v_mfma_f32_16x16x32_bf16 v[108:111], v[140:143], v[190:193], 0
	v_mfma_f32_16x16x32_bf16 v[96:99], v[132:135], v[198:201], 0
	v_mfma_f32_16x16x32_bf16 v[92:95], v[140:143], v[198:201], 0
	v_mfma_f32_16x16x32_bf16 v[80:83], v[132:135], v[206:209], 0
	v_mfma_f32_16x16x32_bf16 v[76:79], v[140:143], v[206:209], 0
	v_mfma_f32_16x16x32_bf16 v[128:131], v[136:139], v[186:189], v[128:131]
	v_mfma_f32_16x16x32_bf16 v[124:127], v[154:157], v[186:189], v[124:127]
	v_mfma_f32_16x16x32_bf16 v[112:115], v[136:139], v[194:197], v[112:115]
	v_mfma_f32_16x16x32_bf16 v[108:111], v[154:157], v[194:197], v[108:111]
	v_mfma_f32_16x16x32_bf16 v[96:99], v[136:139], v[202:205], v[96:99]
	v_mfma_f32_16x16x32_bf16 v[92:95], v[154:157], v[202:205], v[92:95]
	v_mfma_f32_16x16x32_bf16 v[80:83], v[136:139], v[218:221], v[80:83]
	v_mfma_f32_16x16x32_bf16 v[76:79], v[154:157], v[218:221], v[76:79]
	s_setprio 0
	s_setprio 1
	v_mfma_f32_16x16x32_bf16 v[120:123], v[158:161], v[182:185], 0
	v_mfma_f32_16x16x32_bf16 v[116:119], v[174:177], v[182:185], 0
	v_mfma_f32_16x16x32_bf16 v[104:107], v[158:161], v[190:193], 0
	v_mfma_f32_16x16x32_bf16 v[100:103], v[174:177], v[190:193], 0
	v_mfma_f32_16x16x32_bf16 v[88:91], v[158:161], v[198:201], 0
	v_mfma_f32_16x16x32_bf16 v[84:87], v[174:177], v[198:201], 0
	v_mfma_f32_16x16x32_bf16 v[72:75], v[158:161], v[206:209], 0
	v_mfma_f32_16x16x32_bf16 v[68:71], v[174:177], v[206:209], 0
	v_mfma_f32_16x16x32_bf16 v[120:123], v[170:173], v[186:189], v[120:123]
	v_mfma_f32_16x16x32_bf16 v[116:119], v[178:181], v[186:189], v[116:119]
	v_mfma_f32_16x16x32_bf16 v[104:107], v[170:173], v[194:197], v[104:107]
	v_mfma_f32_16x16x32_bf16 v[100:103], v[178:181], v[194:197], v[100:103]
	v_mfma_f32_16x16x32_bf16 v[88:91], v[170:173], v[202:205], v[88:91]
	v_mfma_f32_16x16x32_bf16 v[84:87], v[178:181], v[202:205], v[84:87]
	v_mfma_f32_16x16x32_bf16 v[72:75], v[170:173], v[218:221], v[72:75]
	v_mfma_f32_16x16x32_bf16 v[68:71], v[178:181], v[218:221], v[68:71]
	s_setprio 0
	s_barrier
	s_add_i32 s23, s30, s52
	v_lshl_add_u64 v[162:163], s[28:29], 0, v[2:3]
	s_mov_b32 m0, s23
	ds_read_b128 v[182:185], v168 offset:16384
	ds_read_b128 v[186:189], v168 offset:17408
	ds_read_b128 v[190:193], v168 offset:18432
	ds_read_b128 v[194:197], v168 offset:19456
	ds_read_b128 v[198:201], v168 offset:20480
	ds_read_b128 v[202:205], v168 offset:21504
	ds_read_b128 v[206:209], v168 offset:22528
	ds_read_b128 v[218:221], v168 offset:23552
	global_load_lds_dwordx4 v[162:163], off
	s_add_i32 m0, s23, 0x2000
	v_lshl_add_u64 v[210:211], s[28:29], 0, v[144:145]
	s_add_u32 s28, s28, s8
	s_addc_u32 s29, s29, s9
	s_add_i32 s21, s21, s52
	global_load_lds_dwordx4 v[210:211], off
	v_lshl_add_u64 v[212:213], s[28:29], 0, v[2:3]
	s_mov_b32 m0, s21
	v_lshl_add_u64 v[214:215], s[28:29], 0, v[144:145]
	global_load_lds_dwordx4 v[212:213], off
	s_add_i32 m0, s21, 0x2000
	v_lshl_add_u64 v[222:223], s[26:27], 0, v[148:149]
	global_load_lds_dwordx4 v[214:215], off
	s_mov_b32 m0, s53
	v_lshl_add_u64 v[224:225], s[26:27], 0, v[146:147]
	global_load_lds_dwordx4 v[222:223], off
	s_mov_b32 m0, s54
	s_nop 0
	global_load_lds_dwordx4 v[224:225], off
	s_waitcnt vmcnt(8)
	s_waitcnt lgkmcnt(0)
	s_barrier
	s_setprio 1
	s_waitcnt lgkmcnt(0)
	v_mfma_f32_16x16x32_bf16 v[64:67], v[132:135], v[182:185], 0
	v_mfma_f32_16x16x32_bf16 v[60:63], v[140:143], v[182:185], 0
	v_mfma_f32_16x16x32_bf16 v[48:51], v[132:135], v[190:193], 0
	v_mfma_f32_16x16x32_bf16 v[44:47], v[140:143], v[190:193], 0
	v_mfma_f32_16x16x32_bf16 v[32:35], v[132:135], v[198:201], 0
	v_mfma_f32_16x16x32_bf16 v[28:31], v[140:143], v[198:201], 0
	v_mfma_f32_16x16x32_bf16 v[16:19], v[132:135], v[206:209], 0
	v_mfma_f32_16x16x32_bf16 v[12:15], v[140:143], v[206:209], 0
	v_mfma_f32_16x16x32_bf16 v[64:67], v[136:139], v[186:189], v[64:67]
	v_mfma_f32_16x16x32_bf16 v[60:63], v[154:157], v[186:189], v[60:63]
	v_mfma_f32_16x16x32_bf16 v[48:51], v[136:139], v[194:197], v[48:51]
	v_mfma_f32_16x16x32_bf16 v[44:47], v[154:157], v[194:197], v[44:47]
	v_mfma_f32_16x16x32_bf16 v[32:35], v[136:139], v[202:205], v[32:35]
	v_mfma_f32_16x16x32_bf16 v[28:31], v[154:157], v[202:205], v[28:31]
	v_mfma_f32_16x16x32_bf16 v[16:19], v[136:139], v[218:221], v[16:19]
	v_mfma_f32_16x16x32_bf16 v[12:15], v[154:157], v[218:221], v[12:15]
	s_setprio 0
	s_setprio 1
	v_mfma_f32_16x16x32_bf16 v[56:59], v[158:161], v[182:185], 0
	v_mfma_f32_16x16x32_bf16 v[52:55], v[174:177], v[182:185], 0
	v_mfma_f32_16x16x32_bf16 v[40:43], v[158:161], v[190:193], 0
	v_mfma_f32_16x16x32_bf16 v[36:39], v[174:177], v[190:193], 0
	v_mfma_f32_16x16x32_bf16 v[24:27], v[158:161], v[198:201], 0
	v_mfma_f32_16x16x32_bf16 v[20:23], v[174:177], v[198:201], 0
	v_mfma_f32_16x16x32_bf16 v[8:11], v[158:161], v[206:209], 0
	v_mfma_f32_16x16x32_bf16 v[4:7], v[174:177], v[206:209], 0
	v_mfma_f32_16x16x32_bf16 v[56:59], v[170:173], v[186:189], v[56:59]
	v_mfma_f32_16x16x32_bf16 v[52:55], v[178:181], v[186:189], v[52:55]
	v_mfma_f32_16x16x32_bf16 v[40:43], v[170:173], v[194:197], v[40:43]
	v_mfma_f32_16x16x32_bf16 v[36:39], v[178:181], v[194:197], v[36:39]
	v_mfma_f32_16x16x32_bf16 v[24:27], v[170:173], v[202:205], v[24:27]
	v_mfma_f32_16x16x32_bf16 v[20:23], v[178:181], v[202:205], v[20:23]
	v_mfma_f32_16x16x32_bf16 v[8:11], v[170:173], v[218:221], v[8:11]
	v_mfma_f32_16x16x32_bf16 v[4:7], v[178:181], v[218:221], v[4:7]
	s_setprio 0
	s_barrier
	s_add_i32 s21, 0, 0x18000
	s_add_i32 s23, 0, 0x1c000
	v_add_u32_e32 v154, s21, v166
	v_add_u32_e32 v164, s23, v166
	ds_read_b128 v[132:135], v154
	ds_read_b128 v[136:139], v154 offset:1024
	ds_read_b128 v[140:143], v154 offset:2048
	ds_read_b128 v[154:157], v154 offset:3072
	ds_read_b128 v[158:161], v164
	ds_read_b128 v[170:173], v164 offset:1024
	ds_read_b128 v[174:177], v164 offset:2048
	ds_read_b128 v[178:181], v164 offset:3072
	s_add_u32 s26, s26, s8
	s_addc_u32 s27, s27, s9
	s_mov_b32 m0, s55
	v_lshl_add_u64 v[226:227], s[26:27], 0, v[148:149]
	ds_read_b128 v[182:185], v168 offset:32768
	ds_read_b128 v[186:189], v168 offset:33792
	ds_read_b128 v[190:193], v168 offset:34816
	ds_read_b128 v[194:197], v168 offset:35840
	ds_read_b128 v[198:201], v168 offset:36864
	ds_read_b128 v[202:205], v168 offset:37888
	ds_read_b128 v[206:209], v168 offset:38912
	ds_read_b128 v[218:221], v168 offset:39936
	global_load_lds_dwordx4 v[226:227], off
	v_lshl_add_u64 v[226:227], s[26:27], 0, v[146:147]
	s_mov_b32 m0, s56
	s_nop 0
	global_load_lds_dwordx4 v[226:227], off
	s_waitcnt vmcnt(8)
	s_waitcnt lgkmcnt(0)
	s_barrier
	s_setprio 1
	s_waitcnt lgkmcnt(0)
	v_mfma_f32_16x16x32_bf16 v[128:131], v[132:135], v[182:185], v[128:131]
	v_mfma_f32_16x16x32_bf16 v[124:127], v[140:143], v[182:185], v[124:127]
	v_mfma_f32_16x16x32_bf16 v[112:115], v[132:135], v[190:193], v[112:115]
	v_mfma_f32_16x16x32_bf16 v[108:111], v[140:143], v[190:193], v[108:111]
	v_mfma_f32_16x16x32_bf16 v[96:99], v[132:135], v[198:201], v[96:99]
	v_mfma_f32_16x16x32_bf16 v[92:95], v[140:143], v[198:201], v[92:95]
	v_mfma_f32_16x16x32_bf16 v[80:83], v[132:135], v[206:209], v[80:83]
	v_mfma_f32_16x16x32_bf16 v[76:79], v[140:143], v[206:209], v[76:79]
	v_mfma_f32_16x16x32_bf16 v[128:131], v[136:139], v[186:189], v[128:131]
	v_mfma_f32_16x16x32_bf16 v[124:127], v[154:157], v[186:189], v[124:127]
	v_mfma_f32_16x16x32_bf16 v[112:115], v[136:139], v[194:197], v[112:115]
	v_mfma_f32_16x16x32_bf16 v[108:111], v[154:157], v[194:197], v[108:111]
	v_mfma_f32_16x16x32_bf16 v[96:99], v[136:139], v[202:205], v[96:99]
	v_mfma_f32_16x16x32_bf16 v[92:95], v[154:157], v[202:205], v[92:95]
	v_mfma_f32_16x16x32_bf16 v[80:83], v[136:139], v[218:221], v[80:83]
	v_mfma_f32_16x16x32_bf16 v[76:79], v[154:157], v[218:221], v[76:79]
	s_setprio 0
	s_setprio 1
	v_mfma_f32_16x16x32_bf16 v[120:123], v[158:161], v[182:185], v[120:123]
	v_mfma_f32_16x16x32_bf16 v[116:119], v[174:177], v[182:185], v[116:119]
	v_mfma_f32_16x16x32_bf16 v[104:107], v[158:161], v[190:193], v[104:107]
	v_mfma_f32_16x16x32_bf16 v[100:103], v[174:177], v[190:193], v[100:103]
	v_mfma_f32_16x16x32_bf16 v[88:91], v[158:161], v[198:201], v[88:91]
	v_mfma_f32_16x16x32_bf16 v[84:87], v[174:177], v[198:201], v[84:87]
	v_mfma_f32_16x16x32_bf16 v[72:75], v[158:161], v[206:209], v[72:75]
	v_mfma_f32_16x16x32_bf16 v[68:71], v[174:177], v[206:209], v[68:71]
	v_mfma_f32_16x16x32_bf16 v[120:123], v[170:173], v[186:189], v[120:123]
	v_mfma_f32_16x16x32_bf16 v[116:119], v[178:181], v[186:189], v[116:119]
	v_mfma_f32_16x16x32_bf16 v[104:107], v[170:173], v[194:197], v[104:107]
	v_mfma_f32_16x16x32_bf16 v[100:103], v[178:181], v[194:197], v[100:103]
	v_mfma_f32_16x16x32_bf16 v[88:91], v[170:173], v[202:205], v[88:91]
	v_mfma_f32_16x16x32_bf16 v[84:87], v[178:181], v[202:205], v[84:87]
	v_mfma_f32_16x16x32_bf16 v[72:75], v[170:173], v[218:221], v[72:75]
	v_mfma_f32_16x16x32_bf16 v[68:71], v[178:181], v[218:221], v[68:71]
	s_setprio 0
	s_barrier
	s_add_i32 s21, s21, s52
	v_lshl_add_u64 v[162:163], v[162:163], 0, s[24:25]
	s_mov_b32 m0, s21
	ds_read_b128 v[182:185], v168 offset:49152
	ds_read_b128 v[186:189], v168 offset:50176
	ds_read_b128 v[190:193], v168 offset:51200
	ds_read_b128 v[194:197], v168 offset:52224
	ds_read_b128 v[198:201], v168 offset:53248
	ds_read_b128 v[202:205], v168 offset:54272
	ds_read_b128 v[206:209], v168 offset:55296
	ds_read_b128 v[218:221], v168 offset:56320
	global_load_lds_dwordx4 v[162:163], off
	v_lshl_add_u64 v[162:163], v[210:211], 0, s[24:25]
	s_add_i32 m0, s21, 0x2000
	s_add_i32 s21, s23, s52
	global_load_lds_dwordx4 v[162:163], off
	v_lshl_add_u64 v[162:163], v[212:213], 0, s[24:25]
	s_mov_b32 m0, s21
	s_nop 0
	global_load_lds_dwordx4 v[162:163], off
	v_lshl_add_u64 v[162:163], v[214:215], 0, s[24:25]
	s_add_i32 m0, s21, 0x2000
	s_nop 0
	global_load_lds_dwordx4 v[162:163], off
	v_lshl_add_u64 v[162:163], v[222:223], 0, s[24:25]
	s_mov_b32 m0, s61
	s_nop 0
	global_load_lds_dwordx4 v[162:163], off
	v_lshl_add_u64 v[162:163], v[224:225], 0, s[24:25]
	s_mov_b32 m0, s62
	s_nop 0
	global_load_lds_dwordx4 v[162:163], off
	s_waitcnt vmcnt(8)
	s_waitcnt lgkmcnt(0)
	s_barrier
	s_setprio 1
	s_waitcnt lgkmcnt(0)
	v_mfma_f32_16x16x32_bf16 v[64:67], v[132:135], v[182:185], v[64:67]
	v_mfma_f32_16x16x32_bf16 v[60:63], v[140:143], v[182:185], v[60:63]
	v_mfma_f32_16x16x32_bf16 v[48:51], v[132:135], v[190:193], v[48:51]
	v_mfma_f32_16x16x32_bf16 v[44:47], v[140:143], v[190:193], v[44:47]
	v_mfma_f32_16x16x32_bf16 v[32:35], v[132:135], v[198:201], v[32:35]
	v_mfma_f32_16x16x32_bf16 v[28:31], v[140:143], v[198:201], v[28:31]
	v_mfma_f32_16x16x32_bf16 v[16:19], v[132:135], v[206:209], v[16:19]
	v_mfma_f32_16x16x32_bf16 v[12:15], v[140:143], v[206:209], v[12:15]
	v_mfma_f32_16x16x32_bf16 v[64:67], v[136:139], v[186:189], v[64:67]
	v_mfma_f32_16x16x32_bf16 v[60:63], v[154:157], v[186:189], v[60:63]
	v_mfma_f32_16x16x32_bf16 v[48:51], v[136:139], v[194:197], v[48:51]
	v_mfma_f32_16x16x32_bf16 v[44:47], v[154:157], v[194:197], v[44:47]
	v_mfma_f32_16x16x32_bf16 v[32:35], v[136:139], v[202:205], v[32:35]
	v_mfma_f32_16x16x32_bf16 v[28:31], v[154:157], v[202:205], v[28:31]
	v_mfma_f32_16x16x32_bf16 v[16:19], v[136:139], v[218:221], v[16:19]
	v_mfma_f32_16x16x32_bf16 v[12:15], v[154:157], v[218:221], v[12:15]
	s_setprio 0
	s_setprio 1
	v_mfma_f32_16x16x32_bf16 v[56:59], v[158:161], v[182:185], v[56:59]
	v_mfma_f32_16x16x32_bf16 v[52:55], v[174:177], v[182:185], v[52:55]
	v_mfma_f32_16x16x32_bf16 v[40:43], v[158:161], v[190:193], v[40:43]
	v_mfma_f32_16x16x32_bf16 v[36:39], v[174:177], v[190:193], v[36:39]
	v_mfma_f32_16x16x32_bf16 v[24:27], v[158:161], v[198:201], v[24:27]
	v_mfma_f32_16x16x32_bf16 v[20:23], v[174:177], v[198:201], v[20:23]
	v_mfma_f32_16x16x32_bf16 v[8:11], v[158:161], v[206:209], v[8:11]
	v_mfma_f32_16x16x32_bf16 v[4:7], v[174:177], v[206:209], v[4:7]
	v_mfma_f32_16x16x32_bf16 v[56:59], v[170:173], v[186:189], v[56:59]
	v_mfma_f32_16x16x32_bf16 v[52:55], v[178:181], v[186:189], v[52:55]
	v_mfma_f32_16x16x32_bf16 v[40:43], v[170:173], v[194:197], v[40:43]
	v_mfma_f32_16x16x32_bf16 v[36:39], v[178:181], v[194:197], v[36:39]
	v_mfma_f32_16x16x32_bf16 v[24:27], v[170:173], v[202:205], v[24:27]
	v_mfma_f32_16x16x32_bf16 v[20:23], v[178:181], v[202:205], v[20:23]
	v_mfma_f32_16x16x32_bf16 v[8:11], v[170:173], v[218:221], v[8:11]
	v_mfma_f32_16x16x32_bf16 v[4:7], v[178:181], v[218:221], v[4:7]
	s_setprio 0
	s_add_u32 s2, s2, 0x100
	s_addc_u32 s3, s3, 0
	s_add_u32 s19, s19, 0x100
	s_addc_u32 s20, s20, 0
	s_cmp_ge_i32 s22, s59
	s_mov_b32 s21, s22
	s_cbranch_scc1 .Lmy_rot2
	s_add_i32 s22, s21, 2
	s_add_u32 s23, s2, 0x80
	s_addc_u32 s26, s3, 0
	s_add_i32 s30, 0, 0x10000
	s_cmp_eq_u32 s63, s21
	s_cselect_b32 s27, s45, s26
	s_cselect_b32 s26, s44, s23
	s_cselect_b32 s29, s47, s20
	s_cselect_b32 s28, s46, s19
	s_add_i32 s21, 0, 0x14000
.LBB0_1329:
	s_barrier
	v_add_u32_e32 v154, s30, v166
	v_add_u32_e32 v162, s21, v166
	ds_read_b128 v[132:135], v154
	ds_read_b128 v[136:139], v154 offset:1024
	ds_read_b128 v[140:143], v154 offset:2048
	ds_read_b128 v[154:157], v154 offset:3072
	ds_read_b128 v[158:161], v162
	ds_read_b128 v[170:173], v162 offset:1024
	ds_read_b128 v[174:177], v162 offset:2048
	ds_read_b128 v[178:181], v162 offset:3072
	v_lshl_add_u64 v[162:163], s[2:3], 0, v[150:151]
	s_add_i32 m0, s53, 0xc000
	ds_read_b128 v[182:185], v168
	ds_read_b128 v[186:189], v168 offset:1024
	ds_read_b128 v[190:193], v168 offset:2048
	ds_read_b128 v[194:197], v168 offset:3072
	ds_read_b128 v[198:201], v168 offset:4096
	ds_read_b128 v[202:205], v168 offset:5120
	ds_read_b128 v[206:209], v168 offset:6144
	ds_read_b128 v[218:221], v168 offset:7168
	global_load_lds_dwordx4 v[162:163], off
	v_lshl_add_u64 v[162:163], s[2:3], 0, v[152:153]
	s_add_i32 m0, s53, 0xe000
	s_nop 0
	global_load_lds_dwordx4 v[162:163], off
	s_waitcnt vmcnt(8)
	s_waitcnt lgkmcnt(0)
	s_barrier
	s_setprio 1
	s_waitcnt lgkmcnt(0)
	v_mfma_f32_16x16x32_bf16 v[128:131], v[132:135], v[182:185], v[128:131]
	v_mfma_f32_16x16x32_bf16 v[124:127], v[140:143], v[182:185], v[124:127]
	v_mfma_f32_16x16x32_bf16 v[112:115], v[132:135], v[190:193], v[112:115]
	v_mfma_f32_16x16x32_bf16 v[108:111], v[140:143], v[190:193], v[108:111]
	v_mfma_f32_16x16x32_bf16 v[96:99], v[132:135], v[198:201], v[96:99]
	v_mfma_f32_16x16x32_bf16 v[92:95], v[140:143], v[198:201], v[92:95]
	v_mfma_f32_16x16x32_bf16 v[80:83], v[132:135], v[206:209], v[80:83]
	v_mfma_f32_16x16x32_bf16 v[76:79], v[140:143], v[206:209], v[76:79]
	v_mfma_f32_16x16x32_bf16 v[128:131], v[136:139], v[186:189], v[128:131]
	v_mfma_f32_16x16x32_bf16 v[124:127], v[154:157], v[186:189], v[124:127]
	v_mfma_f32_16x16x32_bf16 v[112:115], v[136:139], v[194:197], v[112:115]
	v_mfma_f32_16x16x32_bf16 v[108:111], v[154:157], v[194:197], v[108:111]
	v_mfma_f32_16x16x32_bf16 v[96:99], v[136:139], v[202:205], v[96:99]
	v_mfma_f32_16x16x32_bf16 v[92:95], v[154:157], v[202:205], v[92:95]
	v_mfma_f32_16x16x32_bf16 v[80:83], v[136:139], v[218:221], v[80:83]
	v_mfma_f32_16x16x32_bf16 v[76:79], v[154:157], v[218:221], v[76:79]
	s_setprio 0
	s_setprio 1
	v_mfma_f32_16x16x32_bf16 v[120:123], v[158:161], v[182:185], v[120:123]
	v_mfma_f32_16x16x32_bf16 v[116:119], v[174:177], v[182:185], v[116:119]
	v_mfma_f32_16x16x32_bf16 v[104:107], v[158:161], v[190:193], v[104:107]
	v_mfma_f32_16x16x32_bf16 v[100:103], v[174:177], v[190:193], v[100:103]
	v_mfma_f32_16x16x32_bf16 v[88:91], v[158:161], v[198:201], v[88:91]
	v_mfma_f32_16x16x32_bf16 v[84:87], v[174:177], v[198:201], v[84:87]
	v_mfma_f32_16x16x32_bf16 v[72:75], v[158:161], v[206:209], v[72:75]
	v_mfma_f32_16x16x32_bf16 v[68:71], v[174:177], v[206:209], v[68:71]
	v_mfma_f32_16x16x32_bf16 v[120:123], v[170:173], v[186:189], v[120:123]
	v_mfma_f32_16x16x32_bf16 v[116:119], v[178:181], v[186:189], v[116:119]
	v_mfma_f32_16x16x32_bf16 v[104:107], v[170:173], v[194:197], v[104:107]
	v_mfma_f32_16x16x32_bf16 v[100:103], v[178:181], v[194:197], v[100:103]
	v_mfma_f32_16x16x32_bf16 v[88:91], v[170:173], v[202:205], v[88:91]
	v_mfma_f32_16x16x32_bf16 v[84:87], v[178:181], v[202:205], v[84:87]
	v_mfma_f32_16x16x32_bf16 v[72:75], v[170:173], v[218:221], v[72:75]
	v_mfma_f32_16x16x32_bf16 v[68:71], v[178:181], v[218:221], v[68:71]
	s_setprio 0
	s_barrier
	s_add_i32 s23, s30, s52
	v_lshl_add_u64 v[162:163], s[28:29], 0, v[2:3]
	s_mov_b32 m0, s23
	ds_read_b128 v[182:185], v168 offset:16384
	ds_read_b128 v[186:189], v168 offset:17408
	ds_read_b128 v[190:193], v168 offset:18432
	ds_read_b128 v[194:197], v168 offset:19456
	ds_read_b128 v[198:201], v168 offset:20480
	ds_read_b128 v[202:205], v168 offset:21504
	ds_read_b128 v[206:209], v168 offset:22528
	ds_read_b128 v[218:221], v168 offset:23552
	global_load_lds_dwordx4 v[162:163], off
	s_add_i32 m0, s23, 0x2000
	v_lshl_add_u64 v[210:211], s[28:29], 0, v[144:145]
	s_add_u32 s28, s28, s8
	s_addc_u32 s29, s29, s9
	s_add_i32 s21, s21, s52
	global_load_lds_dwordx4 v[210:211], off
	v_lshl_add_u64 v[212:213], s[28:29], 0, v[2:3]
	s_mov_b32 m0, s21
	v_lshl_add_u64 v[214:215], s[28:29], 0, v[144:145]
	global_load_lds_dwordx4 v[212:213], off
	s_add_i32 m0, s21, 0x2000
	v_lshl_add_u64 v[222:223], s[26:27], 0, v[148:149]
	global_load_lds_dwordx4 v[214:215], off
	s_mov_b32 m0, s53
	v_lshl_add_u64 v[224:225], s[26:27], 0, v[146:147]
	global_load_lds_dwordx4 v[222:223], off
	s_mov_b32 m0, s54
	s_nop 0
	global_load_lds_dwordx4 v[224:225], off
	s_waitcnt vmcnt(8)
	s_waitcnt lgkmcnt(0)
	s_barrier
	s_setprio 1
	s_waitcnt lgkmcnt(0)
	v_mfma_f32_16x16x32_bf16 v[64:67], v[132:135], v[182:185], v[64:67]
	v_mfma_f32_16x16x32_bf16 v[60:63], v[140:143], v[182:185], v[60:63]
	v_mfma_f32_16x16x32_bf16 v[48:51], v[132:135], v[190:193], v[48:51]
	v_mfma_f32_16x16x32_bf16 v[44:47], v[140:143], v[190:193], v[44:47]
	v_mfma_f32_16x16x32_bf16 v[32:35], v[132:135], v[198:201], v[32:35]
	v_mfma_f32_16x16x32_bf16 v[28:31], v[140:143], v[198:201], v[28:31]
	v_mfma_f32_16x16x32_bf16 v[16:19], v[132:135], v[206:209], v[16:19]
	v_mfma_f32_16x16x32_bf16 v[12:15], v[140:143], v[206:209], v[12:15]
	v_mfma_f32_16x16x32_bf16 v[64:67], v[136:139], v[186:189], v[64:67]
	v_mfma_f32_16x16x32_bf16 v[60:63], v[154:157], v[186:189], v[60:63]
	v_mfma_f32_16x16x32_bf16 v[48:51], v[136:139], v[194:197], v[48:51]
	v_mfma_f32_16x16x32_bf16 v[44:47], v[154:157], v[194:197], v[44:47]
	v_mfma_f32_16x16x32_bf16 v[32:35], v[136:139], v[202:205], v[32:35]
	v_mfma_f32_16x16x32_bf16 v[28:31], v[154:157], v[202:205], v[28:31]
	v_mfma_f32_16x16x32_bf16 v[16:19], v[136:139], v[218:221], v[16:19]
	v_mfma_f32_16x16x32_bf16 v[12:15], v[154:157], v[218:221], v[12:15]
	s_setprio 0
	s_setprio 1
	v_mfma_f32_16x16x32_bf16 v[56:59], v[158:161], v[182:185], v[56:59]
	v_mfma_f32_16x16x32_bf16 v[52:55], v[174:177], v[182:185], v[52:55]
	v_mfma_f32_16x16x32_bf16 v[40:43], v[158:161], v[190:193], v[40:43]
	v_mfma_f32_16x16x32_bf16 v[36:39], v[174:177], v[190:193], v[36:39]
	v_mfma_f32_16x16x32_bf16 v[24:27], v[158:161], v[198:201], v[24:27]
	v_mfma_f32_16x16x32_bf16 v[20:23], v[174:177], v[198:201], v[20:23]
	v_mfma_f32_16x16x32_bf16 v[8:11], v[158:161], v[206:209], v[8:11]
	v_mfma_f32_16x16x32_bf16 v[4:7], v[174:177], v[206:209], v[4:7]
	v_mfma_f32_16x16x32_bf16 v[56:59], v[170:173], v[186:189], v[56:59]
	v_mfma_f32_16x16x32_bf16 v[52:55], v[178:181], v[186:189], v[52:55]
	v_mfma_f32_16x16x32_bf16 v[40:43], v[170:173], v[194:197], v[40:43]
	v_mfma_f32_16x16x32_bf16 v[36:39], v[178:181], v[194:197], v[36:39]
	v_mfma_f32_16x16x32_bf16 v[24:27], v[170:173], v[202:205], v[24:27]
	v_mfma_f32_16x16x32_bf16 v[20:23], v[178:181], v[202:205], v[20:23]
	v_mfma_f32_16x16x32_bf16 v[8:11], v[170:173], v[218:221], v[8:11]
	v_mfma_f32_16x16x32_bf16 v[4:7], v[178:181], v[218:221], v[4:7]
	s_setprio 0
	s_barrier
	s_add_i32 s21, 0, 0x18000
	s_add_i32 s23, 0, 0x1c000
	v_add_u32_e32 v154, s21, v166
	v_add_u32_e32 v164, s23, v166
	ds_read_b128 v[132:135], v154
	ds_read_b128 v[136:139], v154 offset:1024
	ds_read_b128 v[140:143], v154 offset:2048
	ds_read_b128 v[154:157], v154 offset:3072
	ds_read_b128 v[158:161], v164
	ds_read_b128 v[170:173], v164 offset:1024
	ds_read_b128 v[174:177], v164 offset:2048
	ds_read_b128 v[178:181], v164 offset:3072
	s_add_u32 s26, s26, s8
	s_addc_u32 s27, s27, s9
	s_mov_b32 m0, s55
	v_lshl_add_u64 v[226:227], s[26:27], 0, v[148:149]
	ds_read_b128 v[182:185], v168 offset:32768
	ds_read_b128 v[186:189], v168 offset:33792
	ds_read_b128 v[190:193], v168 offset:34816
	ds_read_b128 v[194:197], v168 offset:35840
	ds_read_b128 v[198:201], v168 offset:36864
	ds_read_b128 v[202:205], v168 offset:37888
	ds_read_b128 v[206:209], v168 offset:38912
	ds_read_b128 v[218:221], v168 offset:39936
	global_load_lds_dwordx4 v[226:227], off
	v_lshl_add_u64 v[226:227], s[26:27], 0, v[146:147]
	s_mov_b32 m0, s56
	s_nop 0
	global_load_lds_dwordx4 v[226:227], off
	s_waitcnt vmcnt(8)
	s_waitcnt lgkmcnt(0)
	s_barrier
	s_setprio 1
	s_waitcnt lgkmcnt(0)
	v_mfma_f32_16x16x32_bf16 v[128:131], v[132:135], v[182:185], v[128:131]
	v_mfma_f32_16x16x32_bf16 v[124:127], v[140:143], v[182:185], v[124:127]
	v_mfma_f32_16x16x32_bf16 v[112:115], v[132:135], v[190:193], v[112:115]
	v_mfma_f32_16x16x32_bf16 v[108:111], v[140:143], v[190:193], v[108:111]
	v_mfma_f32_16x16x32_bf16 v[96:99], v[132:135], v[198:201], v[96:99]
	v_mfma_f32_16x16x32_bf16 v[92:95], v[140:143], v[198:201], v[92:95]
	v_mfma_f32_16x16x32_bf16 v[80:83], v[132:135], v[206:209], v[80:83]
	v_mfma_f32_16x16x32_bf16 v[76:79], v[140:143], v[206:209], v[76:79]
	v_mfma_f32_16x16x32_bf16 v[128:131], v[136:139], v[186:189], v[128:131]
	v_mfma_f32_16x16x32_bf16 v[124:127], v[154:157], v[186:189], v[124:127]
	v_mfma_f32_16x16x32_bf16 v[112:115], v[136:139], v[194:197], v[112:115]
	v_mfma_f32_16x16x32_bf16 v[108:111], v[154:157], v[194:197], v[108:111]
	v_mfma_f32_16x16x32_bf16 v[96:99], v[136:139], v[202:205], v[96:99]
	v_mfma_f32_16x16x32_bf16 v[92:95], v[154:157], v[202:205], v[92:95]
	v_mfma_f32_16x16x32_bf16 v[80:83], v[136:139], v[218:221], v[80:83]
	v_mfma_f32_16x16x32_bf16 v[76:79], v[154:157], v[218:221], v[76:79]
	s_setprio 0
	s_setprio 1
	v_mfma_f32_16x16x32_bf16 v[120:123], v[158:161], v[182:185], v[120:123]
	v_mfma_f32_16x16x32_bf16 v[116:119], v[174:177], v[182:185], v[116:119]
	v_mfma_f32_16x16x32_bf16 v[104:107], v[158:161], v[190:193], v[104:107]
	v_mfma_f32_16x16x32_bf16 v[100:103], v[174:177], v[190:193], v[100:103]
	v_mfma_f32_16x16x32_bf16 v[88:91], v[158:161], v[198:201], v[88:91]
	v_mfma_f32_16x16x32_bf16 v[84:87], v[174:177], v[198:201], v[84:87]
	v_mfma_f32_16x16x32_bf16 v[72:75], v[158:161], v[206:209], v[72:75]
	v_mfma_f32_16x16x32_bf16 v[68:71], v[174:177], v[206:209], v[68:71]
	v_mfma_f32_16x16x32_bf16 v[120:123], v[170:173], v[186:189], v[120:123]
	v_mfma_f32_16x16x32_bf16 v[116:119], v[178:181], v[186:189], v[116:119]
	v_mfma_f32_16x16x32_bf16 v[104:107], v[170:173], v[194:197], v[104:107]
	v_mfma_f32_16x16x32_bf16 v[100:103], v[178:181], v[194:197], v[100:103]
	v_mfma_f32_16x16x32_bf16 v[88:91], v[170:173], v[202:205], v[88:91]
	v_mfma_f32_16x16x32_bf16 v[84:87], v[178:181], v[202:205], v[84:87]
	v_mfma_f32_16x16x32_bf16 v[72:75], v[170:173], v[218:221], v[72:75]
	v_mfma_f32_16x16x32_bf16 v[68:71], v[178:181], v[218:221], v[68:71]
	s_setprio 0
	s_barrier
	s_add_i32 s21, s21, s52
	v_lshl_add_u64 v[162:163], v[162:163], 0, s[24:25]
	s_mov_b32 m0, s21
	ds_read_b128 v[182:185], v168 offset:49152
	ds_read_b128 v[186:189], v168 offset:50176
	ds_read_b128 v[190:193], v168 offset:51200
	ds_read_b128 v[194:197], v168 offset:52224
	ds_read_b128 v[198:201], v168 offset:53248
	ds_read_b128 v[202:205], v168 offset:54272
	ds_read_b128 v[206:209], v168 offset:55296
	ds_read_b128 v[218:221], v168 offset:56320
	global_load_lds_dwordx4 v[162:163], off
	v_lshl_add_u64 v[162:163], v[210:211], 0, s[24:25]
	s_add_i32 m0, s21, 0x2000
	s_add_i32 s21, s23, s52
	global_load_lds_dwordx4 v[162:163], off
	v_lshl_add_u64 v[162:163], v[212:213], 0, s[24:25]
	s_mov_b32 m0, s21
	s_nop 0
	global_load_lds_dwordx4 v[162:163], off
	v_lshl_add_u64 v[162:163], v[214:215], 0, s[24:25]
	s_add_i32 m0, s21, 0x2000
	s_nop 0
	global_load_lds_dwordx4 v[162:163], off
	v_lshl_add_u64 v[162:163], v[222:223], 0, s[24:25]
	s_mov_b32 m0, s61
	s_nop 0
	global_load_lds_dwordx4 v[162:163], off
	v_lshl_add_u64 v[162:163], v[224:225], 0, s[24:25]
	s_mov_b32 m0, s62
	s_nop 0
	global_load_lds_dwordx4 v[162:163], off
	s_waitcnt vmcnt(8)
	s_waitcnt lgkmcnt(0)
	s_barrier
	s_setprio 1
	s_waitcnt lgkmcnt(0)
	v_mfma_f32_16x16x32_bf16 v[64:67], v[132:135], v[182:185], v[64:67]
	v_mfma_f32_16x16x32_bf16 v[60:63], v[140:143], v[182:185], v[60:63]
	v_mfma_f32_16x16x32_bf16 v[48:51], v[132:135], v[190:193], v[48:51]
	v_mfma_f32_16x16x32_bf16 v[44:47], v[140:143], v[190:193], v[44:47]
	v_mfma_f32_16x16x32_bf16 v[32:35], v[132:135], v[198:201], v[32:35]
	v_mfma_f32_16x16x32_bf16 v[28:31], v[140:143], v[198:201], v[28:31]
	v_mfma_f32_16x16x32_bf16 v[16:19], v[132:135], v[206:209], v[16:19]
	v_mfma_f32_16x16x32_bf16 v[12:15], v[140:143], v[206:209], v[12:15]
	v_mfma_f32_16x16x32_bf16 v[64:67], v[136:139], v[186:189], v[64:67]
	v_mfma_f32_16x16x32_bf16 v[60:63], v[154:157], v[186:189], v[60:63]
	v_mfma_f32_16x16x32_bf16 v[48:51], v[136:139], v[194:197], v[48:51]
	v_mfma_f32_16x16x32_bf16 v[44:47], v[154:157], v[194:197], v[44:47]
	v_mfma_f32_16x16x32_bf16 v[32:35], v[136:139], v[202:205], v[32:35]
	v_mfma_f32_16x16x32_bf16 v[28:31], v[154:157], v[202:205], v[28:31]
	v_mfma_f32_16x16x32_bf16 v[16:19], v[136:139], v[218:221], v[16:19]
	v_mfma_f32_16x16x32_bf16 v[12:15], v[154:157], v[218:221], v[12:15]
	s_setprio 0
	s_setprio 1
	v_mfma_f32_16x16x32_bf16 v[56:59], v[158:161], v[182:185], v[56:59]
	v_mfma_f32_16x16x32_bf16 v[52:55], v[174:177], v[182:185], v[52:55]
	v_mfma_f32_16x16x32_bf16 v[40:43], v[158:161], v[190:193], v[40:43]
	v_mfma_f32_16x16x32_bf16 v[36:39], v[174:177], v[190:193], v[36:39]
	v_mfma_f32_16x16x32_bf16 v[24:27], v[158:161], v[198:201], v[24:27]
	v_mfma_f32_16x16x32_bf16 v[20:23], v[174:177], v[198:201], v[20:23]
	v_mfma_f32_16x16x32_bf16 v[8:11], v[158:161], v[206:209], v[8:11]
	v_mfma_f32_16x16x32_bf16 v[4:7], v[174:177], v[206:209], v[4:7]
	v_mfma_f32_16x16x32_bf16 v[56:59], v[170:173], v[186:189], v[56:59]
	v_mfma_f32_16x16x32_bf16 v[52:55], v[178:181], v[186:189], v[52:55]
	v_mfma_f32_16x16x32_bf16 v[40:43], v[170:173], v[194:197], v[40:43]
	v_mfma_f32_16x16x32_bf16 v[36:39], v[178:181], v[194:197], v[36:39]
	v_mfma_f32_16x16x32_bf16 v[24:27], v[170:173], v[202:205], v[24:27]
	v_mfma_f32_16x16x32_bf16 v[20:23], v[178:181], v[202:205], v[20:23]
	v_mfma_f32_16x16x32_bf16 v[8:11], v[170:173], v[218:221], v[8:11]
	v_mfma_f32_16x16x32_bf16 v[4:7], v[178:181], v[218:221], v[4:7]
	s_setprio 0
	s_add_u32 s2, s2, 0x100
	s_addc_u32 s3, s3, 0
	s_add_u32 s19, s19, 0x100
	s_addc_u32 s20, s20, 0
	s_cmp_ge_i32 s22, s59
	s_mov_b32 s21, s22
	s_cbranch_scc1 .Lmy_rot2
	s_add_i32 s22, s21, 2
	s_add_u32 s23, s2, 0x80
	s_addc_u32 s26, s3, 0
	s_add_i32 s30, 0, 0x10000
	s_cmp_eq_u32 s63, s21
	s_cselect_b32 s27, s45, s26
	s_cselect_b32 s26, s44, s23
	s_cselect_b32 s29, s47, s20
	s_cselect_b32 s28, s46, s19
	s_add_i32 s21, 0, 0x14000
	s_branch .LBB0_1329
.Lmy_rot2:
	s_barrier
.LBB0_1330:
	s_and_b64 vcc, exec, s[40:41]
	s_cbranch_vccz .LBB0_1332
	s_barrier

.LBB0_3265:
	s_andn2_b64 vcc, exec, s[14:15]
	s_cbranch_vccnz .LBB0_3268
	v_mov_b32_e32 v141, v3
	v_mov_b32_e32 v145, v3
	s_add_u32 s19, s26, 0x100
	s_addc_u32 s20, s27, 0
	v_lshl_add_u64 v[148:149], s[36:37], 0, v[140:141]
	v_lshl_add_u64 v[150:151], s[36:37], 0, v[144:145]
	s_mov_b32 s21, 0
	s_mov_b64 s[26:27], 0
	s_cmp_eq_u32 s56, s21
	s_cselect_b64 vcc, -1, 0
	s_add_i32 s21, s21, 2
	s_add_u32 s30, s26, 0x100
	s_addc_u32 s31, s27, 0
	s_and_b64 s[22:23], vcc, exec
	s_cselect_b32 s23, 0, s30
	s_cselect_b32 s22, 0, s31
	s_add_u32 s40, s2, s23
	s_addc_u32 s41, s3, s22
	s_add_u32 s28, s19, s26
	s_addc_u32 s29, s20, s27
	s_add_i32 s65, 0, 0x10000
	s_and_b64 s[22:23], vcc, exec
	v_add_u32_e32 v141, s65, v147
	s_cselect_b32 s23, s43, s29
	s_cselect_b32 s22, s42, s28
	s_add_i32 s28, 0, 0x14000
	ds_read_b128 v[158:161], v141
	ds_read_b128 v[162:165], v141 offset:1024
	ds_read_b128 v[166:169], v141 offset:2048
	ds_read_b128 v[170:173], v141 offset:3072
	v_add_u32_e32 v141, s28, v147
	ds_read_b128 v[174:177], v141
	ds_read_b128 v[178:181], v141 offset:1024
	ds_read_b128 v[182:185], v141 offset:2048
	ds_read_b128 v[186:189], v141 offset:3072
	v_cndmask_b32_e32 v2, v142, v157, vcc
	v_cndmask_b32_e32 v141, v140, v156, vcc
	v_cndmask_b32_e32 v210, v146, v154, vcc
	v_cndmask_b32_e32 v145, v144, v155, vcc
	v_lshl_add_u64 v[212:213], v[148:149], 0, s[26:27]
	s_add_i32 m0, s49, 0xc000
	ds_read_b128 v[190:193], v153
	ds_read_b128 v[194:197], v153 offset:1024
	ds_read_b128 v[198:201], v153 offset:2048
	ds_read_b128 v[202:205], v153 offset:3072
	ds_read_b128 v[206:209], v153 offset:4096
	ds_read_b128 v[218:221], v153 offset:5120
	ds_read_b128 v[222:225], v153 offset:6144
	ds_read_b128 v[226:229], v153 offset:7168
	global_load_lds_dwordx4 v[212:213], off
	v_lshl_add_u64 v[212:213], v[150:151], 0, s[26:27]
	s_add_i32 m0, s49, 0xe000
	s_nop 0
	global_load_lds_dwordx4 v[212:213], off
	s_waitcnt vmcnt(8)
	s_waitcnt lgkmcnt(0)
	s_barrier
	s_setprio 1
	s_waitcnt lgkmcnt(0)
	v_mfma_f32_16x16x32_bf16 v[124:127], v[158:161], v[190:193], 0
	v_mfma_f32_16x16x32_bf16 v[120:123], v[166:169], v[190:193], 0
	v_mfma_f32_16x16x32_bf16 v[112:115], v[158:161], v[198:201], 0
	v_mfma_f32_16x16x32_bf16 v[104:107], v[166:169], v[198:201], 0
	v_mfma_f32_16x16x32_bf16 v[96:99], v[158:161], v[206:209], 0
	v_mfma_f32_16x16x32_bf16 v[88:91], v[166:169], v[206:209], 0
	v_mfma_f32_16x16x32_bf16 v[80:83], v[158:161], v[222:225], 0
	v_mfma_f32_16x16x32_bf16 v[72:75], v[166:169], v[222:225], 0
	v_mfma_f32_16x16x32_bf16 v[124:127], v[162:165], v[194:197], v[124:127]
	v_mfma_f32_16x16x32_bf16 v[120:123], v[170:173], v[194:197], v[120:123]
	v_mfma_f32_16x16x32_bf16 v[112:115], v[162:165], v[202:205], v[112:115]
	v_mfma_f32_16x16x32_bf16 v[104:107], v[170:173], v[202:205], v[104:107]
	v_mfma_f32_16x16x32_bf16 v[96:99], v[162:165], v[218:221], v[96:99]
	v_mfma_f32_16x16x32_bf16 v[88:91], v[170:173], v[218:221], v[88:91]
	v_mfma_f32_16x16x32_bf16 v[80:83], v[162:165], v[226:229], v[80:83]
	v_mfma_f32_16x16x32_bf16 v[72:75], v[170:173], v[226:229], v[72:75]
	s_setprio 0
	s_setprio 1
	v_mfma_f32_16x16x32_bf16 v[128:131], v[174:177], v[190:193], 0
	v_mfma_f32_16x16x32_bf16 v[116:119], v[182:185], v[190:193], 0
	v_mfma_f32_16x16x32_bf16 v[108:111], v[174:177], v[198:201], 0
	v_mfma_f32_16x16x32_bf16 v[100:103], v[182:185], v[198:201], 0
	v_mfma_f32_16x16x32_bf16 v[92:95], v[174:177], v[206:209], 0
	v_mfma_f32_16x16x32_bf16 v[84:87], v[182:185], v[206:209], 0
	v_mfma_f32_16x16x32_bf16 v[76:79], v[174:177], v[222:225], 0
	v_mfma_f32_16x16x32_bf16 v[68:71], v[182:185], v[222:225], 0
	v_mfma_f32_16x16x32_bf16 v[128:131], v[178:181], v[194:197], v[128:131]
	v_mfma_f32_16x16x32_bf16 v[116:119], v[186:189], v[194:197], v[116:119]
	v_mfma_f32_16x16x32_bf16 v[108:111], v[178:181], v[202:205], v[108:111]
	v_mfma_f32_16x16x32_bf16 v[100:103], v[186:189], v[202:205], v[100:103]
	v_mfma_f32_16x16x32_bf16 v[92:95], v[178:181], v[218:221], v[92:95]
	v_mfma_f32_16x16x32_bf16 v[84:87], v[186:189], v[218:221], v[84:87]
	v_mfma_f32_16x16x32_bf16 v[76:79], v[178:181], v[226:229], v[76:79]
	v_mfma_f32_16x16x32_bf16 v[68:71], v[186:189], v[226:229], v[68:71]
	s_setprio 0
	s_barrier
	s_add_i32 s26, s65, s47
	v_lshl_add_u64 v[212:213], s[22:23], 0, v[138:139]
	s_mov_b32 m0, s26
	ds_read_b128 v[190:193], v153 offset:16384
	ds_read_b128 v[194:197], v153 offset:17408
	ds_read_b128 v[198:201], v153 offset:18432
	ds_read_b128 v[202:205], v153 offset:19456
	ds_read_b128 v[206:209], v153 offset:20480
	ds_read_b128 v[218:221], v153 offset:21504
	ds_read_b128 v[222:225], v153 offset:22528
	ds_read_b128 v[226:229], v153 offset:23552
	global_load_lds_dwordx4 v[212:213], off
	s_add_i32 m0, s26, 0x2000
	v_lshl_add_u64 v[214:215], s[22:23], 0, v[136:137]
	s_add_u32 s22, s22, s6
	s_addc_u32 s23, s23, s7
	s_add_i32 s26, s28, s47
	global_load_lds_dwordx4 v[214:215], off
	v_lshl_add_u64 v[230:231], s[22:23], 0, v[138:139]
	s_mov_b32 m0, s26
	v_lshl_add_u64 v[240:241], s[22:23], 0, v[136:137]
	global_load_lds_dwordx4 v[230:231], off
	s_add_i32 m0, s26, 0x2000
	v_mov_b32_e32 v211, v3
	global_load_lds_dwordx4 v[240:241], off
	s_mov_b32 m0, s49
	v_lshl_add_u64 v[242:243], s[40:41], 0, v[2:3]
	global_load_lds_dwordx4 v2, s[40:41]
	s_mov_b32 m0, s50
	s_nop 0
	global_load_lds_dwordx4 v210, s[40:41]
	s_waitcnt vmcnt(8)
	s_waitcnt lgkmcnt(0)
	v_lshl_add_u64 v[210:211], s[40:41], 0, v[210:211]
	s_barrier
	s_setprio 1
	s_waitcnt lgkmcnt(0)
	v_mfma_f32_16x16x32_bf16 v[64:67], v[158:161], v[190:193], 0
	v_mfma_f32_16x16x32_bf16 v[56:59], v[166:169], v[190:193], 0
	v_mfma_f32_16x16x32_bf16 v[48:51], v[158:161], v[198:201], 0
	v_mfma_f32_16x16x32_bf16 v[40:43], v[166:169], v[198:201], 0
	v_mfma_f32_16x16x32_bf16 v[32:35], v[158:161], v[206:209], 0
	v_mfma_f32_16x16x32_bf16 v[24:27], v[166:169], v[206:209], 0
	v_mfma_f32_16x16x32_bf16 v[16:19], v[158:161], v[222:225], 0
	v_mfma_f32_16x16x32_bf16 v[8:11], v[166:169], v[222:225], 0
	v_mfma_f32_16x16x32_bf16 v[64:67], v[162:165], v[194:197], v[64:67]
	v_mfma_f32_16x16x32_bf16 v[56:59], v[170:173], v[194:197], v[56:59]
	v_mfma_f32_16x16x32_bf16 v[48:51], v[162:165], v[202:205], v[48:51]
	v_mfma_f32_16x16x32_bf16 v[40:43], v[170:173], v[202:205], v[40:43]
	v_mfma_f32_16x16x32_bf16 v[32:35], v[162:165], v[218:221], v[32:35]
	v_mfma_f32_16x16x32_bf16 v[24:27], v[170:173], v[218:221], v[24:27]
	v_mfma_f32_16x16x32_bf16 v[16:19], v[162:165], v[226:229], v[16:19]
	v_mfma_f32_16x16x32_bf16 v[8:11], v[170:173], v[226:229], v[8:11]
	s_setprio 0
	s_setprio 1
	v_mfma_f32_16x16x32_bf16 v[60:63], v[174:177], v[190:193], 0
	v_mfma_f32_16x16x32_bf16 v[52:55], v[182:185], v[190:193], 0
	v_mfma_f32_16x16x32_bf16 v[44:47], v[174:177], v[198:201], 0
	v_mfma_f32_16x16x32_bf16 v[36:39], v[182:185], v[198:201], 0
	v_mfma_f32_16x16x32_bf16 v[28:31], v[174:177], v[206:209], 0
	v_mfma_f32_16x16x32_bf16 v[20:23], v[182:185], v[206:209], 0
	v_mfma_f32_16x16x32_bf16 v[12:15], v[174:177], v[222:225], 0
	v_mfma_f32_16x16x32_bf16 v[4:7], v[182:185], v[222:225], 0
	v_mfma_f32_16x16x32_bf16 v[60:63], v[178:181], v[194:197], v[60:63]
	v_mfma_f32_16x16x32_bf16 v[52:55], v[186:189], v[194:197], v[52:55]
	v_mfma_f32_16x16x32_bf16 v[44:47], v[178:181], v[202:205], v[44:47]
	v_mfma_f32_16x16x32_bf16 v[36:39], v[186:189], v[202:205], v[36:39]
	v_mfma_f32_16x16x32_bf16 v[28:31], v[178:181], v[218:221], v[28:31]
	v_mfma_f32_16x16x32_bf16 v[20:23], v[186:189], v[218:221], v[20:23]
	v_mfma_f32_16x16x32_bf16 v[12:15], v[178:181], v[226:229], v[12:15]
	v_mfma_f32_16x16x32_bf16 v[4:7], v[186:189], v[226:229], v[4:7]
	s_setprio 0
	s_barrier
	s_add_i32 s22, 0, 0x18000
	v_add_u32_e32 v2, s22, v147
	s_add_i32 s23, 0, 0x1c000
	ds_read_b128 v[158:161], v2
	ds_read_b128 v[162:165], v2 offset:1024
	ds_read_b128 v[166:169], v2 offset:2048
	ds_read_b128 v[170:173], v2 offset:3072
	v_add_u32_e32 v2, s23, v147
	ds_read_b128 v[174:177], v2
	ds_read_b128 v[178:181], v2 offset:1024
	ds_read_b128 v[182:185], v2 offset:2048
	ds_read_b128 v[186:189], v2 offset:3072
	s_mov_b32 m0, s51
	ds_read_b128 v[190:193], v153 offset:32768
	ds_read_b128 v[194:197], v153 offset:33792
	ds_read_b128 v[198:201], v153 offset:34816
	ds_read_b128 v[202:205], v153 offset:35840
	ds_read_b128 v[206:209], v153 offset:36864
	ds_read_b128 v[218:221], v153 offset:37888
	ds_read_b128 v[222:225], v153 offset:38912
	ds_read_b128 v[226:229], v153 offset:39936
	global_load_lds_dwordx4 v141, s[40:41]
	s_mov_b32 m0, s52
	s_nop 0
	global_load_lds_dwordx4 v145, s[40:41]
	s_waitcnt vmcnt(8)
	s_waitcnt lgkmcnt(0)
	s_barrier
	s_setprio 1
	s_waitcnt lgkmcnt(0)
	v_mfma_f32_16x16x32_bf16 v[124:127], v[158:161], v[190:193], v[124:127]
	v_mfma_f32_16x16x32_bf16 v[120:123], v[166:169], v[190:193], v[120:123]
	v_mfma_f32_16x16x32_bf16 v[112:115], v[158:161], v[198:201], v[112:115]
	v_mfma_f32_16x16x32_bf16 v[104:107], v[166:169], v[198:201], v[104:107]
	v_mfma_f32_16x16x32_bf16 v[96:99], v[158:161], v[206:209], v[96:99]
	v_mfma_f32_16x16x32_bf16 v[88:91], v[166:169], v[206:209], v[88:91]
	v_mfma_f32_16x16x32_bf16 v[80:83], v[158:161], v[222:225], v[80:83]
	v_mfma_f32_16x16x32_bf16 v[72:75], v[166:169], v[222:225], v[72:75]
	v_mfma_f32_16x16x32_bf16 v[124:127], v[162:165], v[194:197], v[124:127]
	v_mfma_f32_16x16x32_bf16 v[120:123], v[170:173], v[194:197], v[120:123]
	v_mfma_f32_16x16x32_bf16 v[112:115], v[162:165], v[202:205], v[112:115]
	v_mfma_f32_16x16x32_bf16 v[104:107], v[170:173], v[202:205], v[104:107]
	v_mfma_f32_16x16x32_bf16 v[96:99], v[162:165], v[218:221], v[96:99]
	v_mfma_f32_16x16x32_bf16 v[88:91], v[170:173], v[218:221], v[88:91]
	v_mfma_f32_16x16x32_bf16 v[80:83], v[162:165], v[226:229], v[80:83]
	v_mfma_f32_16x16x32_bf16 v[72:75], v[170:173], v[226:229], v[72:75]
	s_setprio 0
	s_setprio 1
	v_mfma_f32_16x16x32_bf16 v[128:131], v[174:177], v[190:193], v[128:131]
	v_mfma_f32_16x16x32_bf16 v[116:119], v[182:185], v[190:193], v[116:119]
	v_mfma_f32_16x16x32_bf16 v[108:111], v[174:177], v[198:201], v[108:111]
	v_mfma_f32_16x16x32_bf16 v[100:103], v[182:185], v[198:201], v[100:103]
	v_mfma_f32_16x16x32_bf16 v[92:95], v[174:177], v[206:209], v[92:95]
	v_mfma_f32_16x16x32_bf16 v[84:87], v[182:185], v[206:209], v[84:87]
	v_mfma_f32_16x16x32_bf16 v[76:79], v[174:177], v[222:225], v[76:79]
	v_mfma_f32_16x16x32_bf16 v[68:71], v[182:185], v[222:225], v[68:71]
	v_mfma_f32_16x16x32_bf16 v[128:131], v[178:181], v[194:197], v[128:131]
	v_mfma_f32_16x16x32_bf16 v[116:119], v[186:189], v[194:197], v[116:119]
	v_mfma_f32_16x16x32_bf16 v[108:111], v[178:181], v[202:205], v[108:111]
	v_mfma_f32_16x16x32_bf16 v[100:103], v[186:189], v[202:205], v[100:103]
	v_mfma_f32_16x16x32_bf16 v[92:95], v[178:181], v[218:221], v[92:95]
	v_mfma_f32_16x16x32_bf16 v[84:87], v[186:189], v[218:221], v[84:87]
	v_mfma_f32_16x16x32_bf16 v[76:79], v[178:181], v[226:229], v[76:79]
	v_mfma_f32_16x16x32_bf16 v[68:71], v[186:189], v[226:229], v[68:71]
	s_setprio 0
	s_barrier
	s_add_i32 s22, s22, s47
	v_lshl_add_u64 v[212:213], v[212:213], 0, s[24:25]
	s_mov_b32 m0, s22
	ds_read_b128 v[190:193], v153 offset:49152
	ds_read_b128 v[194:197], v153 offset:50176
	ds_read_b128 v[198:201], v153 offset:51200
	ds_read_b128 v[202:205], v153 offset:52224
	ds_read_b128 v[206:209], v153 offset:53248
	ds_read_b128 v[218:221], v153 offset:54272
	ds_read_b128 v[222:225], v153 offset:55296
	ds_read_b128 v[226:229], v153 offset:56320
	global_load_lds_dwordx4 v[212:213], off
	v_lshl_add_u64 v[212:213], v[214:215], 0, s[24:25]
	s_add_i32 m0, s22, 0x2000
	s_add_i32 s22, s23, s47
	global_load_lds_dwordx4 v[212:213], off
	v_lshl_add_u64 v[212:213], v[230:231], 0, s[24:25]
	s_mov_b32 m0, s22
	v_lshl_add_u64 v[210:211], v[210:211], 0, s[24:25]
	global_load_lds_dwordx4 v[212:213], off
	v_lshl_add_u64 v[212:213], v[240:241], 0, s[24:25]
	s_add_i32 m0, s22, 0x2000
	s_nop 0
	global_load_lds_dwordx4 v[212:213], off
	v_lshl_add_u64 v[212:213], v[242:243], 0, s[24:25]
	s_mov_b32 m0, s53
	s_nop 0
	global_load_lds_dwordx4 v[212:213], off
	s_mov_b32 m0, s54
	s_nop 0
	global_load_lds_dwordx4 v[210:211], off
	s_waitcnt vmcnt(8)
	s_waitcnt lgkmcnt(0)
	s_barrier
	s_setprio 1
	s_waitcnt lgkmcnt(0)
	v_mfma_f32_16x16x32_bf16 v[64:67], v[158:161], v[190:193], v[64:67]
	v_mfma_f32_16x16x32_bf16 v[56:59], v[166:169], v[190:193], v[56:59]
	v_mfma_f32_16x16x32_bf16 v[48:51], v[158:161], v[198:201], v[48:51]
	v_mfma_f32_16x16x32_bf16 v[40:43], v[166:169], v[198:201], v[40:43]
	v_mfma_f32_16x16x32_bf16 v[32:35], v[158:161], v[206:209], v[32:35]
	v_mfma_f32_16x16x32_bf16 v[24:27], v[166:169], v[206:209], v[24:27]
	v_mfma_f32_16x16x32_bf16 v[16:19], v[158:161], v[222:225], v[16:19]
	v_mfma_f32_16x16x32_bf16 v[8:11], v[166:169], v[222:225], v[8:11]
	v_mfma_f32_16x16x32_bf16 v[64:67], v[162:165], v[194:197], v[64:67]
	v_mfma_f32_16x16x32_bf16 v[56:59], v[170:173], v[194:197], v[56:59]
	v_mfma_f32_16x16x32_bf16 v[48:51], v[162:165], v[202:205], v[48:51]
	v_mfma_f32_16x16x32_bf16 v[40:43], v[170:173], v[202:205], v[40:43]
	v_mfma_f32_16x16x32_bf16 v[32:35], v[162:165], v[218:221], v[32:35]
	v_mfma_f32_16x16x32_bf16 v[24:27], v[170:173], v[218:221], v[24:27]
	v_mfma_f32_16x16x32_bf16 v[16:19], v[162:165], v[226:229], v[16:19]
	v_mfma_f32_16x16x32_bf16 v[8:11], v[170:173], v[226:229], v[8:11]
	s_setprio 0
	s_setprio 1
	v_mfma_f32_16x16x32_bf16 v[60:63], v[174:177], v[190:193], v[60:63]
	v_mfma_f32_16x16x32_bf16 v[52:55], v[182:185], v[190:193], v[52:55]
	v_mfma_f32_16x16x32_bf16 v[44:47], v[174:177], v[198:201], v[44:47]
	v_mfma_f32_16x16x32_bf16 v[36:39], v[182:185], v[198:201], v[36:39]
	v_mfma_f32_16x16x32_bf16 v[28:31], v[174:177], v[206:209], v[28:31]
	v_mfma_f32_16x16x32_bf16 v[20:23], v[182:185], v[206:209], v[20:23]
	v_mfma_f32_16x16x32_bf16 v[12:15], v[174:177], v[222:225], v[12:15]
	v_mfma_f32_16x16x32_bf16 v[4:7], v[182:185], v[222:225], v[4:7]
	v_mfma_f32_16x16x32_bf16 v[60:63], v[178:181], v[194:197], v[60:63]
	v_mfma_f32_16x16x32_bf16 v[52:55], v[186:189], v[194:197], v[52:55]
	v_mfma_f32_16x16x32_bf16 v[44:47], v[178:181], v[202:205], v[44:47]
	v_mfma_f32_16x16x32_bf16 v[36:39], v[186:189], v[202:205], v[36:39]
	v_mfma_f32_16x16x32_bf16 v[28:31], v[178:181], v[218:221], v[28:31]
	v_mfma_f32_16x16x32_bf16 v[20:23], v[186:189], v[218:221], v[20:23]
	v_mfma_f32_16x16x32_bf16 v[12:15], v[178:181], v[226:229], v[12:15]
	v_mfma_f32_16x16x32_bf16 v[4:7], v[186:189], v[226:229], v[4:7]
	s_setprio 0
	s_cmp_ge_i32 s21, s55
	s_mov_b64 s[26:27], s[30:31]
	s_cbranch_scc1 .Lmy_rot3
	s_cmp_eq_u32 s56, s21
	s_cselect_b64 vcc, -1, 0
	s_add_i32 s21, s21, 2
	s_add_u32 s30, s26, 0x100
	s_addc_u32 s31, s27, 0
	s_and_b64 s[22:23], vcc, exec
	s_cselect_b32 s23, 0, s30
	s_cselect_b32 s22, 0, s31
	s_add_u32 s40, s2, s23
	s_addc_u32 s41, s3, s22
	s_add_u32 s28, s19, s26
	s_addc_u32 s29, s20, s27
	s_add_i32 s65, 0, 0x10000
	s_and_b64 s[22:23], vcc, exec
	s_cselect_b32 s23, s43, s29
	s_cselect_b32 s22, s42, s28
	s_add_i32 s28, 0, 0x14000
.LBB0_3267:
	s_barrier
	v_add_u32_e32 v141, s65, v147
	ds_read_b128 v[158:161], v141
	ds_read_b128 v[162:165], v141 offset:1024
	ds_read_b128 v[166:169], v141 offset:2048
	ds_read_b128 v[170:173], v141 offset:3072
	v_add_u32_e32 v141, s28, v147
	ds_read_b128 v[174:177], v141
	ds_read_b128 v[178:181], v141 offset:1024
	ds_read_b128 v[182:185], v141 offset:2048
	ds_read_b128 v[186:189], v141 offset:3072
	v_cndmask_b32_e32 v2, v142, v157, vcc
	v_cndmask_b32_e32 v141, v140, v156, vcc
	v_cndmask_b32_e32 v210, v146, v154, vcc
	v_cndmask_b32_e32 v145, v144, v155, vcc
	v_lshl_add_u64 v[212:213], v[148:149], 0, s[26:27]
	s_add_i32 m0, s49, 0xc000
	ds_read_b128 v[190:193], v153
	ds_read_b128 v[194:197], v153 offset:1024
	ds_read_b128 v[198:201], v153 offset:2048
	ds_read_b128 v[202:205], v153 offset:3072
	ds_read_b128 v[206:209], v153 offset:4096
	ds_read_b128 v[218:221], v153 offset:5120
	ds_read_b128 v[222:225], v153 offset:6144
	ds_read_b128 v[226:229], v153 offset:7168
	global_load_lds_dwordx4 v[212:213], off
	v_lshl_add_u64 v[212:213], v[150:151], 0, s[26:27]
	s_add_i32 m0, s49, 0xe000
	s_nop 0
	global_load_lds_dwordx4 v[212:213], off
	s_waitcnt vmcnt(8)
	s_waitcnt lgkmcnt(0)
	s_barrier
	s_setprio 1
	s_waitcnt lgkmcnt(0)
	v_mfma_f32_16x16x32_bf16 v[124:127], v[158:161], v[190:193], v[124:127]
	v_mfma_f32_16x16x32_bf16 v[120:123], v[166:169], v[190:193], v[120:123]
	v_mfma_f32_16x16x32_bf16 v[112:115], v[158:161], v[198:201], v[112:115]
	v_mfma_f32_16x16x32_bf16 v[104:107], v[166:169], v[198:201], v[104:107]
	v_mfma_f32_16x16x32_bf16 v[96:99], v[158:161], v[206:209], v[96:99]
	v_mfma_f32_16x16x32_bf16 v[88:91], v[166:169], v[206:209], v[88:91]
	v_mfma_f32_16x16x32_bf16 v[80:83], v[158:161], v[222:225], v[80:83]
	v_mfma_f32_16x16x32_bf16 v[72:75], v[166:169], v[222:225], v[72:75]
	v_mfma_f32_16x16x32_bf16 v[124:127], v[162:165], v[194:197], v[124:127]
	v_mfma_f32_16x16x32_bf16 v[120:123], v[170:173], v[194:197], v[120:123]
	v_mfma_f32_16x16x32_bf16 v[112:115], v[162:165], v[202:205], v[112:115]
	v_mfma_f32_16x16x32_bf16 v[104:107], v[170:173], v[202:205], v[104:107]
	v_mfma_f32_16x16x32_bf16 v[96:99], v[162:165], v[218:221], v[96:99]
	v_mfma_f32_16x16x32_bf16 v[88:91], v[170:173], v[218:221], v[88:91]
	v_mfma_f32_16x16x32_bf16 v[80:83], v[162:165], v[226:229], v[80:83]
	v_mfma_f32_16x16x32_bf16 v[72:75], v[170:173], v[226:229], v[72:75]
	s_setprio 0
	s_setprio 1
	v_mfma_f32_16x16x32_bf16 v[128:131], v[174:177], v[190:193], v[128:131]
	v_mfma_f32_16x16x32_bf16 v[116:119], v[182:185], v[190:193], v[116:119]
	v_mfma_f32_16x16x32_bf16 v[108:111], v[174:177], v[198:201], v[108:111]
	v_mfma_f32_16x16x32_bf16 v[100:103], v[182:185], v[198:201], v[100:103]
	v_mfma_f32_16x16x32_bf16 v[92:95], v[174:177], v[206:209], v[92:95]
	v_mfma_f32_16x16x32_bf16 v[84:87], v[182:185], v[206:209], v[84:87]
	v_mfma_f32_16x16x32_bf16 v[76:79], v[174:177], v[222:225], v[76:79]
	v_mfma_f32_16x16x32_bf16 v[68:71], v[182:185], v[222:225], v[68:71]
	v_mfma_f32_16x16x32_bf16 v[128:131], v[178:181], v[194:197], v[128:131]
	v_mfma_f32_16x16x32_bf16 v[116:119], v[186:189], v[194:197], v[116:119]
	v_mfma_f32_16x16x32_bf16 v[108:111], v[178:181], v[202:205], v[108:111]
	v_mfma_f32_16x16x32_bf16 v[100:103], v[186:189], v[202:205], v[100:103]
	v_mfma_f32_16x16x32_bf16 v[92:95], v[178:181], v[218:221], v[92:95]
	v_mfma_f32_16x16x32_bf16 v[84:87], v[186:189], v[218:221], v[84:87]
	v_mfma_f32_16x16x32_bf16 v[76:79], v[178:181], v[226:229], v[76:79]
	v_mfma_f32_16x16x32_bf16 v[68:71], v[186:189], v[226:229], v[68:71]
	s_setprio 0
	s_barrier
	s_add_i32 s26, s65, s47
	v_lshl_add_u64 v[212:213], s[22:23], 0, v[138:139]
	s_mov_b32 m0, s26
	ds_read_b128 v[190:193], v153 offset:16384
	ds_read_b128 v[194:197], v153 offset:17408
	ds_read_b128 v[198:201], v153 offset:18432
	ds_read_b128 v[202:205], v153 offset:19456
	ds_read_b128 v[206:209], v153 offset:20480
	ds_read_b128 v[218:221], v153 offset:21504
	ds_read_b128 v[222:225], v153 offset:22528
	ds_read_b128 v[226:229], v153 offset:23552
	global_load_lds_dwordx4 v[212:213], off
	s_add_i32 m0, s26, 0x2000
	v_lshl_add_u64 v[214:215], s[22:23], 0, v[136:137]
	s_add_u32 s22, s22, s6
	s_addc_u32 s23, s23, s7
	s_add_i32 s26, s28, s47
	global_load_lds_dwordx4 v[214:215], off
	v_lshl_add_u64 v[230:231], s[22:23], 0, v[138:139]
	s_mov_b32 m0, s26
	v_lshl_add_u64 v[240:241], s[22:23], 0, v[136:137]
	global_load_lds_dwordx4 v[230:231], off
	s_add_i32 m0, s26, 0x2000
	v_mov_b32_e32 v211, v3
	global_load_lds_dwordx4 v[240:241], off
	s_mov_b32 m0, s49
	v_lshl_add_u64 v[242:243], s[40:41], 0, v[2:3]
	global_load_lds_dwordx4 v2, s[40:41]
	s_mov_b32 m0, s50
	s_nop 0
	global_load_lds_dwordx4 v210, s[40:41]
	s_waitcnt vmcnt(8)
	s_waitcnt lgkmcnt(0)
	v_lshl_add_u64 v[210:211], s[40:41], 0, v[210:211]
	s_barrier
	s_setprio 1
	s_waitcnt lgkmcnt(0)
	v_mfma_f32_16x16x32_bf16 v[64:67], v[158:161], v[190:193], v[64:67]
	v_mfma_f32_16x16x32_bf16 v[56:59], v[166:169], v[190:193], v[56:59]
	v_mfma_f32_16x16x32_bf16 v[48:51], v[158:161], v[198:201], v[48:51]
	v_mfma_f32_16x16x32_bf16 v[40:43], v[166:169], v[198:201], v[40:43]
	v_mfma_f32_16x16x32_bf16 v[32:35], v[158:161], v[206:209], v[32:35]
	v_mfma_f32_16x16x32_bf16 v[24:27], v[166:169], v[206:209], v[24:27]
	v_mfma_f32_16x16x32_bf16 v[16:19], v[158:161], v[222:225], v[16:19]
	v_mfma_f32_16x16x32_bf16 v[8:11], v[166:169], v[222:225], v[8:11]
	v_mfma_f32_16x16x32_bf16 v[64:67], v[162:165], v[194:197], v[64:67]
	v_mfma_f32_16x16x32_bf16 v[56:59], v[170:173], v[194:197], v[56:59]
	v_mfma_f32_16x16x32_bf16 v[48:51], v[162:165], v[202:205], v[48:51]
	v_mfma_f32_16x16x32_bf16 v[40:43], v[170:173], v[202:205], v[40:43]
	v_mfma_f32_16x16x32_bf16 v[32:35], v[162:165], v[218:221], v[32:35]
	v_mfma_f32_16x16x32_bf16 v[24:27], v[170:173], v[218:221], v[24:27]
	v_mfma_f32_16x16x32_bf16 v[16:19], v[162:165], v[226:229], v[16:19]
	v_mfma_f32_16x16x32_bf16 v[8:11], v[170:173], v[226:229], v[8:11]
	s_setprio 0
	s_setprio 1
	v_mfma_f32_16x16x32_bf16 v[60:63], v[174:177], v[190:193], v[60:63]
	v_mfma_f32_16x16x32_bf16 v[52:55], v[182:185], v[190:193], v[52:55]
	v_mfma_f32_16x16x32_bf16 v[44:47], v[174:177], v[198:201], v[44:47]
	v_mfma_f32_16x16x32_bf16 v[36:39], v[182:185], v[198:201], v[36:39]
	v_mfma_f32_16x16x32_bf16 v[28:31], v[174:177], v[206:209], v[28:31]
	v_mfma_f32_16x16x32_bf16 v[20:23], v[182:185], v[206:209], v[20:23]
	v_mfma_f32_16x16x32_bf16 v[12:15], v[174:177], v[222:225], v[12:15]
	v_mfma_f32_16x16x32_bf16 v[4:7], v[182:185], v[222:225], v[4:7]
	v_mfma_f32_16x16x32_bf16 v[60:63], v[178:181], v[194:197], v[60:63]
	v_mfma_f32_16x16x32_bf16 v[52:55], v[186:189], v[194:197], v[52:55]
	v_mfma_f32_16x16x32_bf16 v[44:47], v[178:181], v[202:205], v[44:47]
	v_mfma_f32_16x16x32_bf16 v[36:39], v[186:189], v[202:205], v[36:39]
	v_mfma_f32_16x16x32_bf16 v[28:31], v[178:181], v[218:221], v[28:31]
	v_mfma_f32_16x16x32_bf16 v[20:23], v[186:189], v[218:221], v[20:23]
	v_mfma_f32_16x16x32_bf16 v[12:15], v[178:181], v[226:229], v[12:15]
	v_mfma_f32_16x16x32_bf16 v[4:7], v[186:189], v[226:229], v[4:7]
	s_setprio 0
	s_barrier
	s_add_i32 s22, 0, 0x18000
	v_add_u32_e32 v2, s22, v147
	s_add_i32 s23, 0, 0x1c000
	ds_read_b128 v[158:161], v2
	ds_read_b128 v[162:165], v2 offset:1024
	ds_read_b128 v[166:169], v2 offset:2048
	ds_read_b128 v[170:173], v2 offset:3072
	v_add_u32_e32 v2, s23, v147
	ds_read_b128 v[174:177], v2
	ds_read_b128 v[178:181], v2 offset:1024
	ds_read_b128 v[182:185], v2 offset:2048
	ds_read_b128 v[186:189], v2 offset:3072
	s_mov_b32 m0, s51
	ds_read_b128 v[190:193], v153 offset:32768
	ds_read_b128 v[194:197], v153 offset:33792
	ds_read_b128 v[198:201], v153 offset:34816
	ds_read_b128 v[202:205], v153 offset:35840
	ds_read_b128 v[206:209], v153 offset:36864
	ds_read_b128 v[218:221], v153 offset:37888
	ds_read_b128 v[222:225], v153 offset:38912
	ds_read_b128 v[226:229], v153 offset:39936
	global_load_lds_dwordx4 v141, s[40:41]
	s_mov_b32 m0, s52
	s_nop 0
	global_load_lds_dwordx4 v145, s[40:41]
	s_waitcnt vmcnt(8)
	s_waitcnt lgkmcnt(0)
	s_barrier
	s_setprio 1
	s_waitcnt lgkmcnt(0)
	v_mfma_f32_16x16x32_bf16 v[124:127], v[158:161], v[190:193], v[124:127]
	v_mfma_f32_16x16x32_bf16 v[120:123], v[166:169], v[190:193], v[120:123]
	v_mfma_f32_16x16x32_bf16 v[112:115], v[158:161], v[198:201], v[112:115]
	v_mfma_f32_16x16x32_bf16 v[104:107], v[166:169], v[198:201], v[104:107]
	v_mfma_f32_16x16x32_bf16 v[96:99], v[158:161], v[206:209], v[96:99]
	v_mfma_f32_16x16x32_bf16 v[88:91], v[166:169], v[206:209], v[88:91]
	v_mfma_f32_16x16x32_bf16 v[80:83], v[158:161], v[222:225], v[80:83]
	v_mfma_f32_16x16x32_bf16 v[72:75], v[166:169], v[222:225], v[72:75]
	v_mfma_f32_16x16x32_bf16 v[124:127], v[162:165], v[194:197], v[124:127]
	v_mfma_f32_16x16x32_bf16 v[120:123], v[170:173], v[194:197], v[120:123]
	v_mfma_f32_16x16x32_bf16 v[112:115], v[162:165], v[202:205], v[112:115]
	v_mfma_f32_16x16x32_bf16 v[104:107], v[170:173], v[202:205], v[104:107]
	v_mfma_f32_16x16x32_bf16 v[96:99], v[162:165], v[218:221], v[96:99]
	v_mfma_f32_16x16x32_bf16 v[88:91], v[170:173], v[218:221], v[88:91]
	v_mfma_f32_16x16x32_bf16 v[80:83], v[162:165], v[226:229], v[80:83]
	v_mfma_f32_16x16x32_bf16 v[72:75], v[170:173], v[226:229], v[72:75]
	s_setprio 0
	s_setprio 1
	v_mfma_f32_16x16x32_bf16 v[128:131], v[174:177], v[190:193], v[128:131]
	v_mfma_f32_16x16x32_bf16 v[116:119], v[182:185], v[190:193], v[116:119]
	v_mfma_f32_16x16x32_bf16 v[108:111], v[174:177], v[198:201], v[108:111]
	v_mfma_f32_16x16x32_bf16 v[100:103], v[182:185], v[198:201], v[100:103]
	v_mfma_f32_16x16x32_bf16 v[92:95], v[174:177], v[206:209], v[92:95]
	v_mfma_f32_16x16x32_bf16 v[84:87], v[182:185], v[206:209], v[84:87]
	v_mfma_f32_16x16x32_bf16 v[76:79], v[174:177], v[222:225], v[76:79]
	v_mfma_f32_16x16x32_bf16 v[68:71], v[182:185], v[222:225], v[68:71]
	v_mfma_f32_16x16x32_bf16 v[128:131], v[178:181], v[194:197], v[128:131]
	v_mfma_f32_16x16x32_bf16 v[116:119], v[186:189], v[194:197], v[116:119]
	v_mfma_f32_16x16x32_bf16 v[108:111], v[178:181], v[202:205], v[108:111]
	v_mfma_f32_16x16x32_bf16 v[100:103], v[186:189], v[202:205], v[100:103]
	v_mfma_f32_16x16x32_bf16 v[92:95], v[178:181], v[218:221], v[92:95]
	v_mfma_f32_16x16x32_bf16 v[84:87], v[186:189], v[218:221], v[84:87]
	v_mfma_f32_16x16x32_bf16 v[76:79], v[178:181], v[226:229], v[76:79]
	v_mfma_f32_16x16x32_bf16 v[68:71], v[186:189], v[226:229], v[68:71]
	s_setprio 0
	s_barrier
	s_add_i32 s22, s22, s47
	v_lshl_add_u64 v[212:213], v[212:213], 0, s[24:25]
	s_mov_b32 m0, s22
	ds_read_b128 v[190:193], v153 offset:49152
	ds_read_b128 v[194:197], v153 offset:50176
	ds_read_b128 v[198:201], v153 offset:51200
	ds_read_b128 v[202:205], v153 offset:52224
	ds_read_b128 v[206:209], v153 offset:53248
	ds_read_b128 v[218:221], v153 offset:54272
	ds_read_b128 v[222:225], v153 offset:55296
	ds_read_b128 v[226:229], v153 offset:56320
	global_load_lds_dwordx4 v[212:213], off
	v_lshl_add_u64 v[212:213], v[214:215], 0, s[24:25]
	s_add_i32 m0, s22, 0x2000
	s_add_i32 s22, s23, s47
	global_load_lds_dwordx4 v[212:213], off
	v_lshl_add_u64 v[212:213], v[230:231], 0, s[24:25]
	s_mov_b32 m0, s22
	v_lshl_add_u64 v[210:211], v[210:211], 0, s[24:25]
	global_load_lds_dwordx4 v[212:213], off
	v_lshl_add_u64 v[212:213], v[240:241], 0, s[24:25]
	s_add_i32 m0, s22, 0x2000
	s_nop 0
	global_load_lds_dwordx4 v[212:213], off
	v_lshl_add_u64 v[212:213], v[242:243], 0, s[24:25]
	s_mov_b32 m0, s53
	s_nop 0
	global_load_lds_dwordx4 v[212:213], off
	s_mov_b32 m0, s54
	s_nop 0
	global_load_lds_dwordx4 v[210:211], off
	s_waitcnt vmcnt(8)
	s_waitcnt lgkmcnt(0)
	s_barrier
	s_setprio 1
	s_waitcnt lgkmcnt(0)
	v_mfma_f32_16x16x32_bf16 v[64:67], v[158:161], v[190:193], v[64:67]
	v_mfma_f32_16x16x32_bf16 v[56:59], v[166:169], v[190:193], v[56:59]
	v_mfma_f32_16x16x32_bf16 v[48:51], v[158:161], v[198:201], v[48:51]
	v_mfma_f32_16x16x32_bf16 v[40:43], v[166:169], v[198:201], v[40:43]
	v_mfma_f32_16x16x32_bf16 v[32:35], v[158:161], v[206:209], v[32:35]
	v_mfma_f32_16x16x32_bf16 v[24:27], v[166:169], v[206:209], v[24:27]
	v_mfma_f32_16x16x32_bf16 v[16:19], v[158:161], v[222:225], v[16:19]
	v_mfma_f32_16x16x32_bf16 v[8:11], v[166:169], v[222:225], v[8:11]
	v_mfma_f32_16x16x32_bf16 v[64:67], v[162:165], v[194:197], v[64:67]
	v_mfma_f32_16x16x32_bf16 v[56:59], v[170:173], v[194:197], v[56:59]
	v_mfma_f32_16x16x32_bf16 v[48:51], v[162:165], v[202:205], v[48:51]
	v_mfma_f32_16x16x32_bf16 v[40:43], v[170:173], v[202:205], v[40:43]
	v_mfma_f32_16x16x32_bf16 v[32:35], v[162:165], v[218:221], v[32:35]
	v_mfma_f32_16x16x32_bf16 v[24:27], v[170:173], v[218:221], v[24:27]
	v_mfma_f32_16x16x32_bf16 v[16:19], v[162:165], v[226:229], v[16:19]
	v_mfma_f32_16x16x32_bf16 v[8:11], v[170:173], v[226:229], v[8:11]
	s_setprio 0
	s_setprio 1
	v_mfma_f32_16x16x32_bf16 v[60:63], v[174:177], v[190:193], v[60:63]
	v_mfma_f32_16x16x32_bf16 v[52:55], v[182:185], v[190:193], v[52:55]
	v_mfma_f32_16x16x32_bf16 v[44:47], v[174:177], v[198:201], v[44:47]
	v_mfma_f32_16x16x32_bf16 v[36:39], v[182:185], v[198:201], v[36:39]
	v_mfma_f32_16x16x32_bf16 v[28:31], v[174:177], v[206:209], v[28:31]
	v_mfma_f32_16x16x32_bf16 v[20:23], v[182:185], v[206:209], v[20:23]
	v_mfma_f32_16x16x32_bf16 v[12:15], v[174:177], v[222:225], v[12:15]
	v_mfma_f32_16x16x32_bf16 v[4:7], v[182:185], v[222:225], v[4:7]
	v_mfma_f32_16x16x32_bf16 v[60:63], v[178:181], v[194:197], v[60:63]
	v_mfma_f32_16x16x32_bf16 v[52:55], v[186:189], v[194:197], v[52:55]
	v_mfma_f32_16x16x32_bf16 v[44:47], v[178:181], v[202:205], v[44:47]
	v_mfma_f32_16x16x32_bf16 v[36:39], v[186:189], v[202:205], v[36:39]
	v_mfma_f32_16x16x32_bf16 v[28:31], v[178:181], v[218:221], v[28:31]
	v_mfma_f32_16x16x32_bf16 v[20:23], v[186:189], v[218:221], v[20:23]
	v_mfma_f32_16x16x32_bf16 v[12:15], v[178:181], v[226:229], v[12:15]
	v_mfma_f32_16x16x32_bf16 v[4:7], v[186:189], v[226:229], v[4:7]
	s_setprio 0
	s_cmp_ge_i32 s21, s55
	s_mov_b64 s[26:27], s[30:31]
	s_cbranch_scc1 .Lmy_rot3
	s_cmp_eq_u32 s56, s21
	s_cselect_b64 vcc, -1, 0
	s_add_i32 s21, s21, 2
	s_add_u32 s30, s26, 0x100
	s_addc_u32 s31, s27, 0
	s_and_b64 s[22:23], vcc, exec
	s_cselect_b32 s23, 0, s30
	s_cselect_b32 s22, 0, s31
	s_add_u32 s40, s2, s23
	s_addc_u32 s41, s3, s22
	s_add_u32 s28, s19, s26
	s_addc_u32 s29, s20, s27
	s_add_i32 s65, 0, 0x10000
	s_and_b64 s[22:23], vcc, exec
	s_cselect_b32 s23, s43, s29
	s_cselect_b32 s22, s42, s28
	s_add_i32 s28, 0, 0x14000
	s_branch .LBB0_3267
.Lmy_rot3:
	s_barrier
.LBB0_3268:
	s_and_b64 vcc, exec, s[44:45]
	s_cbranch_vccz .LBB0_3271
	s_add_i32 s19, s57, 2
	v_readlane_b32 s20, v252, 52
	s_mul_i32 s19, s19, s20
	s_add_i32 s19, s19, s88
	s_cmpk_gt_i32 s19, 0x3ff
	s_mov_b64 s[44:45], 0
	v_readlane_b32 s21, v252, 53
	s_cbranch_scc1 .LBB0_3272
	s_ashr_i32 s21, s19, 5
	s_lshl_b32 s22, s19, 1
	s_and_b32 s20, s19, 7
	s_and_b32 s21, s21, -8
	s_and_b32 s22, s22, 2
	s_bfe_u32 s23, s19, 0x10004
	s_or_b32 s20, s21, s20
	s_or_b32 s22, s22, s23
	s_lshl_b32 s22, s22, 5
	s_and_b32 s23, s20, -2
	s_bfe_u32 s21, s19, 0x30005
	s_add_i32 s22, s22, s23
	s_bfe_u32 s19, s19, 0x10003
	s_or_b32 s60, s22, s19
	s_lshl_b32 s19, s20, 2
	s_and_b32 s19, s19, -8
	s_or_b32 s61, s19, s21
	s_mov_b64 s[44:45], -1
	s_branch .LBB0_3272

.LBB0_3497:
	s_andn2_b64 vcc, exec, s[10:11]
	s_cbranch_vccnz .LBB0_3500
	s_add_u32 s26, s26, 0x80
	s_addc_u32 s27, s27, 0
	s_add_u32 s19, s30, 0x100
	s_addc_u32 s20, s31, 0
	s_mov_b32 s21, 0
	s_add_i32 s22, s21, 2
	s_add_u32 s23, s26, 0x80
	s_addc_u32 s28, s27, 0
	s_add_i32 s55, 0, 0x10000
	s_cmp_eq_u32 s49, s21
	s_cselect_b32 s31, s15, s28
	s_cselect_b32 s30, s14, s23
	v_add_u32_e32 v2, s55, v145
	s_cselect_b32 s29, s17, s20
	s_cselect_b32 s28, s16, s19
	s_add_i32 s21, 0, 0x14000
	ds_read_b128 v[148:151], v2
	ds_read_b128 v[152:155], v2 offset:1024
	ds_read_b128 v[156:159], v2 offset:2048
	ds_read_b128 v[160:163], v2 offset:3072
	v_add_u32_e32 v2, s21, v145
	ds_read_b128 v[164:167], v2
	ds_read_b128 v[168:171], v2 offset:1024
	ds_read_b128 v[172:175], v2 offset:2048
	ds_read_b128 v[176:179], v2 offset:3072
	v_lshl_add_u64 v[212:213], s[26:27], 0, v[140:141]
	s_add_i32 m0, s42, 0xc000
	ds_read_b128 v[180:183], v147
	ds_read_b128 v[184:187], v147 offset:1024
	ds_read_b128 v[188:191], v147 offset:2048
	ds_read_b128 v[192:195], v147 offset:3072
	ds_read_b128 v[196:199], v147 offset:4096
	ds_read_b128 v[200:203], v147 offset:5120
	ds_read_b128 v[204:207], v147 offset:6144
	ds_read_b128 v[208:211], v147 offset:7168
	global_load_lds_dwordx4 v[212:213], off
	v_lshl_add_u64 v[212:213], s[26:27], 0, v[142:143]
	s_add_i32 m0, s42, 0xe000
	s_nop 0
	global_load_lds_dwordx4 v[212:213], off
	s_waitcnt vmcnt(8)
	s_waitcnt lgkmcnt(0)
	s_barrier
	s_setprio 1
	s_waitcnt lgkmcnt(0)
	v_mfma_f32_16x16x32_bf16 v[124:127], v[148:151], v[180:183], 0
	v_mfma_f32_16x16x32_bf16 v[128:131], v[156:159], v[180:183], 0
	v_mfma_f32_16x16x32_bf16 v[112:115], v[148:151], v[188:191], 0
	v_mfma_f32_16x16x32_bf16 v[108:111], v[156:159], v[188:191], 0
	v_mfma_f32_16x16x32_bf16 v[96:99], v[148:151], v[196:199], 0
	v_mfma_f32_16x16x32_bf16 v[92:95], v[156:159], v[196:199], 0
	v_mfma_f32_16x16x32_bf16 v[80:83], v[148:151], v[204:207], 0
	v_mfma_f32_16x16x32_bf16 v[76:79], v[156:159], v[204:207], 0
	v_mfma_f32_16x16x32_bf16 v[124:127], v[152:155], v[184:187], v[124:127]
	v_mfma_f32_16x16x32_bf16 v[128:131], v[160:163], v[184:187], v[128:131]
	v_mfma_f32_16x16x32_bf16 v[112:115], v[152:155], v[192:195], v[112:115]
	v_mfma_f32_16x16x32_bf16 v[108:111], v[160:163], v[192:195], v[108:111]
	v_mfma_f32_16x16x32_bf16 v[96:99], v[152:155], v[200:203], v[96:99]
	v_mfma_f32_16x16x32_bf16 v[92:95], v[160:163], v[200:203], v[92:95]
	v_mfma_f32_16x16x32_bf16 v[80:83], v[152:155], v[208:211], v[80:83]
	v_mfma_f32_16x16x32_bf16 v[76:79], v[160:163], v[208:211], v[76:79]
	s_setprio 0
	s_setprio 1
	v_mfma_f32_16x16x32_bf16 v[120:123], v[164:167], v[180:183], 0
	v_mfma_f32_16x16x32_bf16 v[116:119], v[172:175], v[180:183], 0
	v_mfma_f32_16x16x32_bf16 v[104:107], v[164:167], v[188:191], 0
	v_mfma_f32_16x16x32_bf16 v[100:103], v[172:175], v[188:191], 0
	v_mfma_f32_16x16x32_bf16 v[88:91], v[164:167], v[196:199], 0
	v_mfma_f32_16x16x32_bf16 v[84:87], v[172:175], v[196:199], 0
	v_mfma_f32_16x16x32_bf16 v[72:75], v[164:167], v[204:207], 0
	v_mfma_f32_16x16x32_bf16 v[68:71], v[172:175], v[204:207], 0
	v_mfma_f32_16x16x32_bf16 v[120:123], v[168:171], v[184:187], v[120:123]
	v_mfma_f32_16x16x32_bf16 v[116:119], v[176:179], v[184:187], v[116:119]
	v_mfma_f32_16x16x32_bf16 v[104:107], v[168:171], v[192:195], v[104:107]
	v_mfma_f32_16x16x32_bf16 v[100:103], v[176:179], v[192:195], v[100:103]
	v_mfma_f32_16x16x32_bf16 v[88:91], v[168:171], v[200:203], v[88:91]
	v_mfma_f32_16x16x32_bf16 v[84:87], v[176:179], v[200:203], v[84:87]
	v_mfma_f32_16x16x32_bf16 v[72:75], v[168:171], v[208:211], v[72:75]
	v_mfma_f32_16x16x32_bf16 v[68:71], v[176:179], v[208:211], v[68:71]
	s_setprio 0
	s_barrier
	s_add_i32 s23, s55, s41
	v_lshl_add_u64 v[212:213], s[28:29], 0, v[136:137]
	s_mov_b32 m0, s23
	ds_read_b128 v[180:183], v147 offset:16384
	ds_read_b128 v[184:187], v147 offset:17408
	ds_read_b128 v[188:191], v147 offset:18432
	ds_read_b128 v[192:195], v147 offset:19456
	ds_read_b128 v[196:199], v147 offset:20480
	ds_read_b128 v[200:203], v147 offset:21504
	ds_read_b128 v[204:207], v147 offset:22528
	ds_read_b128 v[208:211], v147 offset:23552
	global_load_lds_dwordx4 v[212:213], off
	s_add_i32 m0, s23, 0x2000
	v_lshl_add_u64 v[214:215], s[28:29], 0, v[132:133]
	s_add_u32 s28, s28, s2
	s_addc_u32 s29, s29, s3
	s_add_i32 s21, s21, s41
	global_load_lds_dwordx4 v[214:215], off
	v_lshl_add_u64 v[218:219], s[28:29], 0, v[136:137]
	s_mov_b32 m0, s21
	v_lshl_add_u64 v[220:221], s[28:29], 0, v[132:133]
	global_load_lds_dwordx4 v[218:219], off
	s_add_i32 m0, s21, 0x2000
	v_lshl_add_u64 v[222:223], s[30:31], 0, v[138:139]
	global_load_lds_dwordx4 v[220:221], off
	s_mov_b32 m0, s42
	v_lshl_add_u64 v[224:225], s[30:31], 0, v[134:135]
	global_load_lds_dwordx4 v[222:223], off
	s_mov_b32 m0, s43
	s_nop 0
	global_load_lds_dwordx4 v[224:225], off
	s_waitcnt vmcnt(8)
	s_waitcnt lgkmcnt(0)
	s_barrier
	s_setprio 1
	s_waitcnt lgkmcnt(0)
	v_mfma_f32_16x16x32_bf16 v[64:67], v[148:151], v[180:183], 0
	v_mfma_f32_16x16x32_bf16 v[60:63], v[156:159], v[180:183], 0
	v_mfma_f32_16x16x32_bf16 v[48:51], v[148:151], v[188:191], 0
	v_mfma_f32_16x16x32_bf16 v[44:47], v[156:159], v[188:191], 0
	v_mfma_f32_16x16x32_bf16 v[32:35], v[148:151], v[196:199], 0
	v_mfma_f32_16x16x32_bf16 v[28:31], v[156:159], v[196:199], 0
	v_mfma_f32_16x16x32_bf16 v[16:19], v[148:151], v[204:207], 0
	v_mfma_f32_16x16x32_bf16 v[12:15], v[156:159], v[204:207], 0
	v_mfma_f32_16x16x32_bf16 v[64:67], v[152:155], v[184:187], v[64:67]
	v_mfma_f32_16x16x32_bf16 v[60:63], v[160:163], v[184:187], v[60:63]
	v_mfma_f32_16x16x32_bf16 v[48:51], v[152:155], v[192:195], v[48:51]
	v_mfma_f32_16x16x32_bf16 v[44:47], v[160:163], v[192:195], v[44:47]
	v_mfma_f32_16x16x32_bf16 v[32:35], v[152:155], v[200:203], v[32:35]
	v_mfma_f32_16x16x32_bf16 v[28:31], v[160:163], v[200:203], v[28:31]
	v_mfma_f32_16x16x32_bf16 v[16:19], v[152:155], v[208:211], v[16:19]
	v_mfma_f32_16x16x32_bf16 v[12:15], v[160:163], v[208:211], v[12:15]
	s_setprio 0
	s_setprio 1
	v_mfma_f32_16x16x32_bf16 v[56:59], v[164:167], v[180:183], 0
	v_mfma_f32_16x16x32_bf16 v[52:55], v[172:175], v[180:183], 0
	v_mfma_f32_16x16x32_bf16 v[40:43], v[164:167], v[188:191], 0
	v_mfma_f32_16x16x32_bf16 v[36:39], v[172:175], v[188:191], 0
	v_mfma_f32_16x16x32_bf16 v[24:27], v[164:167], v[196:199], 0
	v_mfma_f32_16x16x32_bf16 v[20:23], v[172:175], v[196:199], 0
	v_mfma_f32_16x16x32_bf16 v[8:11], v[164:167], v[204:207], 0
	v_mfma_f32_16x16x32_bf16 v[4:7], v[172:175], v[204:207], 0
	v_mfma_f32_16x16x32_bf16 v[56:59], v[168:171], v[184:187], v[56:59]
	v_mfma_f32_16x16x32_bf16 v[52:55], v[176:179], v[184:187], v[52:55]
	v_mfma_f32_16x16x32_bf16 v[40:43], v[168:171], v[192:195], v[40:43]
	v_mfma_f32_16x16x32_bf16 v[36:39], v[176:179], v[192:195], v[36:39]
	v_mfma_f32_16x16x32_bf16 v[24:27], v[168:171], v[200:203], v[24:27]
	v_mfma_f32_16x16x32_bf16 v[20:23], v[176:179], v[200:203], v[20:23]
	v_mfma_f32_16x16x32_bf16 v[8:11], v[168:171], v[208:211], v[8:11]
	v_mfma_f32_16x16x32_bf16 v[4:7], v[176:179], v[208:211], v[4:7]
	s_setprio 0
	s_barrier
	s_add_i32 s21, 0, 0x18000
	v_add_u32_e32 v2, s21, v145
	s_add_i32 s23, 0, 0x1c000
	ds_read_b128 v[148:151], v2
	ds_read_b128 v[152:155], v2 offset:1024
	ds_read_b128 v[156:159], v2 offset:2048
	ds_read_b128 v[160:163], v2 offset:3072
	v_add_u32_e32 v2, s23, v145
	ds_read_b128 v[164:167], v2
	ds_read_b128 v[168:171], v2 offset:1024
	ds_read_b128 v[172:175], v2 offset:2048
	ds_read_b128 v[176:179], v2 offset:3072
	s_add_u32 s28, s30, s2
	s_addc_u32 s29, s31, s3
	s_mov_b32 m0, s44
	v_lshl_add_u64 v[226:227], s[28:29], 0, v[138:139]
	ds_read_b128 v[180:183], v147 offset:32768
	ds_read_b128 v[184:187], v147 offset:33792
	ds_read_b128 v[188:191], v147 offset:34816
	ds_read_b128 v[192:195], v147 offset:35840
	ds_read_b128 v[196:199], v147 offset:36864
	ds_read_b128 v[200:203], v147 offset:37888
	ds_read_b128 v[204:207], v147 offset:38912
	ds_read_b128 v[208:211], v147 offset:39936
	global_load_lds_dwordx4 v[226:227], off
	v_lshl_add_u64 v[226:227], s[28:29], 0, v[134:135]
	s_mov_b32 m0, s45
	s_nop 0
	global_load_lds_dwordx4 v[226:227], off
	s_waitcnt vmcnt(8)
	s_waitcnt lgkmcnt(0)
	s_barrier
	s_setprio 1
	s_waitcnt lgkmcnt(0)
	v_mfma_f32_16x16x32_bf16 v[124:127], v[148:151], v[180:183], v[124:127]
	v_mfma_f32_16x16x32_bf16 v[128:131], v[156:159], v[180:183], v[128:131]
	v_mfma_f32_16x16x32_bf16 v[112:115], v[148:151], v[188:191], v[112:115]
	v_mfma_f32_16x16x32_bf16 v[108:111], v[156:159], v[188:191], v[108:111]
	v_mfma_f32_16x16x32_bf16 v[96:99], v[148:151], v[196:199], v[96:99]
	v_mfma_f32_16x16x32_bf16 v[92:95], v[156:159], v[196:199], v[92:95]
	v_mfma_f32_16x16x32_bf16 v[80:83], v[148:151], v[204:207], v[80:83]
	v_mfma_f32_16x16x32_bf16 v[76:79], v[156:159], v[204:207], v[76:79]
	v_mfma_f32_16x16x32_bf16 v[124:127], v[152:155], v[184:187], v[124:127]
	v_mfma_f32_16x16x32_bf16 v[128:131], v[160:163], v[184:187], v[128:131]
	v_mfma_f32_16x16x32_bf16 v[112:115], v[152:155], v[192:195], v[112:115]
	v_mfma_f32_16x16x32_bf16 v[108:111], v[160:163], v[192:195], v[108:111]
	v_mfma_f32_16x16x32_bf16 v[96:99], v[152:155], v[200:203], v[96:99]
	v_mfma_f32_16x16x32_bf16 v[92:95], v[160:163], v[200:203], v[92:95]
	v_mfma_f32_16x16x32_bf16 v[80:83], v[152:155], v[208:211], v[80:83]
	v_mfma_f32_16x16x32_bf16 v[76:79], v[160:163], v[208:211], v[76:79]
	s_setprio 0
	s_setprio 1
	v_mfma_f32_16x16x32_bf16 v[120:123], v[164:167], v[180:183], v[120:123]
	v_mfma_f32_16x16x32_bf16 v[116:119], v[172:175], v[180:183], v[116:119]
	v_mfma_f32_16x16x32_bf16 v[104:107], v[164:167], v[188:191], v[104:107]
	v_mfma_f32_16x16x32_bf16 v[100:103], v[172:175], v[188:191], v[100:103]
	v_mfma_f32_16x16x32_bf16 v[88:91], v[164:167], v[196:199], v[88:91]
	v_mfma_f32_16x16x32_bf16 v[84:87], v[172:175], v[196:199], v[84:87]
	v_mfma_f32_16x16x32_bf16 v[72:75], v[164:167], v[204:207], v[72:75]
	v_mfma_f32_16x16x32_bf16 v[68:71], v[172:175], v[204:207], v[68:71]
	v_mfma_f32_16x16x32_bf16 v[120:123], v[168:171], v[184:187], v[120:123]
	v_mfma_f32_16x16x32_bf16 v[116:119], v[176:179], v[184:187], v[116:119]
	v_mfma_f32_16x16x32_bf16 v[104:107], v[168:171], v[192:195], v[104:107]
	v_mfma_f32_16x16x32_bf16 v[100:103], v[176:179], v[192:195], v[100:103]
	v_mfma_f32_16x16x32_bf16 v[88:91], v[168:171], v[200:203], v[88:91]
	v_mfma_f32_16x16x32_bf16 v[84:87], v[176:179], v[200:203], v[84:87]
	v_mfma_f32_16x16x32_bf16 v[72:75], v[168:171], v[208:211], v[72:75]
	v_mfma_f32_16x16x32_bf16 v[68:71], v[176:179], v[208:211], v[68:71]
	s_setprio 0
	s_barrier
	s_add_i32 s21, s21, s41
	v_lshl_add_u64 v[212:213], v[212:213], 0, s[24:25]
	s_mov_b32 m0, s21
	ds_read_b128 v[180:183], v147 offset:49152
	ds_read_b128 v[184:187], v147 offset:50176
	ds_read_b128 v[188:191], v147 offset:51200
	ds_read_b128 v[192:195], v147 offset:52224
	ds_read_b128 v[196:199], v147 offset:53248
	ds_read_b128 v[200:203], v147 offset:54272
	ds_read_b128 v[204:207], v147 offset:55296
	ds_read_b128 v[208:211], v147 offset:56320
	global_load_lds_dwordx4 v[212:213], off
	v_lshl_add_u64 v[212:213], v[214:215], 0, s[24:25]
	s_add_i32 m0, s21, 0x2000
	s_add_i32 s21, s23, s41
	global_load_lds_dwordx4 v[212:213], off
	v_lshl_add_u64 v[212:213], v[218:219], 0, s[24:25]
	s_mov_b32 m0, s21
	s_nop 0
	global_load_lds_dwordx4 v[212:213], off
	v_lshl_add_u64 v[212:213], v[220:221], 0, s[24:25]
	s_add_i32 m0, s21, 0x2000
	s_nop 0
	global_load_lds_dwordx4 v[212:213], off
	v_lshl_add_u64 v[212:213], v[222:223], 0, s[24:25]
	s_mov_b32 m0, s47
	s_nop 0
	global_load_lds_dwordx4 v[212:213], off
	v_lshl_add_u64 v[212:213], v[224:225], 0, s[24:25]
	s_mov_b32 m0, s48
	s_nop 0
	global_load_lds_dwordx4 v[212:213], off
	s_waitcnt vmcnt(8)
	s_waitcnt lgkmcnt(0)
	s_barrier
	s_setprio 1
	s_waitcnt lgkmcnt(0)
	v_mfma_f32_16x16x32_bf16 v[64:67], v[148:151], v[180:183], v[64:67]
	v_mfma_f32_16x16x32_bf16 v[60:63], v[156:159], v[180:183], v[60:63]
	v_mfma_f32_16x16x32_bf16 v[48:51], v[148:151], v[188:191], v[48:51]
	v_mfma_f32_16x16x32_bf16 v[44:47], v[156:159], v[188:191], v[44:47]
	v_mfma_f32_16x16x32_bf16 v[32:35], v[148:151], v[196:199], v[32:35]
	v_mfma_f32_16x16x32_bf16 v[28:31], v[156:159], v[196:199], v[28:31]
	v_mfma_f32_16x16x32_bf16 v[16:19], v[148:151], v[204:207], v[16:19]
	v_mfma_f32_16x16x32_bf16 v[12:15], v[156:159], v[204:207], v[12:15]
	v_mfma_f32_16x16x32_bf16 v[64:67], v[152:155], v[184:187], v[64:67]
	v_mfma_f32_16x16x32_bf16 v[60:63], v[160:163], v[184:187], v[60:63]
	v_mfma_f32_16x16x32_bf16 v[48:51], v[152:155], v[192:195], v[48:51]
	v_mfma_f32_16x16x32_bf16 v[44:47], v[160:163], v[192:195], v[44:47]
	v_mfma_f32_16x16x32_bf16 v[32:35], v[152:155], v[200:203], v[32:35]
	v_mfma_f32_16x16x32_bf16 v[28:31], v[160:163], v[200:203], v[28:31]
	v_mfma_f32_16x16x32_bf16 v[16:19], v[152:155], v[208:211], v[16:19]
	v_mfma_f32_16x16x32_bf16 v[12:15], v[160:163], v[208:211], v[12:15]
	s_setprio 0
	s_setprio 1
	v_mfma_f32_16x16x32_bf16 v[56:59], v[164:167], v[180:183], v[56:59]
	v_mfma_f32_16x16x32_bf16 v[52:55], v[172:175], v[180:183], v[52:55]
	v_mfma_f32_16x16x32_bf16 v[40:43], v[164:167], v[188:191], v[40:43]
	v_mfma_f32_16x16x32_bf16 v[36:39], v[172:175], v[188:191], v[36:39]
	v_mfma_f32_16x16x32_bf16 v[24:27], v[164:167], v[196:199], v[24:27]
	v_mfma_f32_16x16x32_bf16 v[20:23], v[172:175], v[196:199], v[20:23]
	v_mfma_f32_16x16x32_bf16 v[8:11], v[164:167], v[204:207], v[8:11]
	v_mfma_f32_16x16x32_bf16 v[4:7], v[172:175], v[204:207], v[4:7]
	v_mfma_f32_16x16x32_bf16 v[56:59], v[168:171], v[184:187], v[56:59]
	v_mfma_f32_16x16x32_bf16 v[52:55], v[176:179], v[184:187], v[52:55]
	v_mfma_f32_16x16x32_bf16 v[40:43], v[168:171], v[192:195], v[40:43]
	v_mfma_f32_16x16x32_bf16 v[36:39], v[176:179], v[192:195], v[36:39]
	v_mfma_f32_16x16x32_bf16 v[24:27], v[168:171], v[200:203], v[24:27]
	v_mfma_f32_16x16x32_bf16 v[20:23], v[176:179], v[200:203], v[20:23]
	v_mfma_f32_16x16x32_bf16 v[8:11], v[168:171], v[208:211], v[8:11]
	v_mfma_f32_16x16x32_bf16 v[4:7], v[176:179], v[208:211], v[4:7]
	s_setprio 0
	s_add_u32 s26, s26, 0x100
	s_addc_u32 s27, s27, 0
	s_add_u32 s19, s19, 0x100
	s_addc_u32 s20, s20, 0
	s_cmp_ge_i32 s22, s46
	s_mov_b32 s21, s22
	s_cbranch_scc1 .Lmy_rot4
	s_add_i32 s22, s21, 2
	s_add_u32 s23, s26, 0x80
	s_addc_u32 s28, s27, 0
	s_add_i32 s55, 0, 0x10000
	s_cmp_eq_u32 s49, s21
	s_cselect_b32 s31, s15, s28
	s_cselect_b32 s30, s14, s23
	s_cselect_b32 s29, s17, s20
	s_cselect_b32 s28, s16, s19
	s_add_i32 s21, 0, 0x14000
.LBB0_3499:
	s_barrier
	v_add_u32_e32 v2, s55, v145
	ds_read_b128 v[148:151], v2
	ds_read_b128 v[152:155], v2 offset:1024
	ds_read_b128 v[156:159], v2 offset:2048
	ds_read_b128 v[160:163], v2 offset:3072
	v_add_u32_e32 v2, s21, v145
	ds_read_b128 v[164:167], v2
	ds_read_b128 v[168:171], v2 offset:1024
	ds_read_b128 v[172:175], v2 offset:2048
	ds_read_b128 v[176:179], v2 offset:3072
	v_lshl_add_u64 v[212:213], s[26:27], 0, v[140:141]
	s_add_i32 m0, s42, 0xc000
	ds_read_b128 v[180:183], v147
	ds_read_b128 v[184:187], v147 offset:1024
	ds_read_b128 v[188:191], v147 offset:2048
	ds_read_b128 v[192:195], v147 offset:3072
	ds_read_b128 v[196:199], v147 offset:4096
	ds_read_b128 v[200:203], v147 offset:5120
	ds_read_b128 v[204:207], v147 offset:6144
	ds_read_b128 v[208:211], v147 offset:7168
	global_load_lds_dwordx4 v[212:213], off
	v_lshl_add_u64 v[212:213], s[26:27], 0, v[142:143]
	s_add_i32 m0, s42, 0xe000
	s_nop 0
	global_load_lds_dwordx4 v[212:213], off
	s_waitcnt vmcnt(8)
	s_waitcnt lgkmcnt(0)
	s_barrier
	s_setprio 1
	s_waitcnt lgkmcnt(0)
	v_mfma_f32_16x16x32_bf16 v[124:127], v[148:151], v[180:183], v[124:127]
	v_mfma_f32_16x16x32_bf16 v[128:131], v[156:159], v[180:183], v[128:131]
	v_mfma_f32_16x16x32_bf16 v[112:115], v[148:151], v[188:191], v[112:115]
	v_mfma_f32_16x16x32_bf16 v[108:111], v[156:159], v[188:191], v[108:111]
	v_mfma_f32_16x16x32_bf16 v[96:99], v[148:151], v[196:199], v[96:99]
	v_mfma_f32_16x16x32_bf16 v[92:95], v[156:159], v[196:199], v[92:95]
	v_mfma_f32_16x16x32_bf16 v[80:83], v[148:151], v[204:207], v[80:83]
	v_mfma_f32_16x16x32_bf16 v[76:79], v[156:159], v[204:207], v[76:79]
	v_mfma_f32_16x16x32_bf16 v[124:127], v[152:155], v[184:187], v[124:127]
	v_mfma_f32_16x16x32_bf16 v[128:131], v[160:163], v[184:187], v[128:131]
	v_mfma_f32_16x16x32_bf16 v[112:115], v[152:155], v[192:195], v[112:115]
	v_mfma_f32_16x16x32_bf16 v[108:111], v[160:163], v[192:195], v[108:111]
	v_mfma_f32_16x16x32_bf16 v[96:99], v[152:155], v[200:203], v[96:99]
	v_mfma_f32_16x16x32_bf16 v[92:95], v[160:163], v[200:203], v[92:95]
	v_mfma_f32_16x16x32_bf16 v[80:83], v[152:155], v[208:211], v[80:83]
	v_mfma_f32_16x16x32_bf16 v[76:79], v[160:163], v[208:211], v[76:79]
	s_setprio 0
	s_setprio 1
	v_mfma_f32_16x16x32_bf16 v[120:123], v[164:167], v[180:183], v[120:123]
	v_mfma_f32_16x16x32_bf16 v[116:119], v[172:175], v[180:183], v[116:119]
	v_mfma_f32_16x16x32_bf16 v[104:107], v[164:167], v[188:191], v[104:107]
	v_mfma_f32_16x16x32_bf16 v[100:103], v[172:175], v[188:191], v[100:103]
	v_mfma_f32_16x16x32_bf16 v[88:91], v[164:167], v[196:199], v[88:91]
	v_mfma_f32_16x16x32_bf16 v[84:87], v[172:175], v[196:199], v[84:87]
	v_mfma_f32_16x16x32_bf16 v[72:75], v[164:167], v[204:207], v[72:75]
	v_mfma_f32_16x16x32_bf16 v[68:71], v[172:175], v[204:207], v[68:71]
	v_mfma_f32_16x16x32_bf16 v[120:123], v[168:171], v[184:187], v[120:123]
	v_mfma_f32_16x16x32_bf16 v[116:119], v[176:179], v[184:187], v[116:119]
	v_mfma_f32_16x16x32_bf16 v[104:107], v[168:171], v[192:195], v[104:107]
	v_mfma_f32_16x16x32_bf16 v[100:103], v[176:179], v[192:195], v[100:103]
	v_mfma_f32_16x16x32_bf16 v[88:91], v[168:171], v[200:203], v[88:91]
	v_mfma_f32_16x16x32_bf16 v[84:87], v[176:179], v[200:203], v[84:87]
	v_mfma_f32_16x16x32_bf16 v[72:75], v[168:171], v[208:211], v[72:75]
	v_mfma_f32_16x16x32_bf16 v[68:71], v[176:179], v[208:211], v[68:71]
	s_setprio 0
	s_barrier
	s_add_i32 s23, s55, s41
	v_lshl_add_u64 v[212:213], s[28:29], 0, v[136:137]
	s_mov_b32 m0, s23
	ds_read_b128 v[180:183], v147 offset:16384
	ds_read_b128 v[184:187], v147 offset:17408
	ds_read_b128 v[188:191], v147 offset:18432
	ds_read_b128 v[192:195], v147 offset:19456
	ds_read_b128 v[196:199], v147 offset:20480
	ds_read_b128 v[200:203], v147 offset:21504
	ds_read_b128 v[204:207], v147 offset:22528
	ds_read_b128 v[208:211], v147 offset:23552
	global_load_lds_dwordx4 v[212:213], off
	s_add_i32 m0, s23, 0x2000
	v_lshl_add_u64 v[214:215], s[28:29], 0, v[132:133]
	s_add_u32 s28, s28, s2
	s_addc_u32 s29, s29, s3
	s_add_i32 s21, s21, s41
	global_load_lds_dwordx4 v[214:215], off
	v_lshl_add_u64 v[218:219], s[28:29], 0, v[136:137]
	s_mov_b32 m0, s21
	v_lshl_add_u64 v[220:221], s[28:29], 0, v[132:133]
	global_load_lds_dwordx4 v[218:219], off
	s_add_i32 m0, s21, 0x2000
	v_lshl_add_u64 v[222:223], s[30:31], 0, v[138:139]
	global_load_lds_dwordx4 v[220:221], off
	s_mov_b32 m0, s42
	v_lshl_add_u64 v[224:225], s[30:31], 0, v[134:135]
	global_load_lds_dwordx4 v[222:223], off
	s_mov_b32 m0, s43
	s_nop 0
	global_load_lds_dwordx4 v[224:225], off
	s_waitcnt vmcnt(8)
	s_waitcnt lgkmcnt(0)
	s_barrier
	s_setprio 1
	s_waitcnt lgkmcnt(0)
	v_mfma_f32_16x16x32_bf16 v[64:67], v[148:151], v[180:183], v[64:67]
	v_mfma_f32_16x16x32_bf16 v[60:63], v[156:159], v[180:183], v[60:63]
	v_mfma_f32_16x16x32_bf16 v[48:51], v[148:151], v[188:191], v[48:51]
	v_mfma_f32_16x16x32_bf16 v[44:47], v[156:159], v[188:191], v[44:47]
	v_mfma_f32_16x16x32_bf16 v[32:35], v[148:151], v[196:199], v[32:35]
	v_mfma_f32_16x16x32_bf16 v[28:31], v[156:159], v[196:199], v[28:31]
	v_mfma_f32_16x16x32_bf16 v[16:19], v[148:151], v[204:207], v[16:19]
	v_mfma_f32_16x16x32_bf16 v[12:15], v[156:159], v[204:207], v[12:15]
	v_mfma_f32_16x16x32_bf16 v[64:67], v[152:155], v[184:187], v[64:67]
	v_mfma_f32_16x16x32_bf16 v[60:63], v[160:163], v[184:187], v[60:63]
	v_mfma_f32_16x16x32_bf16 v[48:51], v[152:155], v[192:195], v[48:51]
	v_mfma_f32_16x16x32_bf16 v[44:47], v[160:163], v[192:195], v[44:47]
	v_mfma_f32_16x16x32_bf16 v[32:35], v[152:155], v[200:203], v[32:35]
	v_mfma_f32_16x16x32_bf16 v[28:31], v[160:163], v[200:203], v[28:31]
	v_mfma_f32_16x16x32_bf16 v[16:19], v[152:155], v[208:211], v[16:19]
	v_mfma_f32_16x16x32_bf16 v[12:15], v[160:163], v[208:211], v[12:15]
	s_setprio 0
	s_setprio 1
	v_mfma_f32_16x16x32_bf16 v[56:59], v[164:167], v[180:183], v[56:59]
	v_mfma_f32_16x16x32_bf16 v[52:55], v[172:175], v[180:183], v[52:55]
	v_mfma_f32_16x16x32_bf16 v[40:43], v[164:167], v[188:191], v[40:43]
	v_mfma_f32_16x16x32_bf16 v[36:39], v[172:175], v[188:191], v[36:39]
	v_mfma_f32_16x16x32_bf16 v[24:27], v[164:167], v[196:199], v[24:27]
	v_mfma_f32_16x16x32_bf16 v[20:23], v[172:175], v[196:199], v[20:23]
	v_mfma_f32_16x16x32_bf16 v[8:11], v[164:167], v[204:207], v[8:11]
	v_mfma_f32_16x16x32_bf16 v[4:7], v[172:175], v[204:207], v[4:7]
	v_mfma_f32_16x16x32_bf16 v[56:59], v[168:171], v[184:187], v[56:59]
	v_mfma_f32_16x16x32_bf16 v[52:55], v[176:179], v[184:187], v[52:55]
	v_mfma_f32_16x16x32_bf16 v[40:43], v[168:171], v[192:195], v[40:43]
	v_mfma_f32_16x16x32_bf16 v[36:39], v[176:179], v[192:195], v[36:39]
	v_mfma_f32_16x16x32_bf16 v[24:27], v[168:171], v[200:203], v[24:27]
	v_mfma_f32_16x16x32_bf16 v[20:23], v[176:179], v[200:203], v[20:23]
	v_mfma_f32_16x16x32_bf16 v[8:11], v[168:171], v[208:211], v[8:11]
	v_mfma_f32_16x16x32_bf16 v[4:7], v[176:179], v[208:211], v[4:7]
	s_setprio 0
	s_barrier
	s_add_i32 s21, 0, 0x18000
	v_add_u32_e32 v2, s21, v145
	s_add_i32 s23, 0, 0x1c000
	ds_read_b128 v[148:151], v2
	ds_read_b128 v[152:155], v2 offset:1024
	ds_read_b128 v[156:159], v2 offset:2048
	ds_read_b128 v[160:163], v2 offset:3072
	v_add_u32_e32 v2, s23, v145
	ds_read_b128 v[164:167], v2
	ds_read_b128 v[168:171], v2 offset:1024
	ds_read_b128 v[172:175], v2 offset:2048
	ds_read_b128 v[176:179], v2 offset:3072
	s_add_u32 s28, s30, s2
	s_addc_u32 s29, s31, s3
	s_mov_b32 m0, s44
	v_lshl_add_u64 v[226:227], s[28:29], 0, v[138:139]
	ds_read_b128 v[180:183], v147 offset:32768
	ds_read_b128 v[184:187], v147 offset:33792
	ds_read_b128 v[188:191], v147 offset:34816
	ds_read_b128 v[192:195], v147 offset:35840
	ds_read_b128 v[196:199], v147 offset:36864
	ds_read_b128 v[200:203], v147 offset:37888
	ds_read_b128 v[204:207], v147 offset:38912
	ds_read_b128 v[208:211], v147 offset:39936
	global_load_lds_dwordx4 v[226:227], off
	v_lshl_add_u64 v[226:227], s[28:29], 0, v[134:135]
	s_mov_b32 m0, s45
	s_nop 0
	global_load_lds_dwordx4 v[226:227], off
	s_waitcnt vmcnt(8)
	s_waitcnt lgkmcnt(0)
	s_barrier
	s_setprio 1
	s_waitcnt lgkmcnt(0)
	v_mfma_f32_16x16x32_bf16 v[124:127], v[148:151], v[180:183], v[124:127]
	v_mfma_f32_16x16x32_bf16 v[128:131], v[156:159], v[180:183], v[128:131]
	v_mfma_f32_16x16x32_bf16 v[112:115], v[148:151], v[188:191], v[112:115]
	v_mfma_f32_16x16x32_bf16 v[108:111], v[156:159], v[188:191], v[108:111]
	v_mfma_f32_16x16x32_bf16 v[96:99], v[148:151], v[196:199], v[96:99]
	v_mfma_f32_16x16x32_bf16 v[92:95], v[156:159], v[196:199], v[92:95]
	v_mfma_f32_16x16x32_bf16 v[80:83], v[148:151], v[204:207], v[80:83]
	v_mfma_f32_16x16x32_bf16 v[76:79], v[156:159], v[204:207], v[76:79]
	v_mfma_f32_16x16x32_bf16 v[124:127], v[152:155], v[184:187], v[124:127]
	v_mfma_f32_16x16x32_bf16 v[128:131], v[160:163], v[184:187], v[128:131]
	v_mfma_f32_16x16x32_bf16 v[112:115], v[152:155], v[192:195], v[112:115]
	v_mfma_f32_16x16x32_bf16 v[108:111], v[160:163], v[192:195], v[108:111]
	v_mfma_f32_16x16x32_bf16 v[96:99], v[152:155], v[200:203], v[96:99]
	v_mfma_f32_16x16x32_bf16 v[92:95], v[160:163], v[200:203], v[92:95]
	v_mfma_f32_16x16x32_bf16 v[80:83], v[152:155], v[208:211], v[80:83]
	v_mfma_f32_16x16x32_bf16 v[76:79], v[160:163], v[208:211], v[76:79]
	s_setprio 0
	s_setprio 1
	v_mfma_f32_16x16x32_bf16 v[120:123], v[164:167], v[180:183], v[120:123]
	v_mfma_f32_16x16x32_bf16 v[116:119], v[172:175], v[180:183], v[116:119]
	v_mfma_f32_16x16x32_bf16 v[104:107], v[164:167], v[188:191], v[104:107]
	v_mfma_f32_16x16x32_bf16 v[100:103], v[172:175], v[188:191], v[100:103]
	v_mfma_f32_16x16x32_bf16 v[88:91], v[164:167], v[196:199], v[88:91]
	v_mfma_f32_16x16x32_bf16 v[84:87], v[172:175], v[196:199], v[84:87]
	v_mfma_f32_16x16x32_bf16 v[72:75], v[164:167], v[204:207], v[72:75]
	v_mfma_f32_16x16x32_bf16 v[68:71], v[172:175], v[204:207], v[68:71]
	v_mfma_f32_16x16x32_bf16 v[120:123], v[168:171], v[184:187], v[120:123]
	v_mfma_f32_16x16x32_bf16 v[116:119], v[176:179], v[184:187], v[116:119]
	v_mfma_f32_16x16x32_bf16 v[104:107], v[168:171], v[192:195], v[104:107]
	v_mfma_f32_16x16x32_bf16 v[100:103], v[176:179], v[192:195], v[100:103]
	v_mfma_f32_16x16x32_bf16 v[88:91], v[168:171], v[200:203], v[88:91]
	v_mfma_f32_16x16x32_bf16 v[84:87], v[176:179], v[200:203], v[84:87]
	v_mfma_f32_16x16x32_bf16 v[72:75], v[168:171], v[208:211], v[72:75]
	v_mfma_f32_16x16x32_bf16 v[68:71], v[176:179], v[208:211], v[68:71]
	s_setprio 0
	s_barrier
	s_add_i32 s21, s21, s41
	v_lshl_add_u64 v[212:213], v[212:213], 0, s[24:25]
	s_mov_b32 m0, s21
	ds_read_b128 v[180:183], v147 offset:49152
	ds_read_b128 v[184:187], v147 offset:50176
	ds_read_b128 v[188:191], v147 offset:51200
	ds_read_b128 v[192:195], v147 offset:52224
	ds_read_b128 v[196:199], v147 offset:53248
	ds_read_b128 v[200:203], v147 offset:54272
	ds_read_b128 v[204:207], v147 offset:55296
	ds_read_b128 v[208:211], v147 offset:56320
	global_load_lds_dwordx4 v[212:213], off
	v_lshl_add_u64 v[212:213], v[214:215], 0, s[24:25]
	s_add_i32 m0, s21, 0x2000
	s_add_i32 s21, s23, s41
	global_load_lds_dwordx4 v[212:213], off
	v_lshl_add_u64 v[212:213], v[218:219], 0, s[24:25]
	s_mov_b32 m0, s21
	s_nop 0
	global_load_lds_dwordx4 v[212:213], off
	v_lshl_add_u64 v[212:213], v[220:221], 0, s[24:25]
	s_add_i32 m0, s21, 0x2000
	s_nop 0
	global_load_lds_dwordx4 v[212:213], off
	v_lshl_add_u64 v[212:213], v[222:223], 0, s[24:25]
	s_mov_b32 m0, s47
	s_nop 0
	global_load_lds_dwordx4 v[212:213], off
	v_lshl_add_u64 v[212:213], v[224:225], 0, s[24:25]
	s_mov_b32 m0, s48
	s_nop 0
	global_load_lds_dwordx4 v[212:213], off
	s_waitcnt vmcnt(8)
	s_waitcnt lgkmcnt(0)
	s_barrier
	s_setprio 1
	s_waitcnt lgkmcnt(0)
	v_mfma_f32_16x16x32_bf16 v[64:67], v[148:151], v[180:183], v[64:67]
	v_mfma_f32_16x16x32_bf16 v[60:63], v[156:159], v[180:183], v[60:63]
	v_mfma_f32_16x16x32_bf16 v[48:51], v[148:151], v[188:191], v[48:51]
	v_mfma_f32_16x16x32_bf16 v[44:47], v[156:159], v[188:191], v[44:47]
	v_mfma_f32_16x16x32_bf16 v[32:35], v[148:151], v[196:199], v[32:35]
	v_mfma_f32_16x16x32_bf16 v[28:31], v[156:159], v[196:199], v[28:31]
	v_mfma_f32_16x16x32_bf16 v[16:19], v[148:151], v[204:207], v[16:19]
	v_mfma_f32_16x16x32_bf16 v[12:15], v[156:159], v[204:207], v[12:15]
	v_mfma_f32_16x16x32_bf16 v[64:67], v[152:155], v[184:187], v[64:67]
	v_mfma_f32_16x16x32_bf16 v[60:63], v[160:163], v[184:187], v[60:63]
	v_mfma_f32_16x16x32_bf16 v[48:51], v[152:155], v[192:195], v[48:51]
	v_mfma_f32_16x16x32_bf16 v[44:47], v[160:163], v[192:195], v[44:47]
	v_mfma_f32_16x16x32_bf16 v[32:35], v[152:155], v[200:203], v[32:35]
	v_mfma_f32_16x16x32_bf16 v[28:31], v[160:163], v[200:203], v[28:31]
	v_mfma_f32_16x16x32_bf16 v[16:19], v[152:155], v[208:211], v[16:19]
	v_mfma_f32_16x16x32_bf16 v[12:15], v[160:163], v[208:211], v[12:15]
	s_setprio 0
	s_setprio 1
	v_mfma_f32_16x16x32_bf16 v[56:59], v[164:167], v[180:183], v[56:59]
	v_mfma_f32_16x16x32_bf16 v[52:55], v[172:175], v[180:183], v[52:55]
	v_mfma_f32_16x16x32_bf16 v[40:43], v[164:167], v[188:191], v[40:43]
	v_mfma_f32_16x16x32_bf16 v[36:39], v[172:175], v[188:191], v[36:39]
	v_mfma_f32_16x16x32_bf16 v[24:27], v[164:167], v[196:199], v[24:27]
	v_mfma_f32_16x16x32_bf16 v[20:23], v[172:175], v[196:199], v[20:23]
	v_mfma_f32_16x16x32_bf16 v[8:11], v[164:167], v[204:207], v[8:11]
	v_mfma_f32_16x16x32_bf16 v[4:7], v[172:175], v[204:207], v[4:7]
	v_mfma_f32_16x16x32_bf16 v[56:59], v[168:171], v[184:187], v[56:59]
	v_mfma_f32_16x16x32_bf16 v[52:55], v[176:179], v[184:187], v[52:55]
	v_mfma_f32_16x16x32_bf16 v[40:43], v[168:171], v[192:195], v[40:43]
	v_mfma_f32_16x16x32_bf16 v[36:39], v[176:179], v[192:195], v[36:39]
	v_mfma_f32_16x16x32_bf16 v[24:27], v[168:171], v[200:203], v[24:27]
	v_mfma_f32_16x16x32_bf16 v[20:23], v[176:179], v[200:203], v[20:23]
	v_mfma_f32_16x16x32_bf16 v[8:11], v[168:171], v[208:211], v[8:11]
	v_mfma_f32_16x16x32_bf16 v[4:7], v[176:179], v[208:211], v[4:7]
	s_setprio 0
	s_add_u32 s26, s26, 0x100
	s_addc_u32 s27, s27, 0
	s_add_u32 s19, s19, 0x100
	s_addc_u32 s20, s20, 0
	s_cmp_ge_i32 s22, s46
	s_mov_b32 s21, s22
	s_cbranch_scc1 .Lmy_rot4
	s_add_i32 s22, s21, 2
	s_add_u32 s23, s26, 0x80
	s_addc_u32 s28, s27, 0
	s_add_i32 s55, 0, 0x10000
	s_cmp_eq_u32 s49, s21
	s_cselect_b32 s31, s15, s28
	s_cselect_b32 s30, s14, s23
	s_cselect_b32 s29, s17, s20
	s_cselect_b32 s28, s16, s19
	s_add_i32 s21, 0, 0x14000
	s_branch .LBB0_3499
.Lmy_rot4:
	s_barrier
.LBB0_3500:
	s_and_b64 vcc, exec, s[12:13]
	s_cbranch_vccz .LBB0_3502
	s_barrier
